# v_AC with flat wave priority in the GEMM K-loops (all 136 per-burst s_setprio 1/0 toggles removed)
# speedup vs baseline: 1.0025x; 1.0025x over previous
.LBB0_216:
	v_add_u32_e32 v130, s88, v196
	v_add_u32_e32 v134, s89, v196
	ds_read_b128 v[158:161], v130
	ds_read_b128 v[150:153], v130 offset:1024
	ds_read_b128 v[154:157], v130 offset:2048
	ds_read_b128 v[146:149], v130 offset:3072
	ds_read_b128 v[142:145], v134
	ds_read_b128 v[130:133], v134 offset:1024
	ds_read_b128 v[138:141], v134 offset:2048
	ds_read_b128 v[134:137], v134 offset:3072
	s_add_u32 s25, s50, 0xfff80080
	s_addc_u32 s56, s51, -1
	s_and_b64 s[18:19], s[18:19], exec
	s_cselect_b32 s59, s31, s56
	s_cselect_b32 s58, s4, s25
	s_cselect_b32 s57, s5, s64
	s_cselect_b32 s56, s29, s92
	s_add_i32 m0, s39, 0xc000
	ds_read_b128 v[186:189], v198
	ds_read_b128 v[190:193], v198 offset:1024
	ds_read_b128 v[200:203], v198 offset:2048
	ds_read_b128 v[204:207], v198 offset:3072
	ds_read_b128 v[208:211], v198 offset:4096
	ds_read_b128 v[212:215], v198 offset:5120
	ds_read_b128 v[216:219], v198 offset:6144
	ds_read_b128 v[220:223], v198 offset:7168
	global_load_lds_dwordx4 v170, s[50:51]
	s_add_i32 m0, s39, 0xe000
	s_nop 0
	global_load_lds_dwordx4 v172, s[50:51]
	s_waitcnt vmcnt(8) lgkmcnt(0)
	s_barrier
	v_mfma_i32_16x16x64_i8 v[126:129], v[158:161], v[186:189], v[126:129]
	v_mfma_i32_16x16x64_i8 v[122:125], v[154:157], v[186:189], v[122:125]
	v_mfma_i32_16x16x64_i8 v[106:109], v[154:157], v[200:203], v[106:109]
	v_mfma_i32_16x16x64_i8 v[110:113], v[158:161], v[200:203], v[110:113]
	v_mfma_i32_16x16x64_i8 v[94:97], v[158:161], v[208:211], v[94:97]
	v_mfma_i32_16x16x64_i8 v[90:93], v[154:157], v[208:211], v[90:93]
	v_mfma_i32_16x16x64_i8 v[74:77], v[154:157], v[216:219], v[74:77]
	v_mfma_i32_16x16x64_i8 v[78:81], v[158:161], v[216:219], v[78:81]
	v_mfma_i32_16x16x64_i8 v[126:129], v[150:153], v[190:193], v[126:129]
	v_mfma_i32_16x16x64_i8 v[122:125], v[146:149], v[190:193], v[122:125]
	v_mfma_i32_16x16x64_i8 v[106:109], v[146:149], v[204:207], v[106:109]
	v_mfma_i32_16x16x64_i8 v[110:113], v[150:153], v[204:207], v[110:113]
	v_mfma_i32_16x16x64_i8 v[94:97], v[150:153], v[212:215], v[94:97]
	v_mfma_i32_16x16x64_i8 v[90:93], v[146:149], v[212:215], v[90:93]
	v_mfma_i32_16x16x64_i8 v[74:77], v[146:149], v[220:223], v[74:77]
	v_mfma_i32_16x16x64_i8 v[78:81], v[150:153], v[220:223], v[78:81]
	v_mfma_i32_16x16x64_i8 v[118:121], v[142:145], v[186:189], v[118:121]
	v_mfma_i32_16x16x64_i8 v[114:117], v[138:141], v[186:189], v[114:117]
	v_mfma_i32_16x16x64_i8 v[98:101], v[138:141], v[200:203], v[98:101]
	v_mfma_i32_16x16x64_i8 v[102:105], v[142:145], v[200:203], v[102:105]
	v_mfma_i32_16x16x64_i8 v[86:89], v[142:145], v[208:211], v[86:89]
	v_mfma_i32_16x16x64_i8 v[82:85], v[138:141], v[208:211], v[82:85]
	v_mfma_i32_16x16x64_i8 v[66:69], v[138:141], v[216:219], v[66:69]
	v_mfma_i32_16x16x64_i8 v[70:73], v[142:145], v[216:219], v[70:73]
	v_mfma_i32_16x16x64_i8 v[118:121], v[130:133], v[190:193], v[118:121]
	v_mfma_i32_16x16x64_i8 v[114:117], v[134:137], v[190:193], v[114:117]
	v_mfma_i32_16x16x64_i8 v[98:101], v[134:137], v[204:207], v[98:101]
	v_mfma_i32_16x16x64_i8 v[102:105], v[130:133], v[204:207], v[102:105]
	v_mfma_i32_16x16x64_i8 v[86:89], v[130:133], v[212:215], v[86:89]
	v_mfma_i32_16x16x64_i8 v[82:85], v[134:137], v[212:215], v[82:85]
	v_mfma_i32_16x16x64_i8 v[66:69], v[134:137], v[220:223], v[66:69]
	v_mfma_i32_16x16x64_i8 v[70:73], v[130:133], v[220:223], v[70:73]
	s_barrier
	s_add_i32 s18, s88, s7
	s_mov_b32 m0, s18
	ds_read_b128 v[200:203], v198 offset:16384
	ds_read_b128 v[204:207], v198 offset:17408
	ds_read_b128 v[208:211], v198 offset:18432
	ds_read_b128 v[212:215], v198 offset:19456
	ds_read_b128 v[216:219], v198 offset:20480
	ds_read_b128 v[220:223], v198 offset:21504
	ds_read_b128 v[224:227], v198 offset:22528
	ds_read_b128 v[228:231], v198 offset:23552
	global_load_lds_dwordx4 v164, s[56:57]
	s_add_i32 m0, s18, 0x2000
	s_add_u32 s18, s56, 0x80000
	s_addc_u32 s19, s57, 0
	s_add_i32 s25, s89, s7
	global_load_lds_dwordx4 v168, s[56:57]
	s_mov_b32 m0, s25
	s_nop 0
	global_load_lds_dwordx4 v164, s[18:19]
	s_add_i32 m0, s25, 0x2000
	s_nop 0
	global_load_lds_dwordx4 v168, s[18:19]
	s_mov_b32 m0, s39
	s_nop 0
	global_load_lds_dwordx4 v162, s[58:59]
	s_mov_b32 m0, s43
	s_nop 0
	global_load_lds_dwordx4 v166, s[58:59]
	s_waitcnt vmcnt(8) lgkmcnt(0)
	s_barrier
	v_mfma_i32_16x16x64_i8 v[62:65], v[158:161], v[200:203], v[62:65]
	v_mfma_i32_16x16x64_i8 v[58:61], v[154:157], v[200:203], v[58:61]
	v_mfma_i32_16x16x64_i8 v[42:45], v[154:157], v[208:211], v[42:45]
	v_mfma_i32_16x16x64_i8 v[46:49], v[158:161], v[208:211], v[46:49]
	v_mfma_i32_16x16x64_i8 v[30:33], v[158:161], v[216:219], v[30:33]
	v_mfma_i32_16x16x64_i8 v[26:29], v[154:157], v[216:219], v[26:29]
	v_mfma_i32_16x16x64_i8 v[10:13], v[154:157], v[224:227], v[10:13]
	v_mfma_i32_16x16x64_i8 v[14:17], v[158:161], v[224:227], v[14:17]
	v_mfma_i32_16x16x64_i8 v[62:65], v[150:153], v[204:207], v[62:65]
	v_mfma_i32_16x16x64_i8 v[58:61], v[146:149], v[204:207], v[58:61]
	v_mfma_i32_16x16x64_i8 v[42:45], v[146:149], v[212:215], v[42:45]
	v_mfma_i32_16x16x64_i8 v[46:49], v[150:153], v[212:215], v[46:49]
	v_mfma_i32_16x16x64_i8 v[30:33], v[150:153], v[220:223], v[30:33]
	v_mfma_i32_16x16x64_i8 v[26:29], v[146:149], v[220:223], v[26:29]
	v_mfma_i32_16x16x64_i8 v[10:13], v[146:149], v[228:231], v[10:13]
	v_mfma_i32_16x16x64_i8 v[14:17], v[150:153], v[228:231], v[14:17]
	v_mfma_i32_16x16x64_i8 v[54:57], v[142:145], v[200:203], v[54:57]
	v_mfma_i32_16x16x64_i8 v[50:53], v[138:141], v[200:203], v[50:53]
	v_mfma_i32_16x16x64_i8 v[34:37], v[138:141], v[208:211], v[34:37]
	v_mfma_i32_16x16x64_i8 v[38:41], v[142:145], v[208:211], v[38:41]
	v_mfma_i32_16x16x64_i8 v[22:25], v[142:145], v[216:219], v[22:25]
	v_mfma_i32_16x16x64_i8 v[18:21], v[138:141], v[216:219], v[18:21]
	v_mfma_i32_16x16x64_i8 v[2:5], v[138:141], v[224:227], v[2:5]
	v_mfma_i32_16x16x64_i8 v[6:9], v[142:145], v[224:227], v[6:9]
	v_mfma_i32_16x16x64_i8 v[54:57], v[130:133], v[204:207], v[54:57]
	v_mfma_i32_16x16x64_i8 v[50:53], v[134:137], v[204:207], v[50:53]
	v_mfma_i32_16x16x64_i8 v[34:37], v[134:137], v[212:215], v[34:37]
	v_mfma_i32_16x16x64_i8 v[38:41], v[130:133], v[212:215], v[38:41]
	v_mfma_i32_16x16x64_i8 v[22:25], v[130:133], v[220:223], v[22:25]
	v_mfma_i32_16x16x64_i8 v[18:21], v[134:137], v[220:223], v[18:21]
	v_mfma_i32_16x16x64_i8 v[2:5], v[134:137], v[228:231], v[2:5]
	v_mfma_i32_16x16x64_i8 v[6:9], v[130:133], v[228:231], v[6:9]
	s_barrier
	s_add_i32 s25, 0, 0x18000
	s_add_i32 vcc_lo, 0, 0x1c000
	v_add_u32_e32 v142, s25, v196
	v_add_u32_e32 v158, vcc_lo, v196
	ds_read_b128 v[130:133], v142
	ds_read_b128 v[134:137], v142 offset:1024
	ds_read_b128 v[138:141], v142 offset:2048
	ds_read_b128 v[142:145], v142 offset:3072
	ds_read_b128 v[146:149], v158
	ds_read_b128 v[150:153], v158 offset:1024
	ds_read_b128 v[154:157], v158 offset:2048
	ds_read_b128 v[158:161], v158 offset:3072
	s_add_u32 s18, s58, 0x80000
	s_addc_u32 s19, s59, 0
	s_mov_b32 m0, s61
	ds_read_b128 v[200:203], v198 offset:32768
	ds_read_b128 v[204:207], v198 offset:33792
	ds_read_b128 v[208:211], v198 offset:34816
	ds_read_b128 v[212:215], v198 offset:35840
	ds_read_b128 v[216:219], v198 offset:36864
	ds_read_b128 v[220:223], v198 offset:37888
	ds_read_b128 v[224:227], v198 offset:38912
	ds_read_b128 v[228:231], v198 offset:39936
	global_load_lds_dwordx4 v162, s[18:19]
	s_mov_b32 m0, s62
	s_nop 0
	global_load_lds_dwordx4 v166, s[18:19]
	s_waitcnt vmcnt(8) lgkmcnt(0)
	s_barrier
	v_mfma_i32_16x16x64_i8 v[126:129], v[130:133], v[200:203], v[126:129]
	v_mfma_i32_16x16x64_i8 v[122:125], v[138:141], v[200:203], v[122:125]
	v_mfma_i32_16x16x64_i8 v[106:109], v[138:141], v[208:211], v[106:109]
	v_mfma_i32_16x16x64_i8 v[110:113], v[130:133], v[208:211], v[110:113]
	v_mfma_i32_16x16x64_i8 v[94:97], v[130:133], v[216:219], v[94:97]
	v_mfma_i32_16x16x64_i8 v[90:93], v[138:141], v[216:219], v[90:93]
	v_mfma_i32_16x16x64_i8 v[74:77], v[138:141], v[224:227], v[74:77]
	v_mfma_i32_16x16x64_i8 v[78:81], v[130:133], v[224:227], v[78:81]
	v_mfma_i32_16x16x64_i8 v[126:129], v[134:137], v[204:207], v[126:129]
	v_mfma_i32_16x16x64_i8 v[122:125], v[142:145], v[204:207], v[122:125]
	v_mfma_i32_16x16x64_i8 v[106:109], v[142:145], v[212:215], v[106:109]
	v_mfma_i32_16x16x64_i8 v[110:113], v[134:137], v[212:215], v[110:113]
	v_mfma_i32_16x16x64_i8 v[94:97], v[134:137], v[220:223], v[94:97]
	v_mfma_i32_16x16x64_i8 v[90:93], v[142:145], v[220:223], v[90:93]
	v_mfma_i32_16x16x64_i8 v[74:77], v[142:145], v[228:231], v[74:77]
	v_mfma_i32_16x16x64_i8 v[78:81], v[134:137], v[228:231], v[78:81]
	v_mfma_i32_16x16x64_i8 v[118:121], v[146:149], v[200:203], v[118:121]
	v_mfma_i32_16x16x64_i8 v[114:117], v[154:157], v[200:203], v[114:117]
	v_mfma_i32_16x16x64_i8 v[98:101], v[154:157], v[208:211], v[98:101]
	v_mfma_i32_16x16x64_i8 v[102:105], v[146:149], v[208:211], v[102:105]
	v_mfma_i32_16x16x64_i8 v[86:89], v[146:149], v[216:219], v[86:89]
	v_mfma_i32_16x16x64_i8 v[82:85], v[154:157], v[216:219], v[82:85]
	v_mfma_i32_16x16x64_i8 v[66:69], v[154:157], v[224:227], v[66:69]
	v_mfma_i32_16x16x64_i8 v[70:73], v[146:149], v[224:227], v[70:73]
	v_mfma_i32_16x16x64_i8 v[118:121], v[150:153], v[204:207], v[118:121]
	v_mfma_i32_16x16x64_i8 v[114:117], v[158:161], v[204:207], v[114:117]
	v_mfma_i32_16x16x64_i8 v[98:101], v[158:161], v[212:215], v[98:101]
	v_mfma_i32_16x16x64_i8 v[102:105], v[150:153], v[212:215], v[102:105]
	v_mfma_i32_16x16x64_i8 v[86:89], v[150:153], v[220:223], v[86:89]
	v_mfma_i32_16x16x64_i8 v[82:85], v[158:161], v[220:223], v[82:85]
	v_mfma_i32_16x16x64_i8 v[66:69], v[158:161], v[228:231], v[66:69]
	v_mfma_i32_16x16x64_i8 v[70:73], v[150:153], v[228:231], v[70:73]
	s_barrier
	s_add_i32 s18, s25, s7
	s_mov_b32 m0, s18
	s_add_u32 s98, s56, 0x80
	s_addc_u32 s99, s57, 0
	s_add_u32 s100, s58, 0x80
	s_addc_u32 s101, s59, 0
	ds_read_b128 v[200:203], v198 offset:49152
	ds_read_b128 v[204:207], v198 offset:50176
	ds_read_b128 v[208:211], v198 offset:51200
	ds_read_b128 v[212:215], v198 offset:52224
	ds_read_b128 v[216:219], v198 offset:53248
	ds_read_b128 v[220:223], v198 offset:54272
	ds_read_b128 v[224:227], v198 offset:55296
	ds_read_b128 v[228:231], v198 offset:56320
	global_load_lds_dwordx4 v164, s[98:99]
	s_add_i32 m0, s18, 0x2000
	s_add_u32 s18, s56, 0x80080
	s_addc_u32 s19, s57, 0
	s_add_i32 s25, vcc_lo, s7
	global_load_lds_dwordx4 v168, s[98:99]
	s_mov_b32 m0, s25
	s_nop 0
	global_load_lds_dwordx4 v164, s[18:19]
	s_add_i32 m0, s25, 0x2000
	s_nop 0
	global_load_lds_dwordx4 v168, s[18:19]
	s_mov_b32 m0, s67
	s_nop 0
	global_load_lds_dwordx4 v162, s[100:101]
	s_mov_b32 m0, s68
	s_nop 0
	global_load_lds_dwordx4 v166, s[100:101]
	s_waitcnt vmcnt(8) lgkmcnt(0)
	s_barrier
	v_mfma_i32_16x16x64_i8 v[62:65], v[130:133], v[200:203], v[62:65]
	v_mfma_i32_16x16x64_i8 v[58:61], v[138:141], v[200:203], v[58:61]
	v_mfma_i32_16x16x64_i8 v[42:45], v[138:141], v[208:211], v[42:45]
	v_mfma_i32_16x16x64_i8 v[46:49], v[130:133], v[208:211], v[46:49]
	v_mfma_i32_16x16x64_i8 v[30:33], v[130:133], v[216:219], v[30:33]
	v_mfma_i32_16x16x64_i8 v[26:29], v[138:141], v[216:219], v[26:29]
	v_mfma_i32_16x16x64_i8 v[10:13], v[138:141], v[224:227], v[10:13]
	v_mfma_i32_16x16x64_i8 v[14:17], v[130:133], v[224:227], v[14:17]
	v_mfma_i32_16x16x64_i8 v[62:65], v[134:137], v[204:207], v[62:65]
	v_mfma_i32_16x16x64_i8 v[58:61], v[142:145], v[204:207], v[58:61]
	v_mfma_i32_16x16x64_i8 v[42:45], v[142:145], v[212:215], v[42:45]
	v_mfma_i32_16x16x64_i8 v[46:49], v[134:137], v[212:215], v[46:49]
	v_mfma_i32_16x16x64_i8 v[30:33], v[134:137], v[220:223], v[30:33]
	v_mfma_i32_16x16x64_i8 v[26:29], v[142:145], v[220:223], v[26:29]
	v_mfma_i32_16x16x64_i8 v[10:13], v[142:145], v[228:231], v[10:13]
	v_mfma_i32_16x16x64_i8 v[14:17], v[134:137], v[228:231], v[14:17]
	v_mfma_i32_16x16x64_i8 v[54:57], v[146:149], v[200:203], v[54:57]
	v_mfma_i32_16x16x64_i8 v[50:53], v[154:157], v[200:203], v[50:53]
	v_mfma_i32_16x16x64_i8 v[34:37], v[154:157], v[208:211], v[34:37]
	v_mfma_i32_16x16x64_i8 v[38:41], v[146:149], v[208:211], v[38:41]
	v_mfma_i32_16x16x64_i8 v[22:25], v[146:149], v[216:219], v[22:25]
	v_mfma_i32_16x16x64_i8 v[18:21], v[154:157], v[216:219], v[18:21]
	v_mfma_i32_16x16x64_i8 v[2:5], v[154:157], v[224:227], v[2:5]
	v_mfma_i32_16x16x64_i8 v[6:9], v[146:149], v[224:227], v[6:9]
	v_mfma_i32_16x16x64_i8 v[54:57], v[150:153], v[204:207], v[54:57]
	v_mfma_i32_16x16x64_i8 v[50:53], v[158:161], v[204:207], v[50:53]
	v_mfma_i32_16x16x64_i8 v[34:37], v[158:161], v[212:215], v[34:37]
	v_mfma_i32_16x16x64_i8 v[38:41], v[150:153], v[212:215], v[38:41]
	v_mfma_i32_16x16x64_i8 v[22:25], v[150:153], v[220:223], v[22:25]
	v_mfma_i32_16x16x64_i8 v[18:21], v[158:161], v[220:223], v[18:21]
	v_mfma_i32_16x16x64_i8 v[2:5], v[158:161], v[228:231], v[2:5]
	v_mfma_i32_16x16x64_i8 v[6:9], v[150:153], v[228:231], v[6:9]
	s_barrier
	s_add_i32 s65, s65, 2
	s_add_u32 s50, s50, 0x100
	s_addc_u32 s51, s51, 0
	s_add_u32 s92, s92, 0x100
	s_addc_u32 s64, s64, 0
	s_cmp_gt_u32 s65, 29
	s_cbranch_scc1 .LBB0_219

.LBB0_242:
	ds_read_b128 v[150:153], v146
	ds_read_b128 v[154:157], v146 offset:1024
	ds_read_b128 v[158:161], v146 offset:2048
	ds_read_b128 v[162:165], v146 offset:3072
	ds_read_b128 v[166:169], v147
	ds_read_b128 v[170:173], v147 offset:1024
	ds_read_b128 v[174:177], v147 offset:2048
	ds_read_b128 v[178:181], v147 offset:3072
	s_add_u32 s36, s34, 0xfff00080
	s_addc_u32 s37, s35, -1
	s_cmp_eq_u32 s25, 60
	s_cselect_b32 s39, s5, s37
	s_cselect_b32 s38, s18, s36
	s_cselect_b32 s37, s17, s24
	s_cselect_b32 s36, s19, s21
	v_lshl_add_u64 v[142:143], s[34:35], 0, v[138:139]
	s_add_i32 m0, s31, 0xc000
	ds_read_b128 v[182:185], v148
	ds_read_b128 v[186:189], v148 offset:1024
	ds_read_b128 v[190:193], v148 offset:2048
	ds_read_b128 v[194:197], v148 offset:3072
	ds_read_b128 v[198:201], v148 offset:4096
	ds_read_b128 v[202:205], v148 offset:5120
	ds_read_b128 v[206:209], v148 offset:6144
	ds_read_b128 v[210:213], v148 offset:7168
	global_load_lds_dwordx4 v[142:143], off
	v_lshl_add_u64 v[142:143], s[34:35], 0, v[140:141]
	s_add_i32 m0, s31, 0xe000
	s_nop 0
	global_load_lds_dwordx4 v[142:143], off
	s_waitcnt vmcnt(8) lgkmcnt(0)
	s_barrier
	v_mfma_f32_16x16x32_bf16 v[126:129], v[150:153], v[182:185], v[126:129]
	v_mfma_f32_16x16x32_bf16 v[122:125], v[158:161], v[182:185], v[122:125]
	v_mfma_f32_16x16x32_bf16 v[114:117], v[150:153], v[190:193], v[114:117]
	v_mfma_f32_16x16x32_bf16 v[106:109], v[158:161], v[190:193], v[106:109]
	v_mfma_f32_16x16x32_bf16 v[98:101], v[150:153], v[198:201], v[98:101]
	v_mfma_f32_16x16x32_bf16 v[90:93], v[158:161], v[198:201], v[90:93]
	v_mfma_f32_16x16x32_bf16 v[78:81], v[150:153], v[206:209], v[78:81]
	v_mfma_f32_16x16x32_bf16 v[74:77], v[158:161], v[206:209], v[74:77]
	v_mfma_f32_16x16x32_bf16 v[126:129], v[154:157], v[186:189], v[126:129]
	v_mfma_f32_16x16x32_bf16 v[122:125], v[162:165], v[186:189], v[122:125]
	v_mfma_f32_16x16x32_bf16 v[114:117], v[154:157], v[194:197], v[114:117]
	v_mfma_f32_16x16x32_bf16 v[106:109], v[162:165], v[194:197], v[106:109]
	v_mfma_f32_16x16x32_bf16 v[98:101], v[154:157], v[202:205], v[98:101]
	v_mfma_f32_16x16x32_bf16 v[90:93], v[162:165], v[202:205], v[90:93]
	v_mfma_f32_16x16x32_bf16 v[78:81], v[154:157], v[210:213], v[78:81]
	v_mfma_f32_16x16x32_bf16 v[74:77], v[162:165], v[210:213], v[74:77]
	v_mfma_f32_16x16x32_bf16 v[118:121], v[166:169], v[182:185], v[118:121]
	v_mfma_f32_16x16x32_bf16 v[110:113], v[174:177], v[182:185], v[110:113]
	v_mfma_f32_16x16x32_bf16 v[102:105], v[166:169], v[190:193], v[102:105]
	v_mfma_f32_16x16x32_bf16 v[94:97], v[174:177], v[190:193], v[94:97]
	v_mfma_f32_16x16x32_bf16 v[86:89], v[166:169], v[198:201], v[86:89]
	v_mfma_f32_16x16x32_bf16 v[82:85], v[174:177], v[198:201], v[82:85]
	v_mfma_f32_16x16x32_bf16 v[70:73], v[166:169], v[206:209], v[70:73]
	v_mfma_f32_16x16x32_bf16 v[66:69], v[174:177], v[206:209], v[66:69]
	v_mfma_f32_16x16x32_bf16 v[118:121], v[170:173], v[186:189], v[118:121]
	v_mfma_f32_16x16x32_bf16 v[110:113], v[178:181], v[186:189], v[110:113]
	v_mfma_f32_16x16x32_bf16 v[102:105], v[170:173], v[194:197], v[102:105]
	v_mfma_f32_16x16x32_bf16 v[94:97], v[178:181], v[194:197], v[94:97]
	v_mfma_f32_16x16x32_bf16 v[86:89], v[170:173], v[202:205], v[86:89]
	v_mfma_f32_16x16x32_bf16 v[82:85], v[178:181], v[202:205], v[82:85]
	v_mfma_f32_16x16x32_bf16 v[70:73], v[170:173], v[210:213], v[70:73]
	v_mfma_f32_16x16x32_bf16 v[66:69], v[178:181], v[210:213], v[66:69]
	s_barrier
	s_add_i32 s61, s59, s42
	v_lshl_add_u64 v[142:143], s[36:37], 0, v[132:133]
	s_mov_b32 m0, s61
	ds_read_b128 v[182:185], v148 offset:16384
	ds_read_b128 v[186:189], v148 offset:17408
	ds_read_b128 v[190:193], v148 offset:18432
	ds_read_b128 v[194:197], v148 offset:19456
	ds_read_b128 v[198:201], v148 offset:20480
	ds_read_b128 v[202:205], v148 offset:21504
	ds_read_b128 v[206:209], v148 offset:22528
	ds_read_b128 v[210:213], v148 offset:23552
	global_load_lds_dwordx4 v[142:143], off
	s_add_i32 m0, s61, 0x2000
	s_add_u32 s62, s36, 0x100000
	v_lshl_add_u64 v[214:215], s[36:37], 0, v[136:137]
	s_addc_u32 s63, s37, 0
	s_add_i32 s61, s60, s42
	global_load_lds_dwordx4 v[214:215], off
	v_lshl_add_u64 v[216:217], s[62:63], 0, v[132:133]
	s_mov_b32 m0, s61
	v_lshl_add_u64 v[218:219], s[38:39], 0, v[134:135]
	global_load_lds_dwordx4 v[216:217], off
	v_lshl_add_u64 v[216:217], s[62:63], 0, v[136:137]
	s_add_i32 m0, s61, 0x2000
	s_nop 0
	global_load_lds_dwordx4 v[216:217], off
	v_lshl_add_u64 v[216:217], s[38:39], 0, v[130:131]
	s_mov_b32 m0, s31
	s_nop 0
	global_load_lds_dwordx4 v[216:217], off
	s_mov_b32 m0, s49
	s_nop 0
	global_load_lds_dwordx4 v[218:219], off
	s_waitcnt vmcnt(8) lgkmcnt(0)
	s_barrier
	v_mfma_f32_16x16x32_bf16 v[62:65], v[150:153], v[182:185], v[62:65]
	v_mfma_f32_16x16x32_bf16 v[58:61], v[158:161], v[182:185], v[58:61]
	v_mfma_f32_16x16x32_bf16 v[50:53], v[150:153], v[190:193], v[50:53]
	v_mfma_f32_16x16x32_bf16 v[42:45], v[158:161], v[190:193], v[42:45]
	v_mfma_f32_16x16x32_bf16 v[34:37], v[150:153], v[198:201], v[34:37]
	v_mfma_f32_16x16x32_bf16 v[26:29], v[158:161], v[198:201], v[26:29]
	v_mfma_f32_16x16x32_bf16 v[18:21], v[150:153], v[206:209], v[18:21]
	v_mfma_f32_16x16x32_bf16 v[10:13], v[158:161], v[206:209], v[10:13]
	v_mfma_f32_16x16x32_bf16 v[62:65], v[154:157], v[186:189], v[62:65]
	v_mfma_f32_16x16x32_bf16 v[58:61], v[162:165], v[186:189], v[58:61]
	v_mfma_f32_16x16x32_bf16 v[50:53], v[154:157], v[194:197], v[50:53]
	v_mfma_f32_16x16x32_bf16 v[42:45], v[162:165], v[194:197], v[42:45]
	v_mfma_f32_16x16x32_bf16 v[34:37], v[154:157], v[202:205], v[34:37]
	v_mfma_f32_16x16x32_bf16 v[26:29], v[162:165], v[202:205], v[26:29]
	v_mfma_f32_16x16x32_bf16 v[18:21], v[154:157], v[210:213], v[18:21]
	v_mfma_f32_16x16x32_bf16 v[10:13], v[162:165], v[210:213], v[10:13]
	v_mfma_f32_16x16x32_bf16 v[54:57], v[166:169], v[182:185], v[54:57]
	v_mfma_f32_16x16x32_bf16 v[46:49], v[174:177], v[182:185], v[46:49]
	v_mfma_f32_16x16x32_bf16 v[38:41], v[166:169], v[190:193], v[38:41]
	v_mfma_f32_16x16x32_bf16 v[30:33], v[174:177], v[190:193], v[30:33]
	v_mfma_f32_16x16x32_bf16 v[22:25], v[166:169], v[198:201], v[22:25]
	v_mfma_f32_16x16x32_bf16 v[14:17], v[174:177], v[198:201], v[14:17]
	v_mfma_f32_16x16x32_bf16 v[6:9], v[166:169], v[206:209], v[6:9]
	v_mfma_f32_16x16x32_bf16 v[2:5], v[174:177], v[206:209], v[2:5]
	v_mfma_f32_16x16x32_bf16 v[54:57], v[170:173], v[186:189], v[54:57]
	v_mfma_f32_16x16x32_bf16 v[46:49], v[178:181], v[186:189], v[46:49]
	v_mfma_f32_16x16x32_bf16 v[38:41], v[170:173], v[194:197], v[38:41]
	v_mfma_f32_16x16x32_bf16 v[30:33], v[178:181], v[194:197], v[30:33]
	v_mfma_f32_16x16x32_bf16 v[22:25], v[170:173], v[202:205], v[22:25]
	v_mfma_f32_16x16x32_bf16 v[14:17], v[178:181], v[202:205], v[14:17]
	v_mfma_f32_16x16x32_bf16 v[6:9], v[170:173], v[210:213], v[6:9]
	v_mfma_f32_16x16x32_bf16 v[2:5], v[178:181], v[210:213], v[2:5]
	s_barrier
	s_add_i32 s61, 0, 0x18000
	v_add_u32_e32 v149, s61, v144
	s_add_i32 s62, 0, 0x1c000
	ds_read_b128 v[150:153], v149
	ds_read_b128 v[154:157], v149 offset:1024
	ds_read_b128 v[158:161], v149 offset:2048
	ds_read_b128 v[162:165], v149 offset:3072
	v_add_u32_e32 v149, s62, v144
	ds_read_b128 v[166:169], v149
	ds_read_b128 v[170:173], v149 offset:1024
	ds_read_b128 v[174:177], v149 offset:2048
	ds_read_b128 v[178:181], v149 offset:3072
	s_add_u32 s38, s38, 0x100000
	s_addc_u32 s39, s39, 0
	s_mov_b32 m0, s50
	v_lshl_add_u64 v[220:221], s[38:39], 0, v[130:131]
	ds_read_b128 v[182:185], v148 offset:32768
	ds_read_b128 v[186:189], v148 offset:33792
	ds_read_b128 v[190:193], v148 offset:34816
	ds_read_b128 v[194:197], v148 offset:35840
	ds_read_b128 v[198:201], v148 offset:36864
	ds_read_b128 v[202:205], v148 offset:37888
	ds_read_b128 v[206:209], v148 offset:38912
	ds_read_b128 v[210:213], v148 offset:39936
	global_load_lds_dwordx4 v[220:221], off
	v_lshl_add_u64 v[220:221], s[38:39], 0, v[134:135]
	s_mov_b32 m0, s51
	s_nop 0
	global_load_lds_dwordx4 v[220:221], off
	s_waitcnt vmcnt(8) lgkmcnt(0)
	s_barrier
	v_mfma_f32_16x16x32_bf16 v[126:129], v[150:153], v[182:185], v[126:129]
	v_mfma_f32_16x16x32_bf16 v[122:125], v[158:161], v[182:185], v[122:125]
	v_mfma_f32_16x16x32_bf16 v[114:117], v[150:153], v[190:193], v[114:117]
	v_mfma_f32_16x16x32_bf16 v[106:109], v[158:161], v[190:193], v[106:109]
	v_mfma_f32_16x16x32_bf16 v[98:101], v[150:153], v[198:201], v[98:101]
	v_mfma_f32_16x16x32_bf16 v[90:93], v[158:161], v[198:201], v[90:93]
	v_mfma_f32_16x16x32_bf16 v[78:81], v[150:153], v[206:209], v[78:81]
	v_mfma_f32_16x16x32_bf16 v[74:77], v[158:161], v[206:209], v[74:77]
	v_mfma_f32_16x16x32_bf16 v[126:129], v[154:157], v[186:189], v[126:129]
	v_mfma_f32_16x16x32_bf16 v[122:125], v[162:165], v[186:189], v[122:125]
	v_mfma_f32_16x16x32_bf16 v[114:117], v[154:157], v[194:197], v[114:117]
	v_mfma_f32_16x16x32_bf16 v[106:109], v[162:165], v[194:197], v[106:109]
	v_mfma_f32_16x16x32_bf16 v[98:101], v[154:157], v[202:205], v[98:101]
	v_mfma_f32_16x16x32_bf16 v[90:93], v[162:165], v[202:205], v[90:93]
	v_mfma_f32_16x16x32_bf16 v[78:81], v[154:157], v[210:213], v[78:81]
	v_mfma_f32_16x16x32_bf16 v[74:77], v[162:165], v[210:213], v[74:77]
	v_mfma_f32_16x16x32_bf16 v[118:121], v[166:169], v[182:185], v[118:121]
	v_mfma_f32_16x16x32_bf16 v[110:113], v[174:177], v[182:185], v[110:113]
	v_mfma_f32_16x16x32_bf16 v[102:105], v[166:169], v[190:193], v[102:105]
	v_mfma_f32_16x16x32_bf16 v[94:97], v[174:177], v[190:193], v[94:97]
	v_mfma_f32_16x16x32_bf16 v[86:89], v[166:169], v[198:201], v[86:89]
	v_mfma_f32_16x16x32_bf16 v[82:85], v[174:177], v[198:201], v[82:85]
	v_mfma_f32_16x16x32_bf16 v[70:73], v[166:169], v[206:209], v[70:73]
	v_mfma_f32_16x16x32_bf16 v[66:69], v[174:177], v[206:209], v[66:69]
	v_mfma_f32_16x16x32_bf16 v[118:121], v[170:173], v[186:189], v[118:121]
	v_mfma_f32_16x16x32_bf16 v[110:113], v[178:181], v[186:189], v[110:113]
	v_mfma_f32_16x16x32_bf16 v[102:105], v[170:173], v[194:197], v[102:105]
	v_mfma_f32_16x16x32_bf16 v[94:97], v[178:181], v[194:197], v[94:97]
	v_mfma_f32_16x16x32_bf16 v[86:89], v[170:173], v[202:205], v[86:89]
	v_mfma_f32_16x16x32_bf16 v[82:85], v[178:181], v[202:205], v[82:85]
	v_mfma_f32_16x16x32_bf16 v[70:73], v[170:173], v[210:213], v[70:73]
	v_mfma_f32_16x16x32_bf16 v[66:69], v[178:181], v[210:213], v[66:69]
	s_barrier
	s_add_i32 s38, s61, s42
	v_lshl_add_u64 v[142:143], v[142:143], 0, s[10:11]
	s_mov_b32 m0, s38
	ds_read_b128 v[182:185], v148 offset:49152
	ds_read_b128 v[186:189], v148 offset:50176
	ds_read_b128 v[190:193], v148 offset:51200
	ds_read_b128 v[194:197], v148 offset:52224
	ds_read_b128 v[198:201], v148 offset:53248
	ds_read_b128 v[202:205], v148 offset:54272
	ds_read_b128 v[206:209], v148 offset:55296
	ds_read_b128 v[210:213], v148 offset:56320
	global_load_lds_dwordx4 v[142:143], off
	s_add_i32 m0, s38, 0x2000
	s_add_u32 s36, s36, 0x100080
	v_lshl_add_u64 v[142:143], v[214:215], 0, s[10:11]
	s_addc_u32 s37, s37, 0
	s_add_i32 s38, s62, s42
	global_load_lds_dwordx4 v[142:143], off
	v_lshl_add_u64 v[142:143], s[36:37], 0, v[132:133]
	s_mov_b32 m0, s38
	s_nop 0
	global_load_lds_dwordx4 v[142:143], off
	v_lshl_add_u64 v[142:143], s[36:37], 0, v[136:137]
	s_add_i32 m0, s38, 0x2000
	s_nop 0
	global_load_lds_dwordx4 v[142:143], off
	v_lshl_add_u64 v[142:143], v[216:217], 0, s[10:11]
	s_mov_b32 m0, s57
	s_nop 0
	global_load_lds_dwordx4 v[142:143], off
	v_lshl_add_u64 v[142:143], v[218:219], 0, s[10:11]
	s_mov_b32 m0, s58
	s_nop 0
	global_load_lds_dwordx4 v[142:143], off
	s_waitcnt vmcnt(8) lgkmcnt(0)
	s_barrier
	v_mfma_f32_16x16x32_bf16 v[62:65], v[150:153], v[182:185], v[62:65]
	v_mfma_f32_16x16x32_bf16 v[58:61], v[158:161], v[182:185], v[58:61]
	v_mfma_f32_16x16x32_bf16 v[50:53], v[150:153], v[190:193], v[50:53]
	v_mfma_f32_16x16x32_bf16 v[42:45], v[158:161], v[190:193], v[42:45]
	v_mfma_f32_16x16x32_bf16 v[34:37], v[150:153], v[198:201], v[34:37]
	v_mfma_f32_16x16x32_bf16 v[26:29], v[158:161], v[198:201], v[26:29]
	v_mfma_f32_16x16x32_bf16 v[18:21], v[150:153], v[206:209], v[18:21]
	v_mfma_f32_16x16x32_bf16 v[10:13], v[158:161], v[206:209], v[10:13]
	v_mfma_f32_16x16x32_bf16 v[62:65], v[154:157], v[186:189], v[62:65]
	v_mfma_f32_16x16x32_bf16 v[58:61], v[162:165], v[186:189], v[58:61]
	v_mfma_f32_16x16x32_bf16 v[50:53], v[154:157], v[194:197], v[50:53]
	v_mfma_f32_16x16x32_bf16 v[42:45], v[162:165], v[194:197], v[42:45]
	v_mfma_f32_16x16x32_bf16 v[34:37], v[154:157], v[202:205], v[34:37]
	v_mfma_f32_16x16x32_bf16 v[26:29], v[162:165], v[202:205], v[26:29]
	v_mfma_f32_16x16x32_bf16 v[18:21], v[154:157], v[210:213], v[18:21]
	v_mfma_f32_16x16x32_bf16 v[10:13], v[162:165], v[210:213], v[10:13]
	v_mfma_f32_16x16x32_bf16 v[54:57], v[166:169], v[182:185], v[54:57]
	v_mfma_f32_16x16x32_bf16 v[46:49], v[174:177], v[182:185], v[46:49]
	v_mfma_f32_16x16x32_bf16 v[38:41], v[166:169], v[190:193], v[38:41]
	v_mfma_f32_16x16x32_bf16 v[30:33], v[174:177], v[190:193], v[30:33]
	v_mfma_f32_16x16x32_bf16 v[22:25], v[166:169], v[198:201], v[22:25]
	v_mfma_f32_16x16x32_bf16 v[14:17], v[174:177], v[198:201], v[14:17]
	v_mfma_f32_16x16x32_bf16 v[6:9], v[166:169], v[206:209], v[6:9]
	v_mfma_f32_16x16x32_bf16 v[2:5], v[174:177], v[206:209], v[2:5]
	v_mfma_f32_16x16x32_bf16 v[54:57], v[170:173], v[186:189], v[54:57]
	v_mfma_f32_16x16x32_bf16 v[46:49], v[178:181], v[186:189], v[46:49]
	v_mfma_f32_16x16x32_bf16 v[38:41], v[170:173], v[194:197], v[38:41]
	v_mfma_f32_16x16x32_bf16 v[30:33], v[178:181], v[194:197], v[30:33]
	v_mfma_f32_16x16x32_bf16 v[22:25], v[170:173], v[202:205], v[22:25]
	v_mfma_f32_16x16x32_bf16 v[14:17], v[178:181], v[202:205], v[14:17]
	v_mfma_f32_16x16x32_bf16 v[6:9], v[170:173], v[210:213], v[6:9]
	v_mfma_f32_16x16x32_bf16 v[2:5], v[178:181], v[210:213], v[2:5]
	s_barrier
	s_add_i32 s25, s25, 2
	s_add_u32 s34, s34, 0x100
	s_addc_u32 s35, s35, 0
	s_add_u32 s21, s21, 0x100
	s_addc_u32 s24, s24, 0
	s_cmp_gt_u32 s25, 61
	s_cbranch_scc0 .LBB0_242
	s_and_b64 vcc, exec, s[12:13]
	s_cbranch_vccz .LBB0_245
	s_barrier

.LBB0_318:
	ds_read_b128 v[26:29], v185
	ds_read_b128 v[30:33], v185 offset:1024
	ds_read_b128 v[18:21], v185 offset:2048
	ds_read_b128 v[22:25], v185 offset:3072
	ds_read_b128 v[10:13], v186
	ds_read_b128 v[14:17], v186 offset:1024
	ds_read_b128 v[2:5], v186 offset:2048
	ds_read_b128 v[6:9], v186 offset:3072
	s_add_u32 s24, s26, 0xffea8080
	s_addc_u32 s25, s27, -1
	s_cmpk_eq_i32 s58, 0x52
	s_cselect_b32 s31, s5, s25
	s_cselect_b32 s30, s4, s24
	s_cselect_b32 s29, s21, s51
	s_cselect_b32 s28, s20, s50
	s_add_i32 m0, s7, 0xc000
	ds_read_b128 v[174:177], v187
	ds_read_b128 v[178:181], v187 offset:1024
	ds_read_b128 v[188:191], v187 offset:2048
	ds_read_b128 v[192:195], v187 offset:3072
	ds_read_b128 v[196:199], v187 offset:4096
	ds_read_b128 v[200:203], v187 offset:5120
	ds_read_b128 v[204:207], v187 offset:6144
	ds_read_b128 v[208:211], v187 offset:7168
	global_load_lds_dwordx4 v166, s[26:27]
	v_lshl_add_u64 v[212:213], s[26:27], 0, v[168:169]
	s_add_i32 m0, s7, 0xe000
	s_nop 0
	global_load_lds_dwordx4 v[212:213], off
	s_waitcnt vmcnt(8) lgkmcnt(0)
	s_barrier
	v_mfma_f32_16x16x128_f8f6f4 v[158:161], v[26:33], v[174:181], v[158:161]
	v_mfma_f32_16x16x128_f8f6f4 v[154:157], v[18:25], v[174:181], v[154:157]
	v_mfma_f32_16x16x128_f8f6f4 v[138:141], v[18:25], v[188:195], v[138:141]
	v_mfma_f32_16x16x128_f8f6f4 v[142:145], v[26:33], v[188:195], v[142:145]
	v_mfma_f32_16x16x128_f8f6f4 v[126:129], v[26:33], v[196:203], v[126:129]
	v_mfma_f32_16x16x128_f8f6f4 v[122:125], v[18:25], v[196:203], v[122:125]
	v_mfma_f32_16x16x128_f8f6f4 v[106:109], v[18:25], v[204:211], v[106:109]
	v_mfma_f32_16x16x128_f8f6f4 v[110:113], v[26:33], v[204:211], v[110:113]
	v_mfma_f32_16x16x128_f8f6f4 v[102:105], v[10:17], v[204:211], v[102:105]
	v_mfma_f32_16x16x128_f8f6f4 v[98:101], v[2:9], v[204:211], v[98:101]
	v_mfma_f32_16x16x128_f8f6f4 v[146:149], v[2:9], v[174:181], v[146:149]
	v_mfma_f32_16x16x128_f8f6f4 v[150:153], v[10:17], v[174:181], v[150:153]
	v_mfma_f32_16x16x128_f8f6f4 v[134:137], v[10:17], v[188:195], v[134:137]
	v_mfma_f32_16x16x128_f8f6f4 v[130:133], v[2:9], v[188:195], v[130:133]
	v_mfma_f32_16x16x128_f8f6f4 v[114:117], v[2:9], v[196:203], v[114:117]
	v_mfma_f32_16x16x128_f8f6f4 v[118:121], v[10:17], v[196:203], v[118:121]
	s_barrier
	s_add_i32 s24, s42, s3
	v_lshl_add_u64 v[174:175], s[28:29], 0, v[164:165]
	s_mov_b32 m0, s24
	ds_read_b128 v[188:191], v187 offset:16384
	ds_read_b128 v[192:195], v187 offset:17408
	ds_read_b128 v[196:199], v187 offset:18432
	ds_read_b128 v[200:203], v187 offset:19456
	ds_read_b128 v[204:207], v187 offset:20480
	ds_read_b128 v[208:211], v187 offset:21504
	ds_read_b128 v[212:215], v187 offset:22528
	ds_read_b128 v[216:219], v187 offset:23552
	global_load_lds_dwordx4 v[174:175], off
	s_add_i32 m0, s24, 0x2000
	s_add_u32 s24, s28, 0x158000
	v_lshl_add_u64 v[176:177], s[28:29], 0, v[162:163]
	s_addc_u32 s25, s29, 0
	s_add_i32 s59, s43, s3
	global_load_lds_dwordx4 v[176:177], off
	s_mov_b32 m0, s59
	v_lshl_add_u64 v[180:181], s[30:31], 0, v[162:163]
	global_load_lds_dwordx4 v164, s[24:25]
	s_add_i32 m0, s59, 0x2000
	s_nop 0
	global_load_lds_dwordx4 v162, s[24:25]
	v_lshl_add_u64 v[178:179], s[30:31], 0, v[164:165]
	s_mov_b32 m0, s7
	s_nop 0
	global_load_lds_dwordx4 v[178:179], off
	s_mov_b32 m0, s17
	s_nop 0
	global_load_lds_dwordx4 v[180:181], off
	s_waitcnt vmcnt(8) lgkmcnt(0)
	s_barrier
	v_mfma_f32_16x16x128_f8f6f4 v[78:81], v[26:33], v[196:203], v[78:81]
	v_mfma_f32_16x16x128_f8f6f4 v[74:77], v[18:25], v[196:203], v[74:77]
	v_mfma_f32_16x16x128_f8f6f4 v[90:93], v[18:25], v[188:195], v[90:93]
	v_mfma_f32_16x16x128_f8f6f4 v[94:97], v[26:33], v[188:195], v[94:97]
	v_mfma_f32_16x16x128_f8f6f4 v[62:65], v[26:33], v[204:211], v[62:65]
	v_mfma_f32_16x16x128_f8f6f4 v[58:61], v[18:25], v[204:211], v[58:61]
	v_mfma_f32_16x16x128_f8f6f4 v[42:45], v[18:25], v[212:219], v[42:45]
	v_mfma_f32_16x16x128_f8f6f4 v[46:49], v[26:33], v[212:219], v[46:49]
	v_mfma_f32_16x16x128_f8f6f4 v[38:41], v[10:17], v[212:219], v[38:41]
	v_mfma_f32_16x16x128_f8f6f4 v[34:37], v[2:9], v[212:219], v[34:37]
	v_mfma_f32_16x16x128_f8f6f4 v[82:85], v[2:9], v[188:195], v[82:85]
	v_mfma_f32_16x16x128_f8f6f4 v[86:89], v[10:17], v[188:195], v[86:89]
	v_mfma_f32_16x16x128_f8f6f4 v[70:73], v[10:17], v[196:203], v[70:73]
	v_mfma_f32_16x16x128_f8f6f4 v[66:69], v[2:9], v[196:203], v[66:69]
	v_mfma_f32_16x16x128_f8f6f4 v[50:53], v[2:9], v[204:211], v[50:53]
	v_mfma_f32_16x16x128_f8f6f4 v[54:57], v[10:17], v[204:211], v[54:57]
	s_barrier
	s_add_i32 s59, 0, 0x18000
	s_add_i32 s60, 0, 0x1c000
	v_add_u32_e32 v14, s59, v183
	v_add_u32_e32 v30, s60, v183
	ds_read_b128 v[2:5], v14
	ds_read_b128 v[6:9], v14 offset:1024
	ds_read_b128 v[10:13], v14 offset:2048
	ds_read_b128 v[14:17], v14 offset:3072
	ds_read_b128 v[18:21], v30
	ds_read_b128 v[22:25], v30 offset:1024
	ds_read_b128 v[26:29], v30 offset:2048
	ds_read_b128 v[30:33], v30 offset:3072
	s_add_u32 s24, s30, 0x158000
	s_addc_u32 s25, s31, 0
	s_mov_b32 m0, s34
	ds_read_b128 v[188:191], v187 offset:32768
	ds_read_b128 v[192:195], v187 offset:33792
	ds_read_b128 v[196:199], v187 offset:34816
	ds_read_b128 v[200:203], v187 offset:35840
	ds_read_b128 v[204:207], v187 offset:36864
	ds_read_b128 v[208:211], v187 offset:37888
	ds_read_b128 v[212:215], v187 offset:38912
	ds_read_b128 v[216:219], v187 offset:39936
	global_load_lds_dwordx4 v164, s[24:25]
	s_mov_b32 m0, s35
	s_nop 0
	global_load_lds_dwordx4 v162, s[24:25]
	s_waitcnt vmcnt(8) lgkmcnt(0)
	s_barrier
	v_mfma_f32_16x16x128_f8f6f4 v[122:125], v[10:17], v[204:211], v[122:125]
	v_mfma_f32_16x16x128_f8f6f4 v[126:129], v[2:9], v[204:211], v[126:129]
	v_mfma_f32_16x16x128_f8f6f4 v[158:161], v[2:9], v[188:195], v[158:161]
	v_mfma_f32_16x16x128_f8f6f4 v[154:157], v[10:17], v[188:195], v[154:157]
	v_mfma_f32_16x16x128_f8f6f4 v[138:141], v[10:17], v[196:203], v[138:141]
	v_mfma_f32_16x16x128_f8f6f4 v[142:145], v[2:9], v[196:203], v[142:145]
	v_mfma_f32_16x16x128_f8f6f4 v[110:113], v[2:9], v[212:219], v[110:113]
	v_mfma_f32_16x16x128_f8f6f4 v[106:109], v[10:17], v[212:219], v[106:109]
	v_mfma_f32_16x16x128_f8f6f4 v[102:105], v[18:25], v[212:219], v[102:105]
	v_mfma_f32_16x16x128_f8f6f4 v[98:101], v[26:33], v[212:219], v[98:101]
	v_mfma_f32_16x16x128_f8f6f4 v[146:149], v[26:33], v[188:195], v[146:149]
	v_mfma_f32_16x16x128_f8f6f4 v[150:153], v[18:25], v[188:195], v[150:153]
	v_mfma_f32_16x16x128_f8f6f4 v[134:137], v[18:25], v[196:203], v[134:137]
	v_mfma_f32_16x16x128_f8f6f4 v[130:133], v[26:33], v[196:203], v[130:133]
	v_mfma_f32_16x16x128_f8f6f4 v[114:117], v[26:33], v[204:211], v[114:117]
	v_mfma_f32_16x16x128_f8f6f4 v[118:121], v[18:25], v[204:211], v[118:121]
	s_barrier
	s_add_i32 s24, s59, s3
	v_lshl_add_u64 v[174:175], v[174:175], 0, s[12:13]
	s_mov_b32 m0, s24
	ds_read_b128 v[188:191], v187 offset:49152
	ds_read_b128 v[192:195], v187 offset:50176
	ds_read_b128 v[196:199], v187 offset:51200
	ds_read_b128 v[200:203], v187 offset:52224
	ds_read_b128 v[204:207], v187 offset:53248
	ds_read_b128 v[208:211], v187 offset:54272
	ds_read_b128 v[212:215], v187 offset:55296
	ds_read_b128 v[216:219], v187 offset:56320
	global_load_lds_dwordx4 v[174:175], off
	s_add_i32 m0, s24, 0x2000
	s_add_u32 s24, s28, 0x158080
	v_lshl_add_u64 v[174:175], v[176:177], 0, s[12:13]
	s_addc_u32 s25, s29, 0
	s_add_i32 s28, s60, s3
	global_load_lds_dwordx4 v[174:175], off
	s_mov_b32 m0, s28
	s_nop 0
	global_load_lds_dwordx4 v164, s[24:25]
	s_add_i32 m0, s28, 0x2000
	s_nop 0
	global_load_lds_dwordx4 v162, s[24:25]
	v_lshl_add_u64 v[174:175], v[178:179], 0, s[12:13]
	s_mov_b32 m0, s38
	s_nop 0
	global_load_lds_dwordx4 v[174:175], off
	v_lshl_add_u64 v[174:175], v[180:181], 0, s[12:13]
	s_mov_b32 m0, s39
	s_nop 0
	global_load_lds_dwordx4 v[174:175], off
	s_waitcnt vmcnt(8) lgkmcnt(0)
	s_barrier
	v_mfma_f32_16x16x128_f8f6f4 v[62:65], v[2:9], v[204:211], v[62:65]
	v_mfma_f32_16x16x128_f8f6f4 v[58:61], v[10:17], v[204:211], v[58:61]
	v_mfma_f32_16x16x128_f8f6f4 v[90:93], v[10:17], v[188:195], v[90:93]
	v_mfma_f32_16x16x128_f8f6f4 v[94:97], v[2:9], v[188:195], v[94:97]
	v_mfma_f32_16x16x128_f8f6f4 v[78:81], v[2:9], v[196:203], v[78:81]
	v_mfma_f32_16x16x128_f8f6f4 v[74:77], v[10:17], v[196:203], v[74:77]
	v_mfma_f32_16x16x128_f8f6f4 v[42:45], v[10:17], v[212:219], v[42:45]
	v_mfma_f32_16x16x128_f8f6f4 v[46:49], v[2:9], v[212:219], v[46:49]
	v_mfma_f32_16x16x128_f8f6f4 v[38:41], v[18:25], v[212:219], v[38:41]
	v_mfma_f32_16x16x128_f8f6f4 v[34:37], v[26:33], v[212:219], v[34:37]
	v_mfma_f32_16x16x128_f8f6f4 v[82:85], v[26:33], v[188:195], v[82:85]
	v_mfma_f32_16x16x128_f8f6f4 v[86:89], v[18:25], v[188:195], v[86:89]
	v_mfma_f32_16x16x128_f8f6f4 v[70:73], v[18:25], v[196:203], v[70:73]
	v_mfma_f32_16x16x128_f8f6f4 v[66:69], v[26:33], v[196:203], v[66:69]
	v_mfma_f32_16x16x128_f8f6f4 v[50:53], v[26:33], v[204:211], v[50:53]
	v_mfma_f32_16x16x128_f8f6f4 v[54:57], v[18:25], v[204:211], v[54:57]
	s_barrier
	s_add_i32 s58, s58, 2
	s_add_u32 s26, s26, 0x100
	s_addc_u32 s27, s27, 0
	s_add_u32 s50, s50, 0x100
	s_addc_u32 s51, s51, 0
	s_cmpk_gt_u32 s58, 0x53
	s_cbranch_scc0 .LBB0_318
	s_and_b64 vcc, exec, s[14:15]
	s_cbranch_vccz .LBB0_321
	s_barrier

.LBB0_332:
	s_add_u32 s6, s61, s4
	s_addc_u32 s7, s62, s5
	s_add_u32 s6, s6, 0x32800100
	s_addc_u32 s7, s7, 0
	s_add_u32 s24, s63, s4
	s_addc_u32 s25, s68, s5
	s_add_i32 s64, 0, 0x10000
	s_cmpk_eq_i32 s4, 0x2a00
	s_cselect_b32 s13, s1, s7
	s_cselect_b32 s12, s0, s6
	s_cselect_b32 s7, s29, s25
	s_cselect_b32 s6, s28, s24
	s_add_i32 s65, 0, 0x14000
	v_add_u32_e32 v2, s64, v188
	v_add_u32_e32 v6, s65, v188
	ds_read_b128 v[26:29], v2
	ds_read_b128 v[30:33], v2 offset:1024
	ds_read_b128 v[18:21], v2 offset:2048
	ds_read_b128 v[22:25], v2 offset:3072
	ds_read_b128 v[10:13], v6
	ds_read_b128 v[14:17], v6 offset:1024
	ds_read_b128 v[2:5], v6 offset:2048
	ds_read_b128 v[6:9], v6 offset:3072
	v_lshl_add_u64 v[214:215], v[168:169], 0, s[4:5]
	s_add_i32 m0, s18, 0xc000
	ds_read_b128 v[172:175], v189
	ds_read_b128 v[176:179], v189 offset:1024
	ds_read_b128 v[190:193], v189 offset:2048
	ds_read_b128 v[194:197], v189 offset:3072
	ds_read_b128 v[198:201], v189 offset:4096
	ds_read_b128 v[202:205], v189 offset:5120
	ds_read_b128 v[206:209], v189 offset:6144
	ds_read_b128 v[210:213], v189 offset:7168
	global_load_lds_dwordx4 v[214:215], off
	v_lshl_add_u64 v[214:215], v[170:171], 0, s[4:5]
	s_add_i32 m0, s18, 0xe000
	s_nop 0
	global_load_lds_dwordx4 v[214:215], off
	s_waitcnt vmcnt(8) lgkmcnt(0)
	s_barrier
	v_mfma_f32_16x16x128_f8f6f4 v[70:73], v[26:33], v[172:179], v[70:73]
	v_mfma_f32_16x16x128_f8f6f4 v[66:69], v[18:25], v[172:179], v[66:69]
	v_mfma_f32_16x16x128_f8f6f4 v[74:77], v[18:25], v[190:197], v[74:77]
	v_mfma_f32_16x16x128_f8f6f4 v[78:81], v[26:33], v[190:197], v[78:81]
	v_mfma_f32_16x16x128_f8f6f4 v[86:89], v[26:33], v[198:205], v[86:89]
	v_mfma_f32_16x16x128_f8f6f4 v[82:85], v[18:25], v[198:205], v[82:85]
	v_mfma_f32_16x16x128_f8f6f4 v[90:93], v[18:25], v[206:213], v[90:93]
	v_mfma_f32_16x16x128_f8f6f4 v[94:97], v[26:33], v[206:213], v[94:97]
	v_mfma_f32_16x16x128_f8f6f4 v[134:137], v[10:17], v[206:213], v[134:137]
	v_mfma_f32_16x16x128_f8f6f4 v[130:133], v[2:9], v[206:213], v[130:133]
	v_mfma_f32_16x16x128_f8f6f4 v[154:157], v[2:9], v[172:179], v[154:157]
	v_mfma_f32_16x16x128_f8f6f4 v[158:161], v[10:17], v[172:179], v[158:161]
	v_mfma_f32_16x16x128_f8f6f4 v[150:153], v[10:17], v[190:197], v[150:153]
	v_mfma_f32_16x16x128_f8f6f4 v[146:149], v[2:9], v[190:197], v[146:149]
	v_mfma_f32_16x16x128_f8f6f4 v[138:141], v[2:9], v[198:205], v[138:141]
	v_mfma_f32_16x16x128_f8f6f4 v[142:145], v[10:17], v[198:205], v[142:145]
	s_barrier
	s_add_i32 s24, s64, s17
	v_lshl_add_u64 v[172:173], s[6:7], 0, v[162:163]
	s_mov_b32 m0, s24
	ds_read_b128 v[190:193], v189 offset:16384
	ds_read_b128 v[194:197], v189 offset:17408
	ds_read_b128 v[198:201], v189 offset:18432
	ds_read_b128 v[202:205], v189 offset:19456
	ds_read_b128 v[206:209], v189 offset:20480
	ds_read_b128 v[210:213], v189 offset:21504
	ds_read_b128 v[214:217], v189 offset:22528
	ds_read_b128 v[218:221], v189 offset:23552
	global_load_lds_dwordx4 v[172:173], off
	s_add_i32 m0, s24, 0x2000
	s_add_u32 s24, s6, 0x158000
	v_lshl_add_u64 v[174:175], s[6:7], 0, v[166:167]
	s_addc_u32 s25, s7, 0
	s_add_i32 s64, s65, s17
	global_load_lds_dwordx4 v[174:175], off
	s_mov_b32 m0, s64
	v_lshl_add_u64 v[178:179], s[12:13], 0, v[166:167]
	global_load_lds_dwordx4 v162, s[24:25]
	s_add_i32 m0, s64, 0x2000
	s_nop 0
	global_load_lds_dwordx4 v166, s[24:25]
	v_lshl_add_u64 v[176:177], s[12:13], 0, v[162:163]
	s_mov_b32 m0, s18
	s_nop 0
	global_load_lds_dwordx4 v[176:177], off
	s_mov_b32 m0, s19
	s_nop 0
	global_load_lds_dwordx4 v[178:179], off
	s_waitcnt vmcnt(8) lgkmcnt(0)
	s_barrier
	v_mfma_f32_16x16x128_f8f6f4 v[110:113], v[26:33], v[198:205], v[110:113]
	v_mfma_f32_16x16x128_f8f6f4 v[106:109], v[18:25], v[198:205], v[106:109]
	v_mfma_f32_16x16x128_f8f6f4 v[98:101], v[18:25], v[190:197], v[98:101]
	v_mfma_f32_16x16x128_f8f6f4 v[102:105], v[26:33], v[190:197], v[102:105]
	v_mfma_f32_16x16x128_f8f6f4 v[118:121], v[26:33], v[206:213], v[118:121]
	v_mfma_f32_16x16x128_f8f6f4 v[114:117], v[18:25], v[206:213], v[114:117]
	v_mfma_f32_16x16x128_f8f6f4 v[122:125], v[18:25], v[214:221], v[122:125]
	v_mfma_f32_16x16x128_f8f6f4 v[126:129], v[26:33], v[214:221], v[126:129]
	v_mfma_f32_16x16x128_f8f6f4 v[62:65], v[10:17], v[214:221], v[62:65]
	v_mfma_f32_16x16x128_f8f6f4 v[58:61], v[2:9], v[214:221], v[58:61]
	v_mfma_f32_16x16x128_f8f6f4 v[34:37], v[2:9], v[190:197], v[34:37]
	v_mfma_f32_16x16x128_f8f6f4 v[38:41], v[10:17], v[190:197], v[38:41]
	v_mfma_f32_16x16x128_f8f6f4 v[46:49], v[10:17], v[198:205], v[46:49]
	v_mfma_f32_16x16x128_f8f6f4 v[42:45], v[2:9], v[198:205], v[42:45]
	v_mfma_f32_16x16x128_f8f6f4 v[50:53], v[2:9], v[206:213], v[50:53]
	v_mfma_f32_16x16x128_f8f6f4 v[54:57], v[10:17], v[206:213], v[54:57]
	s_barrier
	s_add_i32 s24, 0, 0x18000
	s_add_i32 s25, 0, 0x1c000
	v_add_u32_e32 v14, s24, v188
	v_add_u32_e32 v30, s25, v188
	ds_read_b128 v[2:5], v14
	ds_read_b128 v[6:9], v14 offset:1024
	ds_read_b128 v[10:13], v14 offset:2048
	ds_read_b128 v[14:17], v14 offset:3072
	ds_read_b128 v[18:21], v30
	ds_read_b128 v[22:25], v30 offset:1024
	ds_read_b128 v[26:29], v30 offset:2048
	ds_read_b128 v[30:33], v30 offset:3072
	s_add_u32 s12, s12, 0x158000
	s_addc_u32 s13, s13, 0
	s_mov_b32 m0, s93
	ds_read_b128 v[190:193], v189 offset:32768
	ds_read_b128 v[194:197], v189 offset:33792
	ds_read_b128 v[198:201], v189 offset:34816
	ds_read_b128 v[202:205], v189 offset:35840
	ds_read_b128 v[206:209], v189 offset:36864
	ds_read_b128 v[210:213], v189 offset:37888
	ds_read_b128 v[214:217], v189 offset:38912
	ds_read_b128 v[218:221], v189 offset:39936
	global_load_lds_dwordx4 v162, s[12:13]
	s_mov_b32 m0, s94
	s_nop 0
	global_load_lds_dwordx4 v166, s[12:13]
	s_waitcnt vmcnt(8) lgkmcnt(0)
	s_barrier
	v_mfma_f32_16x16x128_f8f6f4 v[82:85], v[10:17], v[206:213], v[82:85]
	v_mfma_f32_16x16x128_f8f6f4 v[86:89], v[2:9], v[206:213], v[86:89]
	v_mfma_f32_16x16x128_f8f6f4 v[70:73], v[2:9], v[190:197], v[70:73]
	v_mfma_f32_16x16x128_f8f6f4 v[66:69], v[10:17], v[190:197], v[66:69]
	v_mfma_f32_16x16x128_f8f6f4 v[74:77], v[10:17], v[198:205], v[74:77]
	v_mfma_f32_16x16x128_f8f6f4 v[78:81], v[2:9], v[198:205], v[78:81]
	v_mfma_f32_16x16x128_f8f6f4 v[94:97], v[2:9], v[214:221], v[94:97]
	v_mfma_f32_16x16x128_f8f6f4 v[90:93], v[10:17], v[214:221], v[90:93]
	v_mfma_f32_16x16x128_f8f6f4 v[134:137], v[18:25], v[214:221], v[134:137]
	v_mfma_f32_16x16x128_f8f6f4 v[130:133], v[26:33], v[214:221], v[130:133]
	v_mfma_f32_16x16x128_f8f6f4 v[154:157], v[26:33], v[190:197], v[154:157]
	v_mfma_f32_16x16x128_f8f6f4 v[158:161], v[18:25], v[190:197], v[158:161]
	v_mfma_f32_16x16x128_f8f6f4 v[150:153], v[18:25], v[198:205], v[150:153]
	v_mfma_f32_16x16x128_f8f6f4 v[146:149], v[26:33], v[198:205], v[146:149]
	v_mfma_f32_16x16x128_f8f6f4 v[138:141], v[26:33], v[206:213], v[138:141]
	v_mfma_f32_16x16x128_f8f6f4 v[142:145], v[18:25], v[206:213], v[142:145]
	s_barrier
	s_add_i32 s12, s24, s17
	v_lshl_add_u64 v[172:173], v[172:173], 0, s[76:77]
	s_mov_b32 m0, s12
	ds_read_b128 v[190:193], v189 offset:49152
	ds_read_b128 v[194:197], v189 offset:50176
	ds_read_b128 v[198:201], v189 offset:51200
	ds_read_b128 v[202:205], v189 offset:52224
	ds_read_b128 v[206:209], v189 offset:53248
	ds_read_b128 v[210:213], v189 offset:54272
	ds_read_b128 v[214:217], v189 offset:55296
	ds_read_b128 v[218:221], v189 offset:56320
	global_load_lds_dwordx4 v[172:173], off
	s_add_i32 m0, s12, 0x2000
	s_add_u32 s6, s6, 0x158080
	v_lshl_add_u64 v[172:173], v[174:175], 0, s[76:77]
	s_addc_u32 s7, s7, 0
	s_add_i32 s12, s25, s17
	global_load_lds_dwordx4 v[172:173], off
	s_mov_b32 m0, s12
	s_nop 0
	global_load_lds_dwordx4 v162, s[6:7]
	s_add_i32 m0, s12, 0x2000
	s_nop 0
	global_load_lds_dwordx4 v166, s[6:7]
	v_lshl_add_u64 v[172:173], v[176:177], 0, s[76:77]
	s_mov_b32 m0, s95
	s_nop 0
	global_load_lds_dwordx4 v[172:173], off
	v_lshl_add_u64 v[172:173], v[178:179], 0, s[76:77]
	s_mov_b32 m0, vcc_lo
	s_nop 0
	global_load_lds_dwordx4 v[172:173], off
	s_waitcnt vmcnt(8) lgkmcnt(0)
	s_barrier
	v_mfma_f32_16x16x128_f8f6f4 v[118:121], v[2:9], v[206:213], v[118:121]
	v_mfma_f32_16x16x128_f8f6f4 v[114:117], v[10:17], v[206:213], v[114:117]
	v_mfma_f32_16x16x128_f8f6f4 v[98:101], v[10:17], v[190:197], v[98:101]
	v_mfma_f32_16x16x128_f8f6f4 v[102:105], v[2:9], v[190:197], v[102:105]
	v_mfma_f32_16x16x128_f8f6f4 v[110:113], v[2:9], v[198:205], v[110:113]
	v_mfma_f32_16x16x128_f8f6f4 v[106:109], v[10:17], v[198:205], v[106:109]
	v_mfma_f32_16x16x128_f8f6f4 v[122:125], v[10:17], v[214:221], v[122:125]
	v_mfma_f32_16x16x128_f8f6f4 v[126:129], v[2:9], v[214:221], v[126:129]
	v_mfma_f32_16x16x128_f8f6f4 v[62:65], v[18:25], v[214:221], v[62:65]
	v_mfma_f32_16x16x128_f8f6f4 v[58:61], v[26:33], v[214:221], v[58:61]
	v_mfma_f32_16x16x128_f8f6f4 v[34:37], v[26:33], v[190:197], v[34:37]
	v_mfma_f32_16x16x128_f8f6f4 v[38:41], v[18:25], v[190:197], v[38:41]
	v_mfma_f32_16x16x128_f8f6f4 v[46:49], v[18:25], v[198:205], v[46:49]
	v_mfma_f32_16x16x128_f8f6f4 v[42:45], v[26:33], v[198:205], v[42:45]
	v_mfma_f32_16x16x128_f8f6f4 v[50:53], v[26:33], v[206:213], v[50:53]
	v_mfma_f32_16x16x128_f8f6f4 v[54:57], v[18:25], v[206:213], v[54:57]
	s_barrier
	s_add_i32 vcc_hi, vcc_hi, 2
	s_add_u32 s4, s4, 0x100
	s_addc_u32 s5, s5, 0
	s_cmpk_lt_u32 vcc_hi, 0x54
	s_cbranch_scc1 .LBB0_332
	s_waitcnt vmcnt(0)
	s_mov_b64 s[12:13], s[54:55]
	s_cmpk_gt_u32 s89, 0xff
	s_cbranch_scc1 .LBB0_335
	s_barrier

.LBB0_758:
	ds_read_b128 v[148:151], v146
	ds_read_b128 v[152:155], v146 offset:1024
	ds_read_b128 v[156:159], v146 offset:2048
	ds_read_b128 v[160:163], v146 offset:3072
	ds_read_b128 v[164:167], v147
	ds_read_b128 v[168:171], v147 offset:1024
	ds_read_b128 v[172:175], v147 offset:2048
	ds_read_b128 v[176:179], v147 offset:3072
	s_add_u32 s16, s42, s14
	s_addc_u32 s17, s43, s15
	s_add_u32 s16, s16, 0x2a800100
	s_addc_u32 s17, s17, 0
	s_add_u32 s60, s48, s14
	s_addc_u32 s61, s49, s15
	s_cmpk_eq_i32 s14, 0x700
	s_cselect_b32 s21, s13, s17
	s_cselect_b32 s20, s12, s16
	s_cselect_b32 s17, s11, s61
	s_cselect_b32 s16, s10, s60
	s_mov_b32 m0, s51
	v_lshl_add_u64 v[212:213], v[138:139], 0, s[14:15]
	ds_read_b128 v[180:183], v145
	ds_read_b128 v[184:187], v145 offset:1024
	ds_read_b128 v[188:191], v145 offset:2048
	ds_read_b128 v[192:195], v145 offset:3072
	ds_read_b128 v[196:199], v145 offset:4096
	ds_read_b128 v[200:203], v145 offset:5120
	ds_read_b128 v[204:207], v145 offset:6144
	ds_read_b128 v[208:211], v145 offset:7168
	global_load_lds_dwordx4 v[212:213], off
	v_lshl_add_u64 v[212:213], v[140:141], 0, s[14:15]
	s_mov_b32 m0, s58
	s_nop 0
	global_load_lds_dwordx4 v[212:213], off
	s_waitcnt vmcnt(8) lgkmcnt(0)
	s_barrier
	v_mfma_f32_16x16x32_bf16 v[126:129], v[148:151], v[180:183], v[126:129]
	v_mfma_f32_16x16x32_bf16 v[122:125], v[156:159], v[180:183], v[122:125]
	v_mfma_f32_16x16x32_bf16 v[118:121], v[148:151], v[188:191], v[118:121]
	v_mfma_f32_16x16x32_bf16 v[114:117], v[156:159], v[188:191], v[114:117]
	v_mfma_f32_16x16x32_bf16 v[106:109], v[148:151], v[196:199], v[106:109]
	v_mfma_f32_16x16x32_bf16 v[98:101], v[156:159], v[196:199], v[98:101]
	v_mfma_f32_16x16x32_bf16 v[90:93], v[148:151], v[204:207], v[90:93]
	v_mfma_f32_16x16x32_bf16 v[82:85], v[156:159], v[204:207], v[82:85]
	v_mfma_f32_16x16x32_bf16 v[126:129], v[152:155], v[184:187], v[126:129]
	v_mfma_f32_16x16x32_bf16 v[122:125], v[160:163], v[184:187], v[122:125]
	v_mfma_f32_16x16x32_bf16 v[118:121], v[152:155], v[192:195], v[118:121]
	v_mfma_f32_16x16x32_bf16 v[114:117], v[160:163], v[192:195], v[114:117]
	v_mfma_f32_16x16x32_bf16 v[106:109], v[152:155], v[200:203], v[106:109]
	v_mfma_f32_16x16x32_bf16 v[98:101], v[160:163], v[200:203], v[98:101]
	v_mfma_f32_16x16x32_bf16 v[90:93], v[152:155], v[208:211], v[90:93]
	v_mfma_f32_16x16x32_bf16 v[82:85], v[160:163], v[208:211], v[82:85]
	v_mfma_f32_16x16x32_bf16 v[110:113], v[164:167], v[180:183], v[110:113]
	v_mfma_f32_16x16x32_bf16 v[102:105], v[172:175], v[180:183], v[102:105]
	v_mfma_f32_16x16x32_bf16 v[94:97], v[164:167], v[188:191], v[94:97]
	v_mfma_f32_16x16x32_bf16 v[86:89], v[172:175], v[188:191], v[86:89]
	v_mfma_f32_16x16x32_bf16 v[78:81], v[164:167], v[196:199], v[78:81]
	v_mfma_f32_16x16x32_bf16 v[74:77], v[172:175], v[196:199], v[74:77]
	v_mfma_f32_16x16x32_bf16 v[70:73], v[164:167], v[204:207], v[70:73]
	v_mfma_f32_16x16x32_bf16 v[66:69], v[172:175], v[204:207], v[66:69]
	v_mfma_f32_16x16x32_bf16 v[110:113], v[168:171], v[184:187], v[110:113]
	v_mfma_f32_16x16x32_bf16 v[102:105], v[176:179], v[184:187], v[102:105]
	v_mfma_f32_16x16x32_bf16 v[94:97], v[168:171], v[192:195], v[94:97]
	v_mfma_f32_16x16x32_bf16 v[86:89], v[176:179], v[192:195], v[86:89]
	v_mfma_f32_16x16x32_bf16 v[78:81], v[168:171], v[200:203], v[78:81]
	v_mfma_f32_16x16x32_bf16 v[74:77], v[176:179], v[200:203], v[74:77]
	v_mfma_f32_16x16x32_bf16 v[70:73], v[168:171], v[208:211], v[70:73]
	v_mfma_f32_16x16x32_bf16 v[66:69], v[176:179], v[208:211], v[66:69]
	s_barrier
	s_mov_b32 m0, s59
	v_lshl_add_u64 v[212:213], s[16:17], 0, v[130:131]
	ds_read_b128 v[180:183], v145 offset:16384
	ds_read_b128 v[184:187], v145 offset:17408
	ds_read_b128 v[188:191], v145 offset:18432
	ds_read_b128 v[192:195], v145 offset:19456
	ds_read_b128 v[196:199], v145 offset:20480
	ds_read_b128 v[200:203], v145 offset:21504
	ds_read_b128 v[204:207], v145 offset:22528
	ds_read_b128 v[208:211], v145 offset:23552
	global_load_lds_dwordx4 v[212:213], off
	s_add_i32 m0, s59, 0x2000
	s_add_u32 s60, s16, 0x100000
	v_lshl_add_u64 v[214:215], s[16:17], 0, v[136:137]
	s_addc_u32 s61, s17, 0
	s_add_i32 s62, s26, s31
	global_load_lds_dwordx4 v[214:215], off
	v_lshl_add_u64 v[216:217], s[60:61], 0, v[130:131]
	s_mov_b32 m0, s62
	v_lshl_add_u64 v[218:219], s[20:21], 0, v[134:135]
	global_load_lds_dwordx4 v[216:217], off
	v_lshl_add_u64 v[216:217], s[60:61], 0, v[136:137]
	s_add_i32 m0, s62, 0x2000
	s_nop 0
	global_load_lds_dwordx4 v[216:217], off
	v_lshl_add_u64 v[216:217], s[20:21], 0, v[132:133]
	s_mov_b32 m0, s7
	s_nop 0
	global_load_lds_dwordx4 v[216:217], off
	s_mov_b32 m0, s34
	s_nop 0
	global_load_lds_dwordx4 v[218:219], off
	s_waitcnt vmcnt(8) lgkmcnt(0)
	s_barrier
	v_mfma_f32_16x16x32_bf16 v[62:65], v[148:151], v[180:183], v[62:65]
	v_mfma_f32_16x16x32_bf16 v[58:61], v[156:159], v[180:183], v[58:61]
	v_mfma_f32_16x16x32_bf16 v[54:57], v[148:151], v[188:191], v[54:57]
	v_mfma_f32_16x16x32_bf16 v[50:53], v[156:159], v[188:191], v[50:53]
	v_mfma_f32_16x16x32_bf16 v[42:45], v[148:151], v[196:199], v[42:45]
	v_mfma_f32_16x16x32_bf16 v[34:37], v[156:159], v[196:199], v[34:37]
	v_mfma_f32_16x16x32_bf16 v[26:29], v[148:151], v[204:207], v[26:29]
	v_mfma_f32_16x16x32_bf16 v[18:21], v[156:159], v[204:207], v[18:21]
	v_mfma_f32_16x16x32_bf16 v[62:65], v[152:155], v[184:187], v[62:65]
	v_mfma_f32_16x16x32_bf16 v[58:61], v[160:163], v[184:187], v[58:61]
	v_mfma_f32_16x16x32_bf16 v[54:57], v[152:155], v[192:195], v[54:57]
	v_mfma_f32_16x16x32_bf16 v[50:53], v[160:163], v[192:195], v[50:53]
	v_mfma_f32_16x16x32_bf16 v[42:45], v[152:155], v[200:203], v[42:45]
	v_mfma_f32_16x16x32_bf16 v[34:37], v[160:163], v[200:203], v[34:37]
	v_mfma_f32_16x16x32_bf16 v[26:29], v[152:155], v[208:211], v[26:29]
	v_mfma_f32_16x16x32_bf16 v[18:21], v[160:163], v[208:211], v[18:21]
	v_mfma_f32_16x16x32_bf16 v[46:49], v[164:167], v[180:183], v[46:49]
	v_mfma_f32_16x16x32_bf16 v[38:41], v[172:175], v[180:183], v[38:41]
	v_mfma_f32_16x16x32_bf16 v[30:33], v[164:167], v[188:191], v[30:33]
	v_mfma_f32_16x16x32_bf16 v[22:25], v[172:175], v[188:191], v[22:25]
	v_mfma_f32_16x16x32_bf16 v[14:17], v[164:167], v[196:199], v[14:17]
	v_mfma_f32_16x16x32_bf16 v[10:13], v[172:175], v[196:199], v[10:13]
	v_mfma_f32_16x16x32_bf16 v[6:9], v[164:167], v[204:207], v[6:9]
	v_mfma_f32_16x16x32_bf16 v[2:5], v[172:175], v[204:207], v[2:5]
	v_mfma_f32_16x16x32_bf16 v[46:49], v[168:171], v[184:187], v[46:49]
	v_mfma_f32_16x16x32_bf16 v[38:41], v[176:179], v[184:187], v[38:41]
	v_mfma_f32_16x16x32_bf16 v[30:33], v[168:171], v[192:195], v[30:33]
	v_mfma_f32_16x16x32_bf16 v[22:25], v[176:179], v[192:195], v[22:25]
	v_mfma_f32_16x16x32_bf16 v[14:17], v[168:171], v[200:203], v[14:17]
	v_mfma_f32_16x16x32_bf16 v[10:13], v[176:179], v[200:203], v[10:13]
	v_mfma_f32_16x16x32_bf16 v[6:9], v[168:171], v[208:211], v[6:9]
	v_mfma_f32_16x16x32_bf16 v[2:5], v[176:179], v[208:211], v[2:5]
	s_barrier
	s_add_i32 s60, 0, 0x18000
	s_add_i32 s61, 0, 0x1c000
	v_add_u32_e32 v160, s60, v144
	v_add_u32_e32 v176, s61, v144
	ds_read_b128 v[148:151], v160
	ds_read_b128 v[152:155], v160 offset:1024
	ds_read_b128 v[156:159], v160 offset:2048
	ds_read_b128 v[160:163], v160 offset:3072
	ds_read_b128 v[164:167], v176
	ds_read_b128 v[168:171], v176 offset:1024
	ds_read_b128 v[172:175], v176 offset:2048
	ds_read_b128 v[176:179], v176 offset:3072
	s_add_u32 s20, s20, 0x100000
	s_addc_u32 s21, s21, 0
	s_mov_b32 m0, s35
	v_lshl_add_u64 v[220:221], s[20:21], 0, v[132:133]
	ds_read_b128 v[180:183], v145 offset:32768
	ds_read_b128 v[184:187], v145 offset:33792
	ds_read_b128 v[188:191], v145 offset:34816
	ds_read_b128 v[192:195], v145 offset:35840
	ds_read_b128 v[196:199], v145 offset:36864
	ds_read_b128 v[200:203], v145 offset:37888
	ds_read_b128 v[204:207], v145 offset:38912
	ds_read_b128 v[208:211], v145 offset:39936
	global_load_lds_dwordx4 v[220:221], off
	v_lshl_add_u64 v[220:221], s[20:21], 0, v[134:135]
	s_mov_b32 m0, s38
	s_nop 0
	global_load_lds_dwordx4 v[220:221], off
	s_waitcnt vmcnt(8) lgkmcnt(0)
	s_barrier
	v_mfma_f32_16x16x32_bf16 v[126:129], v[148:151], v[180:183], v[126:129]
	v_mfma_f32_16x16x32_bf16 v[122:125], v[156:159], v[180:183], v[122:125]
	v_mfma_f32_16x16x32_bf16 v[118:121], v[148:151], v[188:191], v[118:121]
	v_mfma_f32_16x16x32_bf16 v[114:117], v[156:159], v[188:191], v[114:117]
	v_mfma_f32_16x16x32_bf16 v[106:109], v[148:151], v[196:199], v[106:109]
	v_mfma_f32_16x16x32_bf16 v[98:101], v[156:159], v[196:199], v[98:101]
	v_mfma_f32_16x16x32_bf16 v[90:93], v[148:151], v[204:207], v[90:93]
	v_mfma_f32_16x16x32_bf16 v[82:85], v[156:159], v[204:207], v[82:85]
	v_mfma_f32_16x16x32_bf16 v[126:129], v[152:155], v[184:187], v[126:129]
	v_mfma_f32_16x16x32_bf16 v[122:125], v[160:163], v[184:187], v[122:125]
	v_mfma_f32_16x16x32_bf16 v[118:121], v[152:155], v[192:195], v[118:121]
	v_mfma_f32_16x16x32_bf16 v[114:117], v[160:163], v[192:195], v[114:117]
	v_mfma_f32_16x16x32_bf16 v[106:109], v[152:155], v[200:203], v[106:109]
	v_mfma_f32_16x16x32_bf16 v[98:101], v[160:163], v[200:203], v[98:101]
	v_mfma_f32_16x16x32_bf16 v[90:93], v[152:155], v[208:211], v[90:93]
	v_mfma_f32_16x16x32_bf16 v[82:85], v[160:163], v[208:211], v[82:85]
	v_mfma_f32_16x16x32_bf16 v[110:113], v[164:167], v[180:183], v[110:113]
	v_mfma_f32_16x16x32_bf16 v[102:105], v[172:175], v[180:183], v[102:105]
	v_mfma_f32_16x16x32_bf16 v[94:97], v[164:167], v[188:191], v[94:97]
	v_mfma_f32_16x16x32_bf16 v[86:89], v[172:175], v[188:191], v[86:89]
	v_mfma_f32_16x16x32_bf16 v[78:81], v[164:167], v[196:199], v[78:81]
	v_mfma_f32_16x16x32_bf16 v[74:77], v[172:175], v[196:199], v[74:77]
	v_mfma_f32_16x16x32_bf16 v[70:73], v[164:167], v[204:207], v[70:73]
	v_mfma_f32_16x16x32_bf16 v[66:69], v[172:175], v[204:207], v[66:69]
	v_mfma_f32_16x16x32_bf16 v[110:113], v[168:171], v[184:187], v[110:113]
	v_mfma_f32_16x16x32_bf16 v[102:105], v[176:179], v[184:187], v[102:105]
	v_mfma_f32_16x16x32_bf16 v[94:97], v[168:171], v[192:195], v[94:97]
	v_mfma_f32_16x16x32_bf16 v[86:89], v[176:179], v[192:195], v[86:89]
	v_mfma_f32_16x16x32_bf16 v[78:81], v[168:171], v[200:203], v[78:81]
	v_mfma_f32_16x16x32_bf16 v[74:77], v[176:179], v[200:203], v[74:77]
	v_mfma_f32_16x16x32_bf16 v[70:73], v[168:171], v[208:211], v[70:73]
	v_mfma_f32_16x16x32_bf16 v[66:69], v[176:179], v[208:211], v[66:69]
	s_barrier
	s_add_i32 s20, s60, s31
	v_lshl_add_u64 v[212:213], v[212:213], 0, s[4:5]
	s_mov_b32 m0, s20
	ds_read_b128 v[180:183], v145 offset:49152
	ds_read_b128 v[184:187], v145 offset:50176
	ds_read_b128 v[188:191], v145 offset:51200
	ds_read_b128 v[192:195], v145 offset:52224
	ds_read_b128 v[196:199], v145 offset:53248
	ds_read_b128 v[200:203], v145 offset:54272
	ds_read_b128 v[204:207], v145 offset:55296
	ds_read_b128 v[208:211], v145 offset:56320
	global_load_lds_dwordx4 v[212:213], off
	s_add_i32 m0, s20, 0x2000
	s_add_u32 s16, s16, 0x100080
	v_lshl_add_u64 v[212:213], v[214:215], 0, s[4:5]
	s_addc_u32 s17, s17, 0
	s_add_i32 s20, s61, s31
	global_load_lds_dwordx4 v[212:213], off
	v_lshl_add_u64 v[212:213], s[16:17], 0, v[130:131]
	s_mov_b32 m0, s20
	s_nop 0
	global_load_lds_dwordx4 v[212:213], off
	v_lshl_add_u64 v[212:213], s[16:17], 0, v[136:137]
	s_add_i32 m0, s20, 0x2000
	s_nop 0
	global_load_lds_dwordx4 v[212:213], off
	v_lshl_add_u64 v[212:213], v[216:217], 0, s[4:5]
	s_mov_b32 m0, s40
	s_nop 0
	global_load_lds_dwordx4 v[212:213], off
	v_lshl_add_u64 v[212:213], v[218:219], 0, s[4:5]
	s_mov_b32 m0, s41
	s_nop 0
	global_load_lds_dwordx4 v[212:213], off
	s_waitcnt vmcnt(8) lgkmcnt(0)
	s_barrier
	v_mfma_f32_16x16x32_bf16 v[62:65], v[148:151], v[180:183], v[62:65]
	v_mfma_f32_16x16x32_bf16 v[58:61], v[156:159], v[180:183], v[58:61]
	v_mfma_f32_16x16x32_bf16 v[54:57], v[148:151], v[188:191], v[54:57]
	v_mfma_f32_16x16x32_bf16 v[50:53], v[156:159], v[188:191], v[50:53]
	v_mfma_f32_16x16x32_bf16 v[42:45], v[148:151], v[196:199], v[42:45]
	v_mfma_f32_16x16x32_bf16 v[34:37], v[156:159], v[196:199], v[34:37]
	v_mfma_f32_16x16x32_bf16 v[26:29], v[148:151], v[204:207], v[26:29]
	v_mfma_f32_16x16x32_bf16 v[18:21], v[156:159], v[204:207], v[18:21]
	v_mfma_f32_16x16x32_bf16 v[62:65], v[152:155], v[184:187], v[62:65]
	v_mfma_f32_16x16x32_bf16 v[58:61], v[160:163], v[184:187], v[58:61]
	v_mfma_f32_16x16x32_bf16 v[54:57], v[152:155], v[192:195], v[54:57]
	v_mfma_f32_16x16x32_bf16 v[50:53], v[160:163], v[192:195], v[50:53]
	v_mfma_f32_16x16x32_bf16 v[42:45], v[152:155], v[200:203], v[42:45]
	v_mfma_f32_16x16x32_bf16 v[34:37], v[160:163], v[200:203], v[34:37]
	v_mfma_f32_16x16x32_bf16 v[26:29], v[152:155], v[208:211], v[26:29]
	v_mfma_f32_16x16x32_bf16 v[18:21], v[160:163], v[208:211], v[18:21]
	v_mfma_f32_16x16x32_bf16 v[46:49], v[164:167], v[180:183], v[46:49]
	v_mfma_f32_16x16x32_bf16 v[38:41], v[172:175], v[180:183], v[38:41]
	v_mfma_f32_16x16x32_bf16 v[30:33], v[164:167], v[188:191], v[30:33]
	v_mfma_f32_16x16x32_bf16 v[22:25], v[172:175], v[188:191], v[22:25]
	v_mfma_f32_16x16x32_bf16 v[14:17], v[164:167], v[196:199], v[14:17]
	v_mfma_f32_16x16x32_bf16 v[10:13], v[172:175], v[196:199], v[10:13]
	v_mfma_f32_16x16x32_bf16 v[6:9], v[164:167], v[204:207], v[6:9]
	v_mfma_f32_16x16x32_bf16 v[2:5], v[172:175], v[204:207], v[2:5]
	v_mfma_f32_16x16x32_bf16 v[46:49], v[168:171], v[184:187], v[46:49]
	v_mfma_f32_16x16x32_bf16 v[38:41], v[176:179], v[184:187], v[38:41]
	v_mfma_f32_16x16x32_bf16 v[30:33], v[168:171], v[192:195], v[30:33]
	v_mfma_f32_16x16x32_bf16 v[22:25], v[176:179], v[192:195], v[22:25]
	v_mfma_f32_16x16x32_bf16 v[14:17], v[168:171], v[200:203], v[14:17]
	v_mfma_f32_16x16x32_bf16 v[10:13], v[176:179], v[200:203], v[10:13]
	v_mfma_f32_16x16x32_bf16 v[6:9], v[168:171], v[208:211], v[6:9]
	v_mfma_f32_16x16x32_bf16 v[2:5], v[176:179], v[208:211], v[2:5]
	s_barrier
	s_add_i32 s50, s50, 2
	s_add_u32 s14, s14, 0x100
	s_addc_u32 s15, s15, 0
	s_cmp_gt_u32 s50, 13
	s_cbranch_scc0 .LBB0_758
	s_cmpk_lt_u32 s30, 0x100
	s_cbranch_scc0 .LBB0_754
	s_barrier
	s_branch .LBB0_754

.LBB0_768:
	ds_read_b128 v[130:133], v1
	ds_read_b128 v[134:137], v1 offset:1024
	ds_read_b128 v[138:141], v1 offset:2048
	ds_read_b128 v[142:145], v1 offset:3072
	ds_read_b128 v[180:183], v176
	ds_read_b128 v[184:187], v176 offset:1024
	ds_read_b128 v[188:191], v176 offset:2048
	ds_read_b128 v[192:195], v176 offset:3072
	s_add_u32 s1, s16, 0xfff00080
	s_addc_u32 s20, s17, -1
	s_add_u32 s49, s16, 0xdb300080
	s_addc_u32 s21, s17, -1
	s_cmp_eq_u32 s0, 60
	s_cselect_b32 s25, s55, s20
	s_cselect_b32 s24, s54, s1
	s_cselect_b32 s21, s9, s21
	s_cselect_b32 s20, s8, s49
	s_mov_b32 m0, s35
	v_lshl_add_u64 v[228:229], s[16:17], 0, v[172:173]
	ds_read_b128 v[196:199], v177
	ds_read_b128 v[200:203], v177 offset:1024
	ds_read_b128 v[204:207], v177 offset:2048
	ds_read_b128 v[208:211], v177 offset:3072
	ds_read_b128 v[212:215], v177 offset:4096
	ds_read_b128 v[216:219], v177 offset:5120
	ds_read_b128 v[220:223], v177 offset:6144
	ds_read_b128 v[224:227], v177 offset:7168
	global_load_lds_dwordx4 v[228:229], off
	v_lshl_add_u64 v[228:229], s[16:17], 0, v[174:175]
	s_mov_b32 m0, s36
	s_nop 0
	global_load_lds_dwordx4 v[228:229], off
	s_waitcnt vmcnt(8) lgkmcnt(0)
	s_barrier
	v_mfma_f32_16x16x32_bf16 v[126:129], v[130:133], v[196:199], v[126:129]
	v_mfma_f32_16x16x32_bf16 v[122:125], v[138:141], v[196:199], v[122:125]
	v_mfma_f32_16x16x32_bf16 v[114:117], v[130:133], v[204:207], v[114:117]
	v_mfma_f32_16x16x32_bf16 v[106:109], v[138:141], v[204:207], v[106:109]
	v_mfma_f32_16x16x32_bf16 v[98:101], v[130:133], v[212:215], v[98:101]
	v_mfma_f32_16x16x32_bf16 v[90:93], v[138:141], v[212:215], v[90:93]
	v_mfma_f32_16x16x32_bf16 v[82:85], v[130:133], v[220:223], v[82:85]
	v_mfma_f32_16x16x32_bf16 v[74:77], v[138:141], v[220:223], v[74:77]
	v_mfma_f32_16x16x32_bf16 v[126:129], v[134:137], v[200:203], v[126:129]
	v_mfma_f32_16x16x32_bf16 v[122:125], v[142:145], v[200:203], v[122:125]
	v_mfma_f32_16x16x32_bf16 v[114:117], v[134:137], v[208:211], v[114:117]
	v_mfma_f32_16x16x32_bf16 v[106:109], v[142:145], v[208:211], v[106:109]
	v_mfma_f32_16x16x32_bf16 v[98:101], v[134:137], v[216:219], v[98:101]
	v_mfma_f32_16x16x32_bf16 v[90:93], v[142:145], v[216:219], v[90:93]
	v_mfma_f32_16x16x32_bf16 v[82:85], v[134:137], v[224:227], v[82:85]
	v_mfma_f32_16x16x32_bf16 v[74:77], v[142:145], v[224:227], v[74:77]
	v_mfma_f32_16x16x32_bf16 v[118:121], v[180:183], v[196:199], v[118:121]
	v_mfma_f32_16x16x32_bf16 v[110:113], v[188:191], v[196:199], v[110:113]
	v_mfma_f32_16x16x32_bf16 v[102:105], v[180:183], v[204:207], v[102:105]
	v_mfma_f32_16x16x32_bf16 v[94:97], v[188:191], v[204:207], v[94:97]
	v_mfma_f32_16x16x32_bf16 v[86:89], v[180:183], v[212:215], v[86:89]
	v_mfma_f32_16x16x32_bf16 v[78:81], v[188:191], v[212:215], v[78:81]
	v_mfma_f32_16x16x32_bf16 v[70:73], v[180:183], v[220:223], v[70:73]
	v_mfma_f32_16x16x32_bf16 v[66:69], v[188:191], v[220:223], v[66:69]
	v_mfma_f32_16x16x32_bf16 v[118:121], v[184:187], v[200:203], v[118:121]
	v_mfma_f32_16x16x32_bf16 v[110:113], v[192:195], v[200:203], v[110:113]
	v_mfma_f32_16x16x32_bf16 v[102:105], v[184:187], v[208:211], v[102:105]
	v_mfma_f32_16x16x32_bf16 v[94:97], v[192:195], v[208:211], v[94:97]
	v_mfma_f32_16x16x32_bf16 v[86:89], v[184:187], v[216:219], v[86:89]
	v_mfma_f32_16x16x32_bf16 v[78:81], v[192:195], v[216:219], v[78:81]
	v_mfma_f32_16x16x32_bf16 v[70:73], v[184:187], v[224:227], v[70:73]
	v_mfma_f32_16x16x32_bf16 v[66:69], v[192:195], v[224:227], v[66:69]
	s_barrier
	s_mov_b32 m0, s37
	v_lshl_add_u64 v[228:229], s[20:21], 0, v[150:151]
	s_add_u32 s50, s20, 0x100000
	ds_read_b128 v[196:199], v177 offset:16384
	ds_read_b128 v[200:203], v177 offset:17408
	ds_read_b128 v[204:207], v177 offset:18432
	ds_read_b128 v[208:211], v177 offset:19456
	ds_read_b128 v[212:215], v177 offset:20480
	ds_read_b128 v[216:219], v177 offset:21504
	ds_read_b128 v[220:223], v177 offset:22528
	ds_read_b128 v[224:227], v177 offset:23552
	global_load_lds_dwordx4 v[228:229], off
	v_lshl_add_u64 v[230:231], s[20:21], 0, v[146:147]
	s_mov_b32 m0, s38
	s_addc_u32 s51, s21, 0
	global_load_lds_dwordx4 v[230:231], off
	v_lshl_add_u64 v[232:233], s[50:51], 0, v[150:151]
	s_mov_b32 m0, s39
	v_lshl_add_u64 v[234:235], s[24:25], 0, v[148:149]
	global_load_lds_dwordx4 v[232:233], off
	v_lshl_add_u64 v[232:233], s[50:51], 0, v[146:147]
	s_mov_b32 m0, s40
	s_nop 0
	global_load_lds_dwordx4 v[232:233], off
	v_lshl_add_u64 v[232:233], s[24:25], 0, v[152:153]
	s_mov_b32 m0, s26
	s_nop 0
	global_load_lds_dwordx4 v[232:233], off
	s_mov_b32 m0, s27
	s_nop 0
	global_load_lds_dwordx4 v[234:235], off
	s_waitcnt vmcnt(8) lgkmcnt(0)
	s_barrier
	v_mfma_f32_16x16x32_bf16 v[62:65], v[130:133], v[196:199], v[62:65]
	v_mfma_f32_16x16x32_bf16 v[58:61], v[138:141], v[196:199], v[58:61]
	v_mfma_f32_16x16x32_bf16 v[50:53], v[130:133], v[204:207], v[50:53]
	v_mfma_f32_16x16x32_bf16 v[42:45], v[138:141], v[204:207], v[42:45]
	v_mfma_f32_16x16x32_bf16 v[34:37], v[130:133], v[212:215], v[34:37]
	v_mfma_f32_16x16x32_bf16 v[26:29], v[138:141], v[212:215], v[26:29]
	v_mfma_f32_16x16x32_bf16 v[18:21], v[130:133], v[220:223], v[18:21]
	v_mfma_f32_16x16x32_bf16 v[10:13], v[138:141], v[220:223], v[10:13]
	v_mfma_f32_16x16x32_bf16 v[62:65], v[134:137], v[200:203], v[62:65]
	v_mfma_f32_16x16x32_bf16 v[58:61], v[142:145], v[200:203], v[58:61]
	v_mfma_f32_16x16x32_bf16 v[50:53], v[134:137], v[208:211], v[50:53]
	v_mfma_f32_16x16x32_bf16 v[42:45], v[142:145], v[208:211], v[42:45]
	v_mfma_f32_16x16x32_bf16 v[34:37], v[134:137], v[216:219], v[34:37]
	v_mfma_f32_16x16x32_bf16 v[26:29], v[142:145], v[216:219], v[26:29]
	v_mfma_f32_16x16x32_bf16 v[18:21], v[134:137], v[224:227], v[18:21]
	v_mfma_f32_16x16x32_bf16 v[10:13], v[142:145], v[224:227], v[10:13]
	v_mfma_f32_16x16x32_bf16 v[54:57], v[180:183], v[196:199], v[54:57]
	v_mfma_f32_16x16x32_bf16 v[46:49], v[188:191], v[196:199], v[46:49]
	v_mfma_f32_16x16x32_bf16 v[38:41], v[180:183], v[204:207], v[38:41]
	v_mfma_f32_16x16x32_bf16 v[30:33], v[188:191], v[204:207], v[30:33]
	v_mfma_f32_16x16x32_bf16 v[22:25], v[180:183], v[212:215], v[22:25]
	v_mfma_f32_16x16x32_bf16 v[14:17], v[188:191], v[212:215], v[14:17]
	v_mfma_f32_16x16x32_bf16 v[6:9], v[180:183], v[220:223], v[6:9]
	v_mfma_f32_16x16x32_bf16 v[2:5], v[188:191], v[220:223], v[2:5]
	v_mfma_f32_16x16x32_bf16 v[54:57], v[184:187], v[200:203], v[54:57]
	v_mfma_f32_16x16x32_bf16 v[46:49], v[192:195], v[200:203], v[46:49]
	v_mfma_f32_16x16x32_bf16 v[38:41], v[184:187], v[208:211], v[38:41]
	v_mfma_f32_16x16x32_bf16 v[30:33], v[192:195], v[208:211], v[30:33]
	v_mfma_f32_16x16x32_bf16 v[22:25], v[184:187], v[216:219], v[22:25]
	v_mfma_f32_16x16x32_bf16 v[14:17], v[192:195], v[216:219], v[14:17]
	v_mfma_f32_16x16x32_bf16 v[6:9], v[184:187], v[224:227], v[6:9]
	v_mfma_f32_16x16x32_bf16 v[2:5], v[192:195], v[224:227], v[2:5]
	s_barrier
	ds_read_b128 v[130:133], v178
	ds_read_b128 v[134:137], v178 offset:1024
	ds_read_b128 v[138:141], v178 offset:2048
	ds_read_b128 v[142:145], v178 offset:3072
	ds_read_b128 v[180:183], v179
	ds_read_b128 v[184:187], v179 offset:1024
	ds_read_b128 v[188:191], v179 offset:2048
	ds_read_b128 v[192:195], v179 offset:3072
	s_add_u32 s24, s24, 0x100000
	s_addc_u32 s25, s25, 0
	s_mov_b32 m0, s28
	v_lshl_add_u64 v[236:237], s[24:25], 0, v[152:153]
	ds_read_b128 v[196:199], v177 offset:32768
	ds_read_b128 v[200:203], v177 offset:33792
	ds_read_b128 v[204:207], v177 offset:34816
	ds_read_b128 v[208:211], v177 offset:35840
	ds_read_b128 v[212:215], v177 offset:36864
	ds_read_b128 v[216:219], v177 offset:37888
	ds_read_b128 v[220:223], v177 offset:38912
	ds_read_b128 v[224:227], v177 offset:39936
	global_load_lds_dwordx4 v[236:237], off
	v_lshl_add_u64 v[236:237], s[24:25], 0, v[148:149]
	s_mov_b32 m0, s29
	s_nop 0
	global_load_lds_dwordx4 v[236:237], off
	s_waitcnt vmcnt(8) lgkmcnt(0)
	s_barrier
	v_mfma_f32_16x16x32_bf16 v[126:129], v[130:133], v[196:199], v[126:129]
	v_mfma_f32_16x16x32_bf16 v[122:125], v[138:141], v[196:199], v[122:125]
	v_mfma_f32_16x16x32_bf16 v[114:117], v[130:133], v[204:207], v[114:117]
	v_mfma_f32_16x16x32_bf16 v[106:109], v[138:141], v[204:207], v[106:109]
	v_mfma_f32_16x16x32_bf16 v[98:101], v[130:133], v[212:215], v[98:101]
	v_mfma_f32_16x16x32_bf16 v[90:93], v[138:141], v[212:215], v[90:93]
	v_mfma_f32_16x16x32_bf16 v[82:85], v[130:133], v[220:223], v[82:85]
	v_mfma_f32_16x16x32_bf16 v[74:77], v[138:141], v[220:223], v[74:77]
	v_mfma_f32_16x16x32_bf16 v[126:129], v[134:137], v[200:203], v[126:129]
	v_mfma_f32_16x16x32_bf16 v[122:125], v[142:145], v[200:203], v[122:125]
	v_mfma_f32_16x16x32_bf16 v[114:117], v[134:137], v[208:211], v[114:117]
	v_mfma_f32_16x16x32_bf16 v[106:109], v[142:145], v[208:211], v[106:109]
	v_mfma_f32_16x16x32_bf16 v[98:101], v[134:137], v[216:219], v[98:101]
	v_mfma_f32_16x16x32_bf16 v[90:93], v[142:145], v[216:219], v[90:93]
	v_mfma_f32_16x16x32_bf16 v[82:85], v[134:137], v[224:227], v[82:85]
	v_mfma_f32_16x16x32_bf16 v[74:77], v[142:145], v[224:227], v[74:77]
	v_mfma_f32_16x16x32_bf16 v[118:121], v[180:183], v[196:199], v[118:121]
	v_mfma_f32_16x16x32_bf16 v[110:113], v[188:191], v[196:199], v[110:113]
	v_mfma_f32_16x16x32_bf16 v[102:105], v[180:183], v[204:207], v[102:105]
	v_mfma_f32_16x16x32_bf16 v[94:97], v[188:191], v[204:207], v[94:97]
	v_mfma_f32_16x16x32_bf16 v[86:89], v[180:183], v[212:215], v[86:89]
	v_mfma_f32_16x16x32_bf16 v[78:81], v[188:191], v[212:215], v[78:81]
	v_mfma_f32_16x16x32_bf16 v[70:73], v[180:183], v[220:223], v[70:73]
	v_mfma_f32_16x16x32_bf16 v[66:69], v[188:191], v[220:223], v[66:69]
	v_mfma_f32_16x16x32_bf16 v[118:121], v[184:187], v[200:203], v[118:121]
	v_mfma_f32_16x16x32_bf16 v[110:113], v[192:195], v[200:203], v[110:113]
	v_mfma_f32_16x16x32_bf16 v[102:105], v[184:187], v[208:211], v[102:105]
	v_mfma_f32_16x16x32_bf16 v[94:97], v[192:195], v[208:211], v[94:97]
	v_mfma_f32_16x16x32_bf16 v[86:89], v[184:187], v[216:219], v[86:89]
	v_mfma_f32_16x16x32_bf16 v[78:81], v[192:195], v[216:219], v[78:81]
	v_mfma_f32_16x16x32_bf16 v[70:73], v[184:187], v[224:227], v[70:73]
	v_mfma_f32_16x16x32_bf16 v[66:69], v[192:195], v[224:227], v[66:69]
	s_barrier
	s_mov_b32 m0, s41
	v_lshl_add_u64 v[228:229], v[228:229], 0, s[14:15]
	s_add_u32 s20, s20, 0x100080
	ds_read_b128 v[196:199], v177 offset:49152
	ds_read_b128 v[200:203], v177 offset:50176
	ds_read_b128 v[204:207], v177 offset:51200
	ds_read_b128 v[208:211], v177 offset:52224
	ds_read_b128 v[212:215], v177 offset:53248
	ds_read_b128 v[216:219], v177 offset:54272
	ds_read_b128 v[220:223], v177 offset:55296
	ds_read_b128 v[224:227], v177 offset:56320
	global_load_lds_dwordx4 v[228:229], off
	v_lshl_add_u64 v[228:229], v[230:231], 0, s[14:15]
	s_mov_b32 m0, s42
	s_addc_u32 s21, s21, 0
	global_load_lds_dwordx4 v[228:229], off
	v_lshl_add_u64 v[228:229], s[20:21], 0, v[150:151]
	s_mov_b32 m0, s43
	s_nop 0
	global_load_lds_dwordx4 v[228:229], off
	v_lshl_add_u64 v[228:229], s[20:21], 0, v[146:147]
	s_mov_b32 m0, s48
	s_nop 0
	global_load_lds_dwordx4 v[228:229], off
	v_lshl_add_u64 v[228:229], v[232:233], 0, s[14:15]
	s_mov_b32 m0, s31
	s_nop 0
	global_load_lds_dwordx4 v[228:229], off
	v_lshl_add_u64 v[228:229], v[234:235], 0, s[14:15]
	s_mov_b32 m0, s34
	s_nop 0
	global_load_lds_dwordx4 v[228:229], off
	s_waitcnt vmcnt(8) lgkmcnt(0)
	s_barrier
	v_mfma_f32_16x16x32_bf16 v[62:65], v[130:133], v[196:199], v[62:65]
	v_mfma_f32_16x16x32_bf16 v[58:61], v[138:141], v[196:199], v[58:61]
	v_mfma_f32_16x16x32_bf16 v[50:53], v[130:133], v[204:207], v[50:53]
	v_mfma_f32_16x16x32_bf16 v[42:45], v[138:141], v[204:207], v[42:45]
	v_mfma_f32_16x16x32_bf16 v[34:37], v[130:133], v[212:215], v[34:37]
	v_mfma_f32_16x16x32_bf16 v[26:29], v[138:141], v[212:215], v[26:29]
	v_mfma_f32_16x16x32_bf16 v[18:21], v[130:133], v[220:223], v[18:21]
	v_mfma_f32_16x16x32_bf16 v[10:13], v[138:141], v[220:223], v[10:13]
	v_mfma_f32_16x16x32_bf16 v[62:65], v[134:137], v[200:203], v[62:65]
	v_mfma_f32_16x16x32_bf16 v[58:61], v[142:145], v[200:203], v[58:61]
	v_mfma_f32_16x16x32_bf16 v[50:53], v[134:137], v[208:211], v[50:53]
	v_mfma_f32_16x16x32_bf16 v[42:45], v[142:145], v[208:211], v[42:45]
	v_mfma_f32_16x16x32_bf16 v[34:37], v[134:137], v[216:219], v[34:37]
	v_mfma_f32_16x16x32_bf16 v[26:29], v[142:145], v[216:219], v[26:29]
	v_mfma_f32_16x16x32_bf16 v[18:21], v[134:137], v[224:227], v[18:21]
	v_mfma_f32_16x16x32_bf16 v[10:13], v[142:145], v[224:227], v[10:13]
	v_mfma_f32_16x16x32_bf16 v[54:57], v[180:183], v[196:199], v[54:57]
	v_mfma_f32_16x16x32_bf16 v[46:49], v[188:191], v[196:199], v[46:49]
	v_mfma_f32_16x16x32_bf16 v[38:41], v[180:183], v[204:207], v[38:41]
	v_mfma_f32_16x16x32_bf16 v[30:33], v[188:191], v[204:207], v[30:33]
	v_mfma_f32_16x16x32_bf16 v[22:25], v[180:183], v[212:215], v[22:25]
	v_mfma_f32_16x16x32_bf16 v[14:17], v[188:191], v[212:215], v[14:17]
	v_mfma_f32_16x16x32_bf16 v[6:9], v[180:183], v[220:223], v[6:9]
	v_mfma_f32_16x16x32_bf16 v[2:5], v[188:191], v[220:223], v[2:5]
	v_mfma_f32_16x16x32_bf16 v[54:57], v[184:187], v[200:203], v[54:57]
	v_mfma_f32_16x16x32_bf16 v[46:49], v[192:195], v[200:203], v[46:49]
	v_mfma_f32_16x16x32_bf16 v[38:41], v[184:187], v[208:211], v[38:41]
	v_mfma_f32_16x16x32_bf16 v[30:33], v[192:195], v[208:211], v[30:33]
	v_mfma_f32_16x16x32_bf16 v[22:25], v[184:187], v[216:219], v[22:25]
	v_mfma_f32_16x16x32_bf16 v[14:17], v[192:195], v[216:219], v[14:17]
	v_mfma_f32_16x16x32_bf16 v[6:9], v[184:187], v[224:227], v[6:9]
	v_mfma_f32_16x16x32_bf16 v[2:5], v[192:195], v[224:227], v[2:5]
	s_barrier
	s_add_i32 s0, s0, 2
	s_add_u32 s16, s16, 0x100
	s_addc_u32 s17, s17, 0
	s_cmp_gt_u32 s0, 61
	s_cbranch_scc0 .LBB0_768
	s_and_b64 vcc, exec, s[10:11]
	s_cbranch_vccz .LBB0_771
	s_barrier

.LBB0_788:
	v_add_u32_e32 v130, s15, v190
	v_add_u32_e32 v134, s50, v190
	ds_read_b128 v[158:161], v130
	ds_read_b128 v[150:153], v130 offset:1024
	ds_read_b128 v[154:157], v130 offset:2048
	ds_read_b128 v[146:149], v130 offset:3072
	ds_read_b128 v[142:145], v134
	ds_read_b128 v[130:133], v134 offset:1024
	ds_read_b128 v[138:141], v134 offset:2048
	ds_read_b128 v[134:137], v134 offset:3072
	s_add_u32 s36, s34, 0xfff80080
	s_addc_u32 s37, s35, -1
	s_and_b64 s[0:1], s[0:1], exec
	s_cselect_b32 s39, s21, s37
	s_cselect_b32 s38, s60, s36
	s_cselect_b32 s37, s17, s63
	s_cselect_b32 s36, s61, s62
	s_add_i32 m0, s29, 0xc000
	ds_read_b128 v[182:185], v193
	ds_read_b128 v[186:189], v193 offset:1024
	ds_read_b128 v[194:197], v193 offset:2048
	ds_read_b128 v[198:201], v193 offset:3072
	ds_read_b128 v[202:205], v193 offset:4096
	ds_read_b128 v[206:209], v193 offset:5120
	ds_read_b128 v[210:213], v193 offset:6144
	ds_read_b128 v[214:217], v193 offset:7168
	global_load_lds_dwordx4 v172, s[34:35]
	s_add_i32 m0, s29, 0xe000
	s_nop 0
	global_load_lds_dwordx4 v174, s[34:35]
	s_waitcnt vmcnt(8) lgkmcnt(0)
	s_barrier
	v_mfma_i32_16x16x64_i8 v[126:129], v[158:161], v[182:185], v[126:129]
	v_mfma_i32_16x16x64_i8 v[122:125], v[154:157], v[182:185], v[122:125]
	v_mfma_i32_16x16x64_i8 v[106:109], v[154:157], v[194:197], v[106:109]
	v_mfma_i32_16x16x64_i8 v[114:117], v[158:161], v[194:197], v[114:117]
	v_mfma_i32_16x16x64_i8 v[98:101], v[158:161], v[202:205], v[98:101]
	v_mfma_i32_16x16x64_i8 v[90:93], v[154:157], v[202:205], v[90:93]
	v_mfma_i32_16x16x64_i8 v[74:77], v[154:157], v[210:213], v[74:77]
	v_mfma_i32_16x16x64_i8 v[82:85], v[158:161], v[210:213], v[82:85]
	v_mfma_i32_16x16x64_i8 v[126:129], v[150:153], v[186:189], v[126:129]
	v_mfma_i32_16x16x64_i8 v[122:125], v[146:149], v[186:189], v[122:125]
	v_mfma_i32_16x16x64_i8 v[106:109], v[146:149], v[198:201], v[106:109]
	v_mfma_i32_16x16x64_i8 v[114:117], v[150:153], v[198:201], v[114:117]
	v_mfma_i32_16x16x64_i8 v[98:101], v[150:153], v[206:209], v[98:101]
	v_mfma_i32_16x16x64_i8 v[90:93], v[146:149], v[206:209], v[90:93]
	v_mfma_i32_16x16x64_i8 v[74:77], v[146:149], v[214:217], v[74:77]
	v_mfma_i32_16x16x64_i8 v[82:85], v[150:153], v[214:217], v[82:85]
	v_mfma_i32_16x16x64_i8 v[118:121], v[142:145], v[182:185], v[118:121]
	v_mfma_i32_16x16x64_i8 v[110:113], v[138:141], v[182:185], v[110:113]
	v_mfma_i32_16x16x64_i8 v[94:97], v[138:141], v[194:197], v[94:97]
	v_mfma_i32_16x16x64_i8 v[102:105], v[142:145], v[194:197], v[102:105]
	v_mfma_i32_16x16x64_i8 v[86:89], v[142:145], v[202:205], v[86:89]
	v_mfma_i32_16x16x64_i8 v[78:81], v[138:141], v[202:205], v[78:81]
	v_mfma_i32_16x16x64_i8 v[66:69], v[138:141], v[210:213], v[66:69]
	v_mfma_i32_16x16x64_i8 v[70:73], v[142:145], v[210:213], v[70:73]
	v_mfma_i32_16x16x64_i8 v[118:121], v[130:133], v[186:189], v[118:121]
	v_mfma_i32_16x16x64_i8 v[110:113], v[134:137], v[186:189], v[110:113]
	v_mfma_i32_16x16x64_i8 v[94:97], v[134:137], v[198:201], v[94:97]
	v_mfma_i32_16x16x64_i8 v[102:105], v[130:133], v[198:201], v[102:105]
	v_mfma_i32_16x16x64_i8 v[86:89], v[130:133], v[206:209], v[86:89]
	v_mfma_i32_16x16x64_i8 v[78:81], v[134:137], v[206:209], v[78:81]
	v_mfma_i32_16x16x64_i8 v[66:69], v[134:137], v[214:217], v[66:69]
	v_mfma_i32_16x16x64_i8 v[70:73], v[130:133], v[214:217], v[70:73]
	s_barrier
	s_add_i32 s0, s15, s40
	s_mov_b32 m0, s0
	ds_read_b128 v[194:197], v193 offset:16384
	ds_read_b128 v[198:201], v193 offset:17408
	ds_read_b128 v[202:205], v193 offset:18432
	ds_read_b128 v[206:209], v193 offset:19456
	ds_read_b128 v[210:213], v193 offset:20480
	ds_read_b128 v[214:217], v193 offset:21504
	ds_read_b128 v[218:221], v193 offset:22528
	ds_read_b128 v[222:225], v193 offset:23552
	global_load_lds_dwordx4 v164, s[36:37]
	s_add_i32 m0, s0, 0x2000
	s_add_u32 s0, s36, 0x80000
	s_addc_u32 s1, s37, 0
	s_add_i32 s66, s50, s40
	global_load_lds_dwordx4 v168, s[36:37]
	s_mov_b32 m0, s66
	s_nop 0
	global_load_lds_dwordx4 v164, s[0:1]
	s_add_i32 m0, s66, 0x2000
	s_nop 0
	global_load_lds_dwordx4 v168, s[0:1]
	s_mov_b32 m0, s29
	s_nop 0
	global_load_lds_dwordx4 v162, s[38:39]
	s_mov_b32 m0, s31
	s_nop 0
	global_load_lds_dwordx4 v166, s[38:39]
	s_waitcnt vmcnt(8) lgkmcnt(0)
	s_barrier
	v_mfma_i32_16x16x64_i8 v[62:65], v[158:161], v[194:197], v[62:65]
	v_mfma_i32_16x16x64_i8 v[58:61], v[154:157], v[194:197], v[58:61]
	v_mfma_i32_16x16x64_i8 v[42:45], v[154:157], v[202:205], v[42:45]
	v_mfma_i32_16x16x64_i8 v[50:53], v[158:161], v[202:205], v[50:53]
	v_mfma_i32_16x16x64_i8 v[34:37], v[158:161], v[210:213], v[34:37]
	v_mfma_i32_16x16x64_i8 v[26:29], v[154:157], v[210:213], v[26:29]
	v_mfma_i32_16x16x64_i8 v[10:13], v[154:157], v[218:221], v[10:13]
	v_mfma_i32_16x16x64_i8 v[18:21], v[158:161], v[218:221], v[18:21]
	v_mfma_i32_16x16x64_i8 v[62:65], v[150:153], v[198:201], v[62:65]
	v_mfma_i32_16x16x64_i8 v[58:61], v[146:149], v[198:201], v[58:61]
	v_mfma_i32_16x16x64_i8 v[42:45], v[146:149], v[206:209], v[42:45]
	v_mfma_i32_16x16x64_i8 v[50:53], v[150:153], v[206:209], v[50:53]
	v_mfma_i32_16x16x64_i8 v[34:37], v[150:153], v[214:217], v[34:37]
	v_mfma_i32_16x16x64_i8 v[26:29], v[146:149], v[214:217], v[26:29]
	v_mfma_i32_16x16x64_i8 v[10:13], v[146:149], v[222:225], v[10:13]
	v_mfma_i32_16x16x64_i8 v[18:21], v[150:153], v[222:225], v[18:21]
	v_mfma_i32_16x16x64_i8 v[54:57], v[142:145], v[194:197], v[54:57]
	v_mfma_i32_16x16x64_i8 v[46:49], v[138:141], v[194:197], v[46:49]
	v_mfma_i32_16x16x64_i8 v[30:33], v[138:141], v[202:205], v[30:33]
	v_mfma_i32_16x16x64_i8 v[38:41], v[142:145], v[202:205], v[38:41]
	v_mfma_i32_16x16x64_i8 v[22:25], v[142:145], v[210:213], v[22:25]
	v_mfma_i32_16x16x64_i8 v[14:17], v[138:141], v[210:213], v[14:17]
	v_mfma_i32_16x16x64_i8 v[2:5], v[138:141], v[218:221], v[2:5]
	v_mfma_i32_16x16x64_i8 v[6:9], v[142:145], v[218:221], v[6:9]
	v_mfma_i32_16x16x64_i8 v[54:57], v[130:133], v[198:201], v[54:57]
	v_mfma_i32_16x16x64_i8 v[46:49], v[134:137], v[198:201], v[46:49]
	v_mfma_i32_16x16x64_i8 v[30:33], v[134:137], v[206:209], v[30:33]
	v_mfma_i32_16x16x64_i8 v[38:41], v[130:133], v[206:209], v[38:41]
	v_mfma_i32_16x16x64_i8 v[22:25], v[130:133], v[214:217], v[22:25]
	v_mfma_i32_16x16x64_i8 v[14:17], v[134:137], v[214:217], v[14:17]
	v_mfma_i32_16x16x64_i8 v[2:5], v[134:137], v[222:225], v[2:5]
	v_mfma_i32_16x16x64_i8 v[6:9], v[130:133], v[222:225], v[6:9]
	s_barrier
	s_add_i32 s66, 0, 0x18000
	s_add_i32 s67, 0, 0x1c000
	v_add_u32_e32 v142, s66, v190
	v_add_u32_e32 v158, s67, v190
	ds_read_b128 v[130:133], v142
	ds_read_b128 v[134:137], v142 offset:1024
	ds_read_b128 v[138:141], v142 offset:2048
	ds_read_b128 v[142:145], v142 offset:3072
	ds_read_b128 v[146:149], v158
	ds_read_b128 v[150:153], v158 offset:1024
	ds_read_b128 v[154:157], v158 offset:2048
	ds_read_b128 v[158:161], v158 offset:3072
	s_add_u32 s0, s38, 0x80000
	s_addc_u32 s1, s39, 0
	s_mov_b32 m0, s42
	ds_read_b128 v[194:197], v193 offset:32768
	ds_read_b128 v[198:201], v193 offset:33792
	ds_read_b128 v[202:205], v193 offset:34816
	ds_read_b128 v[206:209], v193 offset:35840
	ds_read_b128 v[210:213], v193 offset:36864
	ds_read_b128 v[214:217], v193 offset:37888
	ds_read_b128 v[218:221], v193 offset:38912
	ds_read_b128 v[222:225], v193 offset:39936
	global_load_lds_dwordx4 v162, s[0:1]
	s_mov_b32 m0, s43
	s_nop 0
	global_load_lds_dwordx4 v166, s[0:1]
	s_waitcnt vmcnt(8) lgkmcnt(0)
	s_barrier
	v_mfma_i32_16x16x64_i8 v[126:129], v[130:133], v[194:197], v[126:129]
	v_mfma_i32_16x16x64_i8 v[122:125], v[138:141], v[194:197], v[122:125]
	v_mfma_i32_16x16x64_i8 v[106:109], v[138:141], v[202:205], v[106:109]
	v_mfma_i32_16x16x64_i8 v[114:117], v[130:133], v[202:205], v[114:117]
	v_mfma_i32_16x16x64_i8 v[98:101], v[130:133], v[210:213], v[98:101]
	v_mfma_i32_16x16x64_i8 v[90:93], v[138:141], v[210:213], v[90:93]
	v_mfma_i32_16x16x64_i8 v[74:77], v[138:141], v[218:221], v[74:77]
	v_mfma_i32_16x16x64_i8 v[82:85], v[130:133], v[218:221], v[82:85]
	v_mfma_i32_16x16x64_i8 v[126:129], v[134:137], v[198:201], v[126:129]
	v_mfma_i32_16x16x64_i8 v[122:125], v[142:145], v[198:201], v[122:125]
	v_mfma_i32_16x16x64_i8 v[106:109], v[142:145], v[206:209], v[106:109]
	v_mfma_i32_16x16x64_i8 v[114:117], v[134:137], v[206:209], v[114:117]
	v_mfma_i32_16x16x64_i8 v[98:101], v[134:137], v[214:217], v[98:101]
	v_mfma_i32_16x16x64_i8 v[90:93], v[142:145], v[214:217], v[90:93]
	v_mfma_i32_16x16x64_i8 v[74:77], v[142:145], v[222:225], v[74:77]
	v_mfma_i32_16x16x64_i8 v[82:85], v[134:137], v[222:225], v[82:85]
	v_mfma_i32_16x16x64_i8 v[118:121], v[146:149], v[194:197], v[118:121]
	v_mfma_i32_16x16x64_i8 v[110:113], v[154:157], v[194:197], v[110:113]
	v_mfma_i32_16x16x64_i8 v[94:97], v[154:157], v[202:205], v[94:97]
	v_mfma_i32_16x16x64_i8 v[102:105], v[146:149], v[202:205], v[102:105]
	v_mfma_i32_16x16x64_i8 v[86:89], v[146:149], v[210:213], v[86:89]
	v_mfma_i32_16x16x64_i8 v[78:81], v[154:157], v[210:213], v[78:81]
	v_mfma_i32_16x16x64_i8 v[66:69], v[154:157], v[218:221], v[66:69]
	v_mfma_i32_16x16x64_i8 v[70:73], v[146:149], v[218:221], v[70:73]
	v_mfma_i32_16x16x64_i8 v[118:121], v[150:153], v[198:201], v[118:121]
	v_mfma_i32_16x16x64_i8 v[110:113], v[158:161], v[198:201], v[110:113]
	v_mfma_i32_16x16x64_i8 v[94:97], v[158:161], v[206:209], v[94:97]
	v_mfma_i32_16x16x64_i8 v[102:105], v[150:153], v[206:209], v[102:105]
	v_mfma_i32_16x16x64_i8 v[86:89], v[150:153], v[214:217], v[86:89]
	v_mfma_i32_16x16x64_i8 v[78:81], v[158:161], v[214:217], v[78:81]
	v_mfma_i32_16x16x64_i8 v[66:69], v[158:161], v[222:225], v[66:69]
	v_mfma_i32_16x16x64_i8 v[70:73], v[150:153], v[222:225], v[70:73]
	s_barrier
	s_add_i32 s0, s66, s40
	s_mov_b32 m0, s0
	s_add_u32 s98, s36, 0x80
	s_addc_u32 s99, s37, 0
	s_add_u32 s100, s38, 0x80
	s_addc_u32 s101, s39, 0
	ds_read_b128 v[194:197], v193 offset:49152
	ds_read_b128 v[198:201], v193 offset:50176
	ds_read_b128 v[202:205], v193 offset:51200
	ds_read_b128 v[206:209], v193 offset:52224
	ds_read_b128 v[210:213], v193 offset:53248
	ds_read_b128 v[214:217], v193 offset:54272
	ds_read_b128 v[218:221], v193 offset:55296
	ds_read_b128 v[222:225], v193 offset:56320
	global_load_lds_dwordx4 v164, s[98:99]
	s_add_i32 m0, s0, 0x2000
	s_add_u32 s0, s36, 0x80080
	s_addc_u32 s1, s37, 0
	s_add_i32 s36, s67, s40
	global_load_lds_dwordx4 v168, s[98:99]
	s_mov_b32 m0, s36
	s_nop 0
	global_load_lds_dwordx4 v164, s[0:1]
	s_add_i32 m0, s36, 0x2000
	s_nop 0
	global_load_lds_dwordx4 v168, s[0:1]
	s_mov_b32 m0, s48
	s_nop 0
	global_load_lds_dwordx4 v162, s[100:101]
	s_mov_b32 m0, s49
	s_nop 0
	global_load_lds_dwordx4 v166, s[100:101]
	s_waitcnt vmcnt(8) lgkmcnt(0)
	s_barrier
	v_mfma_i32_16x16x64_i8 v[62:65], v[130:133], v[194:197], v[62:65]
	v_mfma_i32_16x16x64_i8 v[58:61], v[138:141], v[194:197], v[58:61]
	v_mfma_i32_16x16x64_i8 v[42:45], v[138:141], v[202:205], v[42:45]
	v_mfma_i32_16x16x64_i8 v[50:53], v[130:133], v[202:205], v[50:53]
	v_mfma_i32_16x16x64_i8 v[34:37], v[130:133], v[210:213], v[34:37]
	v_mfma_i32_16x16x64_i8 v[26:29], v[138:141], v[210:213], v[26:29]
	v_mfma_i32_16x16x64_i8 v[10:13], v[138:141], v[218:221], v[10:13]
	v_mfma_i32_16x16x64_i8 v[18:21], v[130:133], v[218:221], v[18:21]
	v_mfma_i32_16x16x64_i8 v[62:65], v[134:137], v[198:201], v[62:65]
	v_mfma_i32_16x16x64_i8 v[58:61], v[142:145], v[198:201], v[58:61]
	v_mfma_i32_16x16x64_i8 v[42:45], v[142:145], v[206:209], v[42:45]
	v_mfma_i32_16x16x64_i8 v[50:53], v[134:137], v[206:209], v[50:53]
	v_mfma_i32_16x16x64_i8 v[34:37], v[134:137], v[214:217], v[34:37]
	v_mfma_i32_16x16x64_i8 v[26:29], v[142:145], v[214:217], v[26:29]
	v_mfma_i32_16x16x64_i8 v[10:13], v[142:145], v[222:225], v[10:13]
	v_mfma_i32_16x16x64_i8 v[18:21], v[134:137], v[222:225], v[18:21]
	v_mfma_i32_16x16x64_i8 v[54:57], v[146:149], v[194:197], v[54:57]
	v_mfma_i32_16x16x64_i8 v[46:49], v[154:157], v[194:197], v[46:49]
	v_mfma_i32_16x16x64_i8 v[30:33], v[154:157], v[202:205], v[30:33]
	v_mfma_i32_16x16x64_i8 v[38:41], v[146:149], v[202:205], v[38:41]
	v_mfma_i32_16x16x64_i8 v[22:25], v[146:149], v[210:213], v[22:25]
	v_mfma_i32_16x16x64_i8 v[14:17], v[154:157], v[210:213], v[14:17]
	v_mfma_i32_16x16x64_i8 v[2:5], v[154:157], v[218:221], v[2:5]
	v_mfma_i32_16x16x64_i8 v[6:9], v[146:149], v[218:221], v[6:9]
	v_mfma_i32_16x16x64_i8 v[54:57], v[150:153], v[198:201], v[54:57]
	v_mfma_i32_16x16x64_i8 v[46:49], v[158:161], v[198:201], v[46:49]
	v_mfma_i32_16x16x64_i8 v[30:33], v[158:161], v[206:209], v[30:33]
	v_mfma_i32_16x16x64_i8 v[38:41], v[150:153], v[206:209], v[38:41]
	v_mfma_i32_16x16x64_i8 v[22:25], v[150:153], v[214:217], v[22:25]
	v_mfma_i32_16x16x64_i8 v[14:17], v[158:161], v[214:217], v[14:17]
	v_mfma_i32_16x16x64_i8 v[2:5], v[158:161], v[222:225], v[2:5]
	v_mfma_i32_16x16x64_i8 v[6:9], v[150:153], v[222:225], v[6:9]
	s_barrier
	s_add_i32 s64, s64, 2
	s_add_u32 s34, s34, 0x100
	s_addc_u32 s35, s35, 0
	s_add_u32 s62, s62, 0x100
	s_addc_u32 s63, s63, 0
	s_cmp_gt_u32 s64, 29
	s_cbranch_scc1 .LBB0_791

.LBB0_1051:
	s_add_u32 s8, s17, s6
	s_addc_u32 s9, s48, s7
	s_add_u32 s8, s8, 0x32800100
	s_addc_u32 s9, s9, 0
	s_add_u32 s65, s49, s6
	s_addc_u32 s68, s50, s7
	s_add_i32 s69, 0, 0x10000
	s_cmpk_eq_i32 s6, 0xf00
	s_cselect_b32 s41, s5, s9
	s_cselect_b32 s40, s4, s8
	s_cselect_b32 s9, s21, s68
	s_cselect_b32 s8, s20, s65
	s_add_i32 s65, 0, 0x14000
	v_add_u32_e32 v130, s69, v187
	v_add_u32_e32 v134, s65, v187
	ds_read_b128 v[158:161], v130
	ds_read_b128 v[150:153], v130 offset:1024
	ds_read_b128 v[154:157], v130 offset:2048
	ds_read_b128 v[146:149], v130 offset:3072
	ds_read_b128 v[142:145], v134
	ds_read_b128 v[130:133], v134 offset:1024
	ds_read_b128 v[138:141], v134 offset:2048
	ds_read_b128 v[134:137], v134 offset:3072
	v_lshl_add_u64 v[214:215], v[168:169], 0, s[6:7]
	s_add_i32 m0, s43, 0xc000
	ds_read_b128 v[172:175], v188
	ds_read_b128 v[176:179], v188 offset:1024
	ds_read_b128 v[190:193], v188 offset:2048
	ds_read_b128 v[194:197], v188 offset:3072
	ds_read_b128 v[198:201], v188 offset:4096
	ds_read_b128 v[202:205], v188 offset:5120
	ds_read_b128 v[206:209], v188 offset:6144
	ds_read_b128 v[210:213], v188 offset:7168
	global_load_lds_dwordx4 v[214:215], off
	v_lshl_add_u64 v[214:215], v[170:171], 0, s[6:7]
	s_add_i32 m0, s43, 0xe000
	s_nop 0
	global_load_lds_dwordx4 v[214:215], off
	s_waitcnt vmcnt(8) lgkmcnt(0)
	s_barrier
	v_mfma_i32_16x16x64_i8 v[70:73], v[158:161], v[172:175], v[70:73]
	v_mfma_i32_16x16x64_i8 v[34:37], v[154:157], v[172:175], v[34:37]
	v_mfma_i32_16x16x64_i8 v[54:57], v[154:157], v[190:193], v[54:57]
	v_mfma_i32_16x16x64_i8 v[102:105], v[158:161], v[190:193], v[102:105]
	v_mfma_i32_16x16x64_i8 v[114:117], v[158:161], v[198:201], v[114:117]
	v_mfma_i32_16x16x64_i8 v[86:89], v[154:157], v[198:201], v[86:89]
	v_mfma_i32_16x16x64_i8 v[110:113], v[154:157], v[206:209], v[110:113]
	v_mfma_i32_16x16x64_i8 v[126:129], v[158:161], v[206:209], v[126:129]
	v_mfma_i32_16x16x64_i8 v[70:73], v[150:153], v[176:179], v[70:73]
	v_mfma_i32_16x16x64_i8 v[34:37], v[146:149], v[176:179], v[34:37]
	v_mfma_i32_16x16x64_i8 v[54:57], v[146:149], v[194:197], v[54:57]
	v_mfma_i32_16x16x64_i8 v[102:105], v[150:153], v[194:197], v[102:105]
	v_mfma_i32_16x16x64_i8 v[114:117], v[150:153], v[202:205], v[114:117]
	v_mfma_i32_16x16x64_i8 v[86:89], v[146:149], v[202:205], v[86:89]
	v_mfma_i32_16x16x64_i8 v[110:113], v[146:149], v[210:213], v[110:113]
	v_mfma_i32_16x16x64_i8 v[126:129], v[150:153], v[210:213], v[126:129]
	v_mfma_i32_16x16x64_i8 v[18:21], v[142:145], v[172:175], v[18:21]
	v_mfma_i32_16x16x64_i8 v[2:5], v[138:141], v[172:175], v[2:5]
	v_mfma_i32_16x16x64_i8 v[6:9], v[138:141], v[190:193], v[6:9]
	v_mfma_i32_16x16x64_i8 v[38:41], v[142:145], v[190:193], v[38:41]
	v_mfma_i32_16x16x64_i8 v[66:69], v[142:145], v[198:201], v[66:69]
	v_mfma_i32_16x16x64_i8 v[26:29], v[138:141], v[198:201], v[26:29]
	v_mfma_i32_16x16x64_i8 v[50:53], v[138:141], v[206:209], v[50:53]
	v_mfma_i32_16x16x64_i8 v[90:93], v[142:145], v[206:209], v[90:93]
	v_mfma_i32_16x16x64_i8 v[18:21], v[130:133], v[176:179], v[18:21]
	v_mfma_i32_16x16x64_i8 v[2:5], v[134:137], v[176:179], v[2:5]
	v_mfma_i32_16x16x64_i8 v[6:9], v[134:137], v[194:197], v[6:9]
	v_mfma_i32_16x16x64_i8 v[38:41], v[130:133], v[194:197], v[38:41]
	v_mfma_i32_16x16x64_i8 v[66:69], v[130:133], v[202:205], v[66:69]
	v_mfma_i32_16x16x64_i8 v[26:29], v[134:137], v[202:205], v[26:29]
	v_mfma_i32_16x16x64_i8 v[50:53], v[134:137], v[210:213], v[50:53]
	v_mfma_i32_16x16x64_i8 v[90:93], v[130:133], v[210:213], v[90:93]
	s_barrier
	s_add_i32 s68, s69, s42
	s_mov_b32 m0, s68
	ds_read_b128 v[190:193], v188 offset:16384
	ds_read_b128 v[194:197], v188 offset:17408
	ds_read_b128 v[198:201], v188 offset:18432
	ds_read_b128 v[202:205], v188 offset:19456
	ds_read_b128 v[206:209], v188 offset:20480
	ds_read_b128 v[210:213], v188 offset:21504
	ds_read_b128 v[214:217], v188 offset:22528
	ds_read_b128 v[218:221], v188 offset:23552
	global_load_lds_dwordx4 v162, s[8:9]
	s_add_i32 m0, s68, 0x2000
	s_add_u32 s68, s8, 0x80000
	s_addc_u32 s69, s9, 0
	s_add_i32 s65, s65, s42
	global_load_lds_dwordx4 v166, s[8:9]
	s_mov_b32 m0, s65
	s_nop 0
	global_load_lds_dwordx4 v162, s[68:69]
	s_add_i32 m0, s65, 0x2000
	s_nop 0
	global_load_lds_dwordx4 v166, s[68:69]
	s_mov_b32 m0, s43
	s_nop 0
	global_load_lds_dwordx4 v162, s[40:41]
	s_mov_b32 m0, s60
	s_nop 0
	global_load_lds_dwordx4 v166, s[40:41]
	s_waitcnt vmcnt(8) lgkmcnt(0)
	s_barrier
	v_mfma_i32_16x16x64_i8 v[122:125], v[158:161], v[190:193], v[122:125]
	v_mfma_i32_16x16x64_i8 v[118:121], v[154:157], v[190:193], v[118:121]
	v_mfma_i32_16x16x64_i8 v[94:97], v[154:157], v[198:201], v[94:97]
	v_mfma_i32_16x16x64_i8 v[98:101], v[158:161], v[198:201], v[98:101]
	v_mfma_i32_16x16x64_i8 v[62:65], v[158:161], v[206:209], v[62:65]
	v_mfma_i32_16x16x64_i8 v[58:61], v[154:157], v[206:209], v[58:61]
	v_mfma_i32_16x16x64_i8 v[22:25], v[154:157], v[214:217], v[22:25]
	v_mfma_i32_16x16x64_i8 v[30:33], v[158:161], v[214:217], v[30:33]
	v_mfma_i32_16x16x64_i8 v[122:125], v[150:153], v[194:197], v[122:125]
	v_mfma_i32_16x16x64_i8 v[118:121], v[146:149], v[194:197], v[118:121]
	v_mfma_i32_16x16x64_i8 v[94:97], v[146:149], v[202:205], v[94:97]
	v_mfma_i32_16x16x64_i8 v[98:101], v[150:153], v[202:205], v[98:101]
	v_mfma_i32_16x16x64_i8 v[62:65], v[150:153], v[210:213], v[62:65]
	v_mfma_i32_16x16x64_i8 v[58:61], v[146:149], v[210:213], v[58:61]
	v_mfma_i32_16x16x64_i8 v[22:25], v[146:149], v[218:221], v[22:25]
	v_mfma_i32_16x16x64_i8 v[30:33], v[150:153], v[218:221], v[30:33]
	v_mfma_i32_16x16x64_i8 v[106:109], v[142:145], v[190:193], v[106:109]
	v_mfma_i32_16x16x64_i8 v[82:85], v[138:141], v[190:193], v[82:85]
	v_mfma_i32_16x16x64_i8 v[74:77], v[138:141], v[198:201], v[74:77]
	v_mfma_i32_16x16x64_i8 v[78:81], v[142:145], v[198:201], v[78:81]
	v_mfma_i32_16x16x64_i8 v[46:49], v[142:145], v[206:209], v[46:49]
	v_mfma_i32_16x16x64_i8 v[42:45], v[138:141], v[206:209], v[42:45]
	v_mfma_i32_16x16x64_i8 v[10:13], v[138:141], v[214:217], v[10:13]
	v_mfma_i32_16x16x64_i8 v[14:17], v[142:145], v[214:217], v[14:17]
	v_mfma_i32_16x16x64_i8 v[106:109], v[130:133], v[194:197], v[106:109]
	v_mfma_i32_16x16x64_i8 v[82:85], v[134:137], v[194:197], v[82:85]
	v_mfma_i32_16x16x64_i8 v[74:77], v[134:137], v[202:205], v[74:77]
	v_mfma_i32_16x16x64_i8 v[78:81], v[130:133], v[202:205], v[78:81]
	v_mfma_i32_16x16x64_i8 v[46:49], v[130:133], v[210:213], v[46:49]
	v_mfma_i32_16x16x64_i8 v[42:45], v[134:137], v[210:213], v[42:45]
	v_mfma_i32_16x16x64_i8 v[10:13], v[134:137], v[218:221], v[10:13]
	v_mfma_i32_16x16x64_i8 v[14:17], v[130:133], v[218:221], v[14:17]
	s_barrier
	s_add_i32 s65, 0, 0x18000
	s_add_i32 s68, 0, 0x1c000
	v_add_u32_e32 v142, s65, v187
	v_add_u32_e32 v158, s68, v187
	ds_read_b128 v[130:133], v142
	ds_read_b128 v[134:137], v142 offset:1024
	ds_read_b128 v[138:141], v142 offset:2048
	ds_read_b128 v[142:145], v142 offset:3072
	ds_read_b128 v[146:149], v158
	ds_read_b128 v[150:153], v158 offset:1024
	ds_read_b128 v[154:157], v158 offset:2048
	ds_read_b128 v[158:161], v158 offset:3072
	s_add_u32 s40, s40, 0x80000
	s_addc_u32 s41, s41, 0
	s_add_u32 s100, s40, 0xfff80080
	s_addc_u32 s101, s41, -1
	s_mov_b32 m0, s61
	ds_read_b128 v[190:193], v188 offset:32768
	ds_read_b128 v[194:197], v188 offset:33792
	ds_read_b128 v[198:201], v188 offset:34816
	ds_read_b128 v[202:205], v188 offset:35840
	ds_read_b128 v[206:209], v188 offset:36864
	ds_read_b128 v[210:213], v188 offset:37888
	ds_read_b128 v[214:217], v188 offset:38912
	ds_read_b128 v[218:221], v188 offset:39936
	global_load_lds_dwordx4 v162, s[40:41]
	s_mov_b32 m0, s62
	s_nop 0
	global_load_lds_dwordx4 v166, s[40:41]
	s_waitcnt vmcnt(8) lgkmcnt(0)
	s_barrier
	v_mfma_i32_16x16x64_i8 v[70:73], v[130:133], v[190:193], v[70:73]
	v_mfma_i32_16x16x64_i8 v[34:37], v[138:141], v[190:193], v[34:37]
	v_mfma_i32_16x16x64_i8 v[54:57], v[138:141], v[198:201], v[54:57]
	v_mfma_i32_16x16x64_i8 v[102:105], v[130:133], v[198:201], v[102:105]
	v_mfma_i32_16x16x64_i8 v[114:117], v[130:133], v[206:209], v[114:117]
	v_mfma_i32_16x16x64_i8 v[86:89], v[138:141], v[206:209], v[86:89]
	v_mfma_i32_16x16x64_i8 v[110:113], v[138:141], v[214:217], v[110:113]
	v_mfma_i32_16x16x64_i8 v[126:129], v[130:133], v[214:217], v[126:129]
	v_mfma_i32_16x16x64_i8 v[70:73], v[134:137], v[194:197], v[70:73]
	v_mfma_i32_16x16x64_i8 v[34:37], v[142:145], v[194:197], v[34:37]
	v_mfma_i32_16x16x64_i8 v[54:57], v[142:145], v[202:205], v[54:57]
	v_mfma_i32_16x16x64_i8 v[102:105], v[134:137], v[202:205], v[102:105]
	v_mfma_i32_16x16x64_i8 v[114:117], v[134:137], v[210:213], v[114:117]
	v_mfma_i32_16x16x64_i8 v[86:89], v[142:145], v[210:213], v[86:89]
	v_mfma_i32_16x16x64_i8 v[110:113], v[142:145], v[218:221], v[110:113]
	v_mfma_i32_16x16x64_i8 v[126:129], v[134:137], v[218:221], v[126:129]
	v_mfma_i32_16x16x64_i8 v[18:21], v[146:149], v[190:193], v[18:21]
	v_mfma_i32_16x16x64_i8 v[2:5], v[154:157], v[190:193], v[2:5]
	v_mfma_i32_16x16x64_i8 v[6:9], v[154:157], v[198:201], v[6:9]
	v_mfma_i32_16x16x64_i8 v[38:41], v[146:149], v[198:201], v[38:41]
	v_mfma_i32_16x16x64_i8 v[66:69], v[146:149], v[206:209], v[66:69]
	v_mfma_i32_16x16x64_i8 v[26:29], v[154:157], v[206:209], v[26:29]
	v_mfma_i32_16x16x64_i8 v[50:53], v[154:157], v[214:217], v[50:53]
	v_mfma_i32_16x16x64_i8 v[90:93], v[146:149], v[214:217], v[90:93]
	v_mfma_i32_16x16x64_i8 v[18:21], v[150:153], v[194:197], v[18:21]
	v_mfma_i32_16x16x64_i8 v[2:5], v[158:161], v[194:197], v[2:5]
	v_mfma_i32_16x16x64_i8 v[6:9], v[158:161], v[202:205], v[6:9]
	v_mfma_i32_16x16x64_i8 v[38:41], v[150:153], v[202:205], v[38:41]
	v_mfma_i32_16x16x64_i8 v[66:69], v[150:153], v[210:213], v[66:69]
	v_mfma_i32_16x16x64_i8 v[26:29], v[158:161], v[210:213], v[26:29]
	v_mfma_i32_16x16x64_i8 v[50:53], v[158:161], v[218:221], v[50:53]
	v_mfma_i32_16x16x64_i8 v[90:93], v[150:153], v[218:221], v[90:93]
	s_barrier
	s_add_i32 s40, s65, s42
	s_mov_b32 m0, s40
	s_add_u32 s98, s8, 0x80
	s_addc_u32 s99, s9, 0
	ds_read_b128 v[190:193], v188 offset:49152
	ds_read_b128 v[194:197], v188 offset:50176
	ds_read_b128 v[198:201], v188 offset:51200
	ds_read_b128 v[202:205], v188 offset:52224
	ds_read_b128 v[206:209], v188 offset:53248
	ds_read_b128 v[210:213], v188 offset:54272
	ds_read_b128 v[214:217], v188 offset:55296
	ds_read_b128 v[218:221], v188 offset:56320
	global_load_lds_dwordx4 v162, s[98:99]
	s_add_i32 m0, s40, 0x2000
	s_add_u32 s8, s8, 0x80080
	s_addc_u32 s9, s9, 0
	s_add_i32 s40, s68, s42
	global_load_lds_dwordx4 v166, s[98:99]
	s_mov_b32 m0, s40
	s_nop 0
	global_load_lds_dwordx4 v162, s[8:9]
	s_add_i32 m0, s40, 0x2000
	s_nop 0
	global_load_lds_dwordx4 v166, s[8:9]
	s_mov_b32 m0, s66
	s_nop 0
	global_load_lds_dwordx4 v162, s[100:101]
	s_mov_b32 m0, s67
	s_nop 0
	global_load_lds_dwordx4 v166, s[100:101]
	s_waitcnt vmcnt(8) lgkmcnt(0)
	s_barrier
	v_mfma_i32_16x16x64_i8 v[122:125], v[130:133], v[190:193], v[122:125]
	v_mfma_i32_16x16x64_i8 v[118:121], v[138:141], v[190:193], v[118:121]
	v_mfma_i32_16x16x64_i8 v[94:97], v[138:141], v[198:201], v[94:97]
	v_mfma_i32_16x16x64_i8 v[98:101], v[130:133], v[198:201], v[98:101]
	v_mfma_i32_16x16x64_i8 v[62:65], v[130:133], v[206:209], v[62:65]
	v_mfma_i32_16x16x64_i8 v[58:61], v[138:141], v[206:209], v[58:61]
	v_mfma_i32_16x16x64_i8 v[22:25], v[138:141], v[214:217], v[22:25]
	v_mfma_i32_16x16x64_i8 v[30:33], v[130:133], v[214:217], v[30:33]
	v_mfma_i32_16x16x64_i8 v[122:125], v[134:137], v[194:197], v[122:125]
	v_mfma_i32_16x16x64_i8 v[118:121], v[142:145], v[194:197], v[118:121]
	v_mfma_i32_16x16x64_i8 v[94:97], v[142:145], v[202:205], v[94:97]
	v_mfma_i32_16x16x64_i8 v[98:101], v[134:137], v[202:205], v[98:101]
	v_mfma_i32_16x16x64_i8 v[62:65], v[134:137], v[210:213], v[62:65]
	v_mfma_i32_16x16x64_i8 v[58:61], v[142:145], v[210:213], v[58:61]
	v_mfma_i32_16x16x64_i8 v[22:25], v[142:145], v[218:221], v[22:25]
	v_mfma_i32_16x16x64_i8 v[30:33], v[134:137], v[218:221], v[30:33]
	v_mfma_i32_16x16x64_i8 v[106:109], v[146:149], v[190:193], v[106:109]
	v_mfma_i32_16x16x64_i8 v[82:85], v[154:157], v[190:193], v[82:85]
	v_mfma_i32_16x16x64_i8 v[74:77], v[154:157], v[198:201], v[74:77]
	v_mfma_i32_16x16x64_i8 v[78:81], v[146:149], v[198:201], v[78:81]
	v_mfma_i32_16x16x64_i8 v[46:49], v[146:149], v[206:209], v[46:49]
	v_mfma_i32_16x16x64_i8 v[42:45], v[154:157], v[206:209], v[42:45]
	v_mfma_i32_16x16x64_i8 v[10:13], v[154:157], v[214:217], v[10:13]
	v_mfma_i32_16x16x64_i8 v[14:17], v[146:149], v[214:217], v[14:17]
	v_mfma_i32_16x16x64_i8 v[106:109], v[150:153], v[194:197], v[106:109]
	v_mfma_i32_16x16x64_i8 v[82:85], v[158:161], v[194:197], v[82:85]
	v_mfma_i32_16x16x64_i8 v[74:77], v[158:161], v[202:205], v[74:77]
	v_mfma_i32_16x16x64_i8 v[78:81], v[150:153], v[202:205], v[78:81]
	v_mfma_i32_16x16x64_i8 v[46:49], v[150:153], v[210:213], v[46:49]
	v_mfma_i32_16x16x64_i8 v[42:45], v[158:161], v[210:213], v[42:45]
	v_mfma_i32_16x16x64_i8 v[10:13], v[158:161], v[218:221], v[10:13]
	v_mfma_i32_16x16x64_i8 v[14:17], v[150:153], v[218:221], v[14:17]
	s_barrier
	s_add_i32 s64, s64, 2
	s_add_u32 s6, s6, 0x100
	s_addc_u32 s7, s7, 0
	s_cmp_gt_u32 s64, 29
	s_cbranch_scc0 .LBB0_1051
	s_waitcnt vmcnt(0)
	s_cmpk_lt_u32 s59, 0x100
	s_cbranch_scc0 .LBB0_1054
	s_barrier

.LBB0_1173:
	ds_read_b128 v[158:161], v184
	ds_read_b128 v[150:153], v184 offset:1024
	ds_read_b128 v[154:157], v184 offset:2048
	ds_read_b128 v[146:149], v184 offset:3072
	ds_read_b128 v[142:145], v185
	ds_read_b128 v[130:133], v185 offset:1024
	ds_read_b128 v[138:141], v185 offset:2048
	ds_read_b128 v[134:137], v185 offset:3072
	s_add_u32 s38, s36, 0xfff80080
	s_addc_u32 s39, s37, -1
	s_cmp_eq_u32 s65, 28
	s_cselect_b32 s41, s18, s39
	s_cselect_b32 s40, s19, s38
	s_cselect_b32 s39, s25, s64
	s_cselect_b32 s38, s27, s63
	v_lshl_add_u64 v[212:213], s[36:37], 0, v[166:167]
	s_add_i32 m0, s35, 0xc000
	ds_read_b128 v[174:177], v186
	ds_read_b128 v[178:181], v186 offset:1024
	ds_read_b128 v[188:191], v186 offset:2048
	ds_read_b128 v[192:195], v186 offset:3072
	ds_read_b128 v[196:199], v186 offset:4096
	ds_read_b128 v[200:203], v186 offset:5120
	ds_read_b128 v[204:207], v186 offset:6144
	ds_read_b128 v[208:211], v186 offset:7168
	global_load_lds_dwordx4 v[212:213], off
	v_lshl_add_u64 v[212:213], s[36:37], 0, v[168:169]
	s_add_i32 m0, s35, 0xe000
	s_nop 0
	global_load_lds_dwordx4 v[212:213], off
	s_waitcnt vmcnt(8) lgkmcnt(0)
	s_barrier
	v_mfma_i32_16x16x64_i8 v[126:129], v[158:161], v[174:177], v[126:129]
	v_mfma_i32_16x16x64_i8 v[122:125], v[154:157], v[174:177], v[122:125]
	v_mfma_i32_16x16x64_i8 v[106:109], v[154:157], v[188:191], v[106:109]
	v_mfma_i32_16x16x64_i8 v[110:113], v[158:161], v[188:191], v[110:113]
	v_mfma_i32_16x16x64_i8 v[94:97], v[158:161], v[196:199], v[94:97]
	v_mfma_i32_16x16x64_i8 v[90:93], v[154:157], v[196:199], v[90:93]
	v_mfma_i32_16x16x64_i8 v[74:77], v[154:157], v[204:207], v[74:77]
	v_mfma_i32_16x16x64_i8 v[78:81], v[158:161], v[204:207], v[78:81]
	v_mfma_i32_16x16x64_i8 v[126:129], v[150:153], v[178:181], v[126:129]
	v_mfma_i32_16x16x64_i8 v[122:125], v[146:149], v[178:181], v[122:125]
	v_mfma_i32_16x16x64_i8 v[106:109], v[146:149], v[192:195], v[106:109]
	v_mfma_i32_16x16x64_i8 v[110:113], v[150:153], v[192:195], v[110:113]
	v_mfma_i32_16x16x64_i8 v[94:97], v[150:153], v[200:203], v[94:97]
	v_mfma_i32_16x16x64_i8 v[90:93], v[146:149], v[200:203], v[90:93]
	v_mfma_i32_16x16x64_i8 v[74:77], v[146:149], v[208:211], v[74:77]
	v_mfma_i32_16x16x64_i8 v[78:81], v[150:153], v[208:211], v[78:81]
	v_mfma_i32_16x16x64_i8 v[118:121], v[142:145], v[174:177], v[118:121]
	v_mfma_i32_16x16x64_i8 v[114:117], v[138:141], v[174:177], v[114:117]
	v_mfma_i32_16x16x64_i8 v[98:101], v[138:141], v[188:191], v[98:101]
	v_mfma_i32_16x16x64_i8 v[102:105], v[142:145], v[188:191], v[102:105]
	v_mfma_i32_16x16x64_i8 v[86:89], v[142:145], v[196:199], v[86:89]
	v_mfma_i32_16x16x64_i8 v[82:85], v[138:141], v[196:199], v[82:85]
	v_mfma_i32_16x16x64_i8 v[66:69], v[138:141], v[204:207], v[66:69]
	v_mfma_i32_16x16x64_i8 v[70:73], v[142:145], v[204:207], v[70:73]
	v_mfma_i32_16x16x64_i8 v[118:121], v[130:133], v[178:181], v[118:121]
	v_mfma_i32_16x16x64_i8 v[114:117], v[134:137], v[178:181], v[114:117]
	v_mfma_i32_16x16x64_i8 v[98:101], v[134:137], v[192:195], v[98:101]
	v_mfma_i32_16x16x64_i8 v[102:105], v[130:133], v[192:195], v[102:105]
	v_mfma_i32_16x16x64_i8 v[86:89], v[130:133], v[200:203], v[86:89]
	v_mfma_i32_16x16x64_i8 v[82:85], v[134:137], v[200:203], v[82:85]
	v_mfma_i32_16x16x64_i8 v[66:69], v[134:137], v[208:211], v[66:69]
	v_mfma_i32_16x16x64_i8 v[70:73], v[130:133], v[208:211], v[70:73]
	s_barrier
	s_add_i32 s66, s51, s3
	v_lshl_add_u64 v[174:175], s[38:39], 0, v[164:165]
	s_mov_b32 m0, s66
	ds_read_b128 v[188:191], v186 offset:16384
	ds_read_b128 v[192:195], v186 offset:17408
	ds_read_b128 v[196:199], v186 offset:18432
	ds_read_b128 v[200:203], v186 offset:19456
	ds_read_b128 v[204:207], v186 offset:20480
	ds_read_b128 v[208:211], v186 offset:21504
	ds_read_b128 v[212:215], v186 offset:22528
	ds_read_b128 v[216:219], v186 offset:23552
	global_load_lds_dwordx4 v[174:175], off
	s_add_i32 m0, s66, 0x2000
	s_add_u32 s66, s38, 0x80000
	v_lshl_add_u64 v[176:177], s[38:39], 0, v[162:163]
	s_addc_u32 s67, s39, 0
	s_add_i32 s68, s58, s3
	global_load_lds_dwordx4 v[176:177], off
	v_lshl_add_u64 v[178:179], s[66:67], 0, v[164:165]
	s_mov_b32 m0, s68
	v_lshl_add_u64 v[180:181], s[40:41], 0, v[162:163]
	global_load_lds_dwordx4 v[178:179], off
	v_lshl_add_u64 v[178:179], s[66:67], 0, v[162:163]
	s_add_i32 m0, s68, 0x2000
	s_nop 0
	global_load_lds_dwordx4 v[178:179], off
	v_lshl_add_u64 v[178:179], s[40:41], 0, v[164:165]
	s_mov_b32 m0, s35
	s_nop 0
	global_load_lds_dwordx4 v[178:179], off
	s_mov_b32 m0, s42
	s_nop 0
	global_load_lds_dwordx4 v[180:181], off
	s_waitcnt vmcnt(8) lgkmcnt(0)
	s_barrier
	v_mfma_i32_16x16x64_i8 v[62:65], v[158:161], v[188:191], v[62:65]
	v_mfma_i32_16x16x64_i8 v[58:61], v[154:157], v[188:191], v[58:61]
	v_mfma_i32_16x16x64_i8 v[42:45], v[154:157], v[196:199], v[42:45]
	v_mfma_i32_16x16x64_i8 v[46:49], v[158:161], v[196:199], v[46:49]
	v_mfma_i32_16x16x64_i8 v[30:33], v[158:161], v[204:207], v[30:33]
	v_mfma_i32_16x16x64_i8 v[26:29], v[154:157], v[204:207], v[26:29]
	v_mfma_i32_16x16x64_i8 v[10:13], v[154:157], v[212:215], v[10:13]
	v_mfma_i32_16x16x64_i8 v[14:17], v[158:161], v[212:215], v[14:17]
	v_mfma_i32_16x16x64_i8 v[62:65], v[150:153], v[192:195], v[62:65]
	v_mfma_i32_16x16x64_i8 v[58:61], v[146:149], v[192:195], v[58:61]
	v_mfma_i32_16x16x64_i8 v[42:45], v[146:149], v[200:203], v[42:45]
	v_mfma_i32_16x16x64_i8 v[46:49], v[150:153], v[200:203], v[46:49]
	v_mfma_i32_16x16x64_i8 v[30:33], v[150:153], v[208:211], v[30:33]
	v_mfma_i32_16x16x64_i8 v[26:29], v[146:149], v[208:211], v[26:29]
	v_mfma_i32_16x16x64_i8 v[10:13], v[146:149], v[216:219], v[10:13]
	v_mfma_i32_16x16x64_i8 v[14:17], v[150:153], v[216:219], v[14:17]
	v_mfma_i32_16x16x64_i8 v[54:57], v[142:145], v[188:191], v[54:57]
	v_mfma_i32_16x16x64_i8 v[50:53], v[138:141], v[188:191], v[50:53]
	v_mfma_i32_16x16x64_i8 v[34:37], v[138:141], v[196:199], v[34:37]
	v_mfma_i32_16x16x64_i8 v[38:41], v[142:145], v[196:199], v[38:41]
	v_mfma_i32_16x16x64_i8 v[22:25], v[142:145], v[204:207], v[22:25]
	v_mfma_i32_16x16x64_i8 v[18:21], v[138:141], v[204:207], v[18:21]
	v_mfma_i32_16x16x64_i8 v[2:5], v[138:141], v[212:215], v[2:5]
	v_mfma_i32_16x16x64_i8 v[6:9], v[142:145], v[212:215], v[6:9]
	v_mfma_i32_16x16x64_i8 v[54:57], v[130:133], v[192:195], v[54:57]
	v_mfma_i32_16x16x64_i8 v[50:53], v[134:137], v[192:195], v[50:53]
	v_mfma_i32_16x16x64_i8 v[34:37], v[134:137], v[200:203], v[34:37]
	v_mfma_i32_16x16x64_i8 v[38:41], v[130:133], v[200:203], v[38:41]
	v_mfma_i32_16x16x64_i8 v[22:25], v[130:133], v[208:211], v[22:25]
	v_mfma_i32_16x16x64_i8 v[18:21], v[134:137], v[208:211], v[18:21]
	v_mfma_i32_16x16x64_i8 v[2:5], v[134:137], v[216:219], v[2:5]
	v_mfma_i32_16x16x64_i8 v[6:9], v[130:133], v[216:219], v[6:9]
	s_barrier
	s_add_i32 s66, 0, 0x18000
	s_add_i32 s67, 0, 0x1c000
	v_add_u32_e32 v142, s66, v182
	v_add_u32_e32 v158, s67, v182
	ds_read_b128 v[130:133], v142
	ds_read_b128 v[134:137], v142 offset:1024
	ds_read_b128 v[138:141], v142 offset:2048
	ds_read_b128 v[142:145], v142 offset:3072
	ds_read_b128 v[146:149], v158
	ds_read_b128 v[150:153], v158 offset:1024
	ds_read_b128 v[154:157], v158 offset:2048
	ds_read_b128 v[158:161], v158 offset:3072
	s_add_u32 s40, s40, 0x80000
	s_addc_u32 s41, s41, 0
	s_mov_b32 m0, s43
	v_lshl_add_u64 v[220:221], s[40:41], 0, v[164:165]
	ds_read_b128 v[188:191], v186 offset:32768
	ds_read_b128 v[192:195], v186 offset:33792
	ds_read_b128 v[196:199], v186 offset:34816
	ds_read_b128 v[200:203], v186 offset:35840
	ds_read_b128 v[204:207], v186 offset:36864
	ds_read_b128 v[208:211], v186 offset:37888
	ds_read_b128 v[212:215], v186 offset:38912
	ds_read_b128 v[216:219], v186 offset:39936
	global_load_lds_dwordx4 v[220:221], off
	v_lshl_add_u64 v[220:221], s[40:41], 0, v[162:163]
	s_mov_b32 m0, s44
	s_nop 0
	global_load_lds_dwordx4 v[220:221], off
	s_waitcnt vmcnt(8) lgkmcnt(0)
	s_barrier
	v_mfma_i32_16x16x64_i8 v[126:129], v[130:133], v[188:191], v[126:129]
	v_mfma_i32_16x16x64_i8 v[122:125], v[138:141], v[188:191], v[122:125]
	v_mfma_i32_16x16x64_i8 v[106:109], v[138:141], v[196:199], v[106:109]
	v_mfma_i32_16x16x64_i8 v[110:113], v[130:133], v[196:199], v[110:113]
	v_mfma_i32_16x16x64_i8 v[94:97], v[130:133], v[204:207], v[94:97]
	v_mfma_i32_16x16x64_i8 v[90:93], v[138:141], v[204:207], v[90:93]
	v_mfma_i32_16x16x64_i8 v[74:77], v[138:141], v[212:215], v[74:77]
	v_mfma_i32_16x16x64_i8 v[78:81], v[130:133], v[212:215], v[78:81]
	v_mfma_i32_16x16x64_i8 v[126:129], v[134:137], v[192:195], v[126:129]
	v_mfma_i32_16x16x64_i8 v[122:125], v[142:145], v[192:195], v[122:125]
	v_mfma_i32_16x16x64_i8 v[106:109], v[142:145], v[200:203], v[106:109]
	v_mfma_i32_16x16x64_i8 v[110:113], v[134:137], v[200:203], v[110:113]
	v_mfma_i32_16x16x64_i8 v[94:97], v[134:137], v[208:211], v[94:97]
	v_mfma_i32_16x16x64_i8 v[90:93], v[142:145], v[208:211], v[90:93]
	v_mfma_i32_16x16x64_i8 v[74:77], v[142:145], v[216:219], v[74:77]
	v_mfma_i32_16x16x64_i8 v[78:81], v[134:137], v[216:219], v[78:81]
	v_mfma_i32_16x16x64_i8 v[118:121], v[146:149], v[188:191], v[118:121]
	v_mfma_i32_16x16x64_i8 v[114:117], v[154:157], v[188:191], v[114:117]
	v_mfma_i32_16x16x64_i8 v[98:101], v[154:157], v[196:199], v[98:101]
	v_mfma_i32_16x16x64_i8 v[102:105], v[146:149], v[196:199], v[102:105]
	v_mfma_i32_16x16x64_i8 v[86:89], v[146:149], v[204:207], v[86:89]
	v_mfma_i32_16x16x64_i8 v[82:85], v[154:157], v[204:207], v[82:85]
	v_mfma_i32_16x16x64_i8 v[66:69], v[154:157], v[212:215], v[66:69]
	v_mfma_i32_16x16x64_i8 v[70:73], v[146:149], v[212:215], v[70:73]
	v_mfma_i32_16x16x64_i8 v[118:121], v[150:153], v[192:195], v[118:121]
	v_mfma_i32_16x16x64_i8 v[114:117], v[158:161], v[192:195], v[114:117]
	v_mfma_i32_16x16x64_i8 v[98:101], v[158:161], v[200:203], v[98:101]
	v_mfma_i32_16x16x64_i8 v[102:105], v[150:153], v[200:203], v[102:105]
	v_mfma_i32_16x16x64_i8 v[86:89], v[150:153], v[208:211], v[86:89]
	v_mfma_i32_16x16x64_i8 v[82:85], v[158:161], v[208:211], v[82:85]
	v_mfma_i32_16x16x64_i8 v[66:69], v[158:161], v[216:219], v[66:69]
	v_mfma_i32_16x16x64_i8 v[70:73], v[150:153], v[216:219], v[70:73]
	s_barrier
	s_add_i32 s40, s66, s3
	v_lshl_add_u64 v[174:175], v[174:175], 0, s[8:9]
	s_mov_b32 m0, s40
	ds_read_b128 v[188:191], v186 offset:49152
	ds_read_b128 v[192:195], v186 offset:50176
	ds_read_b128 v[196:199], v186 offset:51200
	ds_read_b128 v[200:203], v186 offset:52224
	ds_read_b128 v[204:207], v186 offset:53248
	ds_read_b128 v[208:211], v186 offset:54272
	ds_read_b128 v[212:215], v186 offset:55296
	ds_read_b128 v[216:219], v186 offset:56320
	global_load_lds_dwordx4 v[174:175], off
	s_add_i32 m0, s40, 0x2000
	s_add_u32 s38, s38, 0x80080
	v_lshl_add_u64 v[174:175], v[176:177], 0, s[8:9]
	s_addc_u32 s39, s39, 0
	s_add_i32 s40, s67, s3
	global_load_lds_dwordx4 v[174:175], off
	v_lshl_add_u64 v[174:175], s[38:39], 0, v[164:165]
	s_mov_b32 m0, s40
	s_nop 0
	global_load_lds_dwordx4 v[174:175], off
	v_lshl_add_u64 v[174:175], s[38:39], 0, v[162:163]
	s_add_i32 m0, s40, 0x2000
	s_nop 0
	global_load_lds_dwordx4 v[174:175], off
	v_lshl_add_u64 v[174:175], v[178:179], 0, s[8:9]
	s_mov_b32 m0, s49
	s_nop 0
	global_load_lds_dwordx4 v[174:175], off
	v_lshl_add_u64 v[174:175], v[180:181], 0, s[8:9]
	s_mov_b32 m0, s50
	s_nop 0
	global_load_lds_dwordx4 v[174:175], off
	s_waitcnt vmcnt(8) lgkmcnt(0)
	s_barrier
	v_mfma_i32_16x16x64_i8 v[62:65], v[130:133], v[188:191], v[62:65]
	v_mfma_i32_16x16x64_i8 v[58:61], v[138:141], v[188:191], v[58:61]
	v_mfma_i32_16x16x64_i8 v[42:45], v[138:141], v[196:199], v[42:45]
	v_mfma_i32_16x16x64_i8 v[46:49], v[130:133], v[196:199], v[46:49]
	v_mfma_i32_16x16x64_i8 v[30:33], v[130:133], v[204:207], v[30:33]
	v_mfma_i32_16x16x64_i8 v[26:29], v[138:141], v[204:207], v[26:29]
	v_mfma_i32_16x16x64_i8 v[10:13], v[138:141], v[212:215], v[10:13]
	v_mfma_i32_16x16x64_i8 v[14:17], v[130:133], v[212:215], v[14:17]
	v_mfma_i32_16x16x64_i8 v[62:65], v[134:137], v[192:195], v[62:65]
	v_mfma_i32_16x16x64_i8 v[58:61], v[142:145], v[192:195], v[58:61]
	v_mfma_i32_16x16x64_i8 v[42:45], v[142:145], v[200:203], v[42:45]
	v_mfma_i32_16x16x64_i8 v[46:49], v[134:137], v[200:203], v[46:49]
	v_mfma_i32_16x16x64_i8 v[30:33], v[134:137], v[208:211], v[30:33]
	v_mfma_i32_16x16x64_i8 v[26:29], v[142:145], v[208:211], v[26:29]
	v_mfma_i32_16x16x64_i8 v[10:13], v[142:145], v[216:219], v[10:13]
	v_mfma_i32_16x16x64_i8 v[14:17], v[134:137], v[216:219], v[14:17]
	v_mfma_i32_16x16x64_i8 v[54:57], v[146:149], v[188:191], v[54:57]
	v_mfma_i32_16x16x64_i8 v[50:53], v[154:157], v[188:191], v[50:53]
	v_mfma_i32_16x16x64_i8 v[34:37], v[154:157], v[196:199], v[34:37]
	v_mfma_i32_16x16x64_i8 v[38:41], v[146:149], v[196:199], v[38:41]
	v_mfma_i32_16x16x64_i8 v[22:25], v[146:149], v[204:207], v[22:25]
	v_mfma_i32_16x16x64_i8 v[18:21], v[154:157], v[204:207], v[18:21]
	v_mfma_i32_16x16x64_i8 v[2:5], v[154:157], v[212:215], v[2:5]
	v_mfma_i32_16x16x64_i8 v[6:9], v[146:149], v[212:215], v[6:9]
	v_mfma_i32_16x16x64_i8 v[54:57], v[150:153], v[192:195], v[54:57]
	v_mfma_i32_16x16x64_i8 v[50:53], v[158:161], v[192:195], v[50:53]
	v_mfma_i32_16x16x64_i8 v[34:37], v[158:161], v[200:203], v[34:37]
	v_mfma_i32_16x16x64_i8 v[38:41], v[150:153], v[200:203], v[38:41]
	v_mfma_i32_16x16x64_i8 v[22:25], v[150:153], v[208:211], v[22:25]
	v_mfma_i32_16x16x64_i8 v[18:21], v[158:161], v[208:211], v[18:21]
	v_mfma_i32_16x16x64_i8 v[2:5], v[158:161], v[216:219], v[2:5]
	v_mfma_i32_16x16x64_i8 v[6:9], v[150:153], v[216:219], v[6:9]
	s_barrier
	s_add_i32 s65, s65, 2
	s_add_u32 s36, s36, 0x100
	s_addc_u32 s37, s37, 0
	s_add_u32 s63, s63, 0x100
	s_addc_u32 s64, s64, 0
	s_cmp_gt_u32 s65, 29
	s_cbranch_scc0 .LBB0_1173
	s_and_b64 vcc, exec, s[12:13]
	s_cbranch_vccz .LBB0_1176
	s_barrier

.LBB0_1291:
	ds_read_b128 v[26:29], v184
	ds_read_b128 v[30:33], v184 offset:1024
	ds_read_b128 v[18:21], v184 offset:2048
	ds_read_b128 v[22:25], v184 offset:3072
	ds_read_b128 v[10:13], v185
	ds_read_b128 v[14:17], v185 offset:1024
	ds_read_b128 v[2:5], v185 offset:2048
	ds_read_b128 v[6:9], v185 offset:3072
	s_add_u32 s20, s14, s16
	s_addc_u32 s21, s15, s17
	s_add_u32 s20, s20, 0x2a800100
	s_addc_u32 s21, s21, 0
	s_add_u32 s48, s31, s16
	s_addc_u32 s49, s34, s17
	s_cmpk_eq_i32 s16, 0x700
	s_cselect_b32 s23, s9, s21
	s_cselect_b32 s22, s8, s20
	s_cselect_b32 s21, s5, s49
	s_cselect_b32 s20, s4, s48
	s_mov_b32 m0, s36
	v_lshl_add_u64 v[214:215], v[170:171], 0, s[16:17]
	ds_read_b128 v[174:177], v186
	ds_read_b128 v[178:181], v186 offset:1024
	ds_read_b128 v[190:193], v186 offset:2048
	ds_read_b128 v[194:197], v186 offset:3072
	ds_read_b128 v[198:201], v186 offset:4096
	ds_read_b128 v[202:205], v186 offset:5120
	ds_read_b128 v[206:209], v186 offset:6144
	ds_read_b128 v[210:213], v186 offset:7168
	global_load_lds_dwordx4 v[214:215], off
	v_lshl_add_u64 v[214:215], v[172:173], 0, s[16:17]
	s_mov_b32 m0, s37
	s_nop 0
	global_load_lds_dwordx4 v[214:215], off
	s_waitcnt vmcnt(8) lgkmcnt(0)
	s_barrier
	v_mfma_f32_16x16x128_f8f6f4 v[158:161], v[26:33], v[174:181], v[158:161]
	v_mfma_f32_16x16x128_f8f6f4 v[154:157], v[18:25], v[174:181], v[154:157]
	v_mfma_f32_16x16x128_f8f6f4 v[138:141], v[18:25], v[190:197], v[138:141]
	v_mfma_f32_16x16x128_f8f6f4 v[146:149], v[26:33], v[190:197], v[146:149]
	v_mfma_f32_16x16x128_f8f6f4 v[130:133], v[26:33], v[198:205], v[130:133]
	v_mfma_f32_16x16x128_f8f6f4 v[122:125], v[18:25], v[198:205], v[122:125]
	v_mfma_f32_16x16x128_f8f6f4 v[106:109], v[18:25], v[206:213], v[106:109]
	v_mfma_f32_16x16x128_f8f6f4 v[114:117], v[26:33], v[206:213], v[114:117]
	v_mfma_f32_16x16x128_f8f6f4 v[102:105], v[10:17], v[206:213], v[102:105]
	v_mfma_f32_16x16x128_f8f6f4 v[98:101], v[2:9], v[206:213], v[98:101]
	v_mfma_f32_16x16x128_f8f6f4 v[142:145], v[2:9], v[174:181], v[142:145]
	v_mfma_f32_16x16x128_f8f6f4 v[150:153], v[10:17], v[174:181], v[150:153]
	v_mfma_f32_16x16x128_f8f6f4 v[134:137], v[10:17], v[190:197], v[134:137]
	v_mfma_f32_16x16x128_f8f6f4 v[126:129], v[2:9], v[190:197], v[126:129]
	v_mfma_f32_16x16x128_f8f6f4 v[110:113], v[2:9], v[198:205], v[110:113]
	v_mfma_f32_16x16x128_f8f6f4 v[118:121], v[10:17], v[198:205], v[118:121]
	s_barrier
	s_mov_b32 m0, s38
	v_lshl_add_u64 v[174:175], s[20:21], 0, v[164:165]
	s_add_u32 s48, s20, 0x80000
	ds_read_b128 v[190:193], v186 offset:16384
	ds_read_b128 v[194:197], v186 offset:17408
	ds_read_b128 v[198:201], v186 offset:18432
	ds_read_b128 v[202:205], v186 offset:19456
	ds_read_b128 v[206:209], v186 offset:20480
	ds_read_b128 v[210:213], v186 offset:21504
	ds_read_b128 v[214:217], v186 offset:22528
	ds_read_b128 v[218:221], v186 offset:23552
	global_load_lds_dwordx4 v[174:175], off
	v_lshl_add_u64 v[176:177], s[20:21], 0, v[168:169]
	s_mov_b32 m0, s39
	s_addc_u32 s49, s21, 0
	global_load_lds_dwordx4 v[176:177], off
	s_mov_b32 m0, s40
	v_lshl_add_u64 v[180:181], s[22:23], 0, v[166:167]
	global_load_lds_dwordx4 v164, s[48:49]
	s_mov_b32 m0, s41
	s_nop 0
	global_load_lds_dwordx4 v168, s[48:49]
	v_lshl_add_u64 v[178:179], s[22:23], 0, v[162:163]
	s_mov_b32 m0, s24
	s_nop 0
	global_load_lds_dwordx4 v[178:179], off
	s_mov_b32 m0, s25
	s_nop 0
	global_load_lds_dwordx4 v[180:181], off
	s_waitcnt vmcnt(8) lgkmcnt(0)
	s_barrier
	v_mfma_f32_16x16x128_f8f6f4 v[82:85], v[26:33], v[198:205], v[82:85]
	v_mfma_f32_16x16x128_f8f6f4 v[74:77], v[18:25], v[198:205], v[74:77]
	v_mfma_f32_16x16x128_f8f6f4 v[90:93], v[18:25], v[190:197], v[90:93]
	v_mfma_f32_16x16x128_f8f6f4 v[94:97], v[26:33], v[190:197], v[94:97]
	v_mfma_f32_16x16x128_f8f6f4 v[66:69], v[26:33], v[206:213], v[66:69]
	v_mfma_f32_16x16x128_f8f6f4 v[58:61], v[18:25], v[206:213], v[58:61]
	v_mfma_f32_16x16x128_f8f6f4 v[42:45], v[18:25], v[214:221], v[42:45]
	v_mfma_f32_16x16x128_f8f6f4 v[50:53], v[26:33], v[214:221], v[50:53]
	v_mfma_f32_16x16x128_f8f6f4 v[38:41], v[10:17], v[214:221], v[38:41]
	v_mfma_f32_16x16x128_f8f6f4 v[34:37], v[2:9], v[214:221], v[34:37]
	v_mfma_f32_16x16x128_f8f6f4 v[78:81], v[2:9], v[190:197], v[78:81]
	v_mfma_f32_16x16x128_f8f6f4 v[86:89], v[10:17], v[190:197], v[86:89]
	v_mfma_f32_16x16x128_f8f6f4 v[70:73], v[10:17], v[198:205], v[70:73]
	v_mfma_f32_16x16x128_f8f6f4 v[62:65], v[2:9], v[198:205], v[62:65]
	v_mfma_f32_16x16x128_f8f6f4 v[46:49], v[2:9], v[206:213], v[46:49]
	v_mfma_f32_16x16x128_f8f6f4 v[54:57], v[10:17], v[206:213], v[54:57]
	s_barrier
	ds_read_b128 v[2:5], v187
	ds_read_b128 v[6:9], v187 offset:1024
	ds_read_b128 v[10:13], v187 offset:2048
	ds_read_b128 v[14:17], v187 offset:3072
	ds_read_b128 v[18:21], v188
	ds_read_b128 v[22:25], v188 offset:1024
	ds_read_b128 v[26:29], v188 offset:2048
	ds_read_b128 v[30:33], v188 offset:3072
	s_add_u32 s22, s22, 0x80000
	s_addc_u32 s23, s23, 0
	s_mov_b32 m0, s26
	ds_read_b128 v[190:193], v186 offset:32768
	ds_read_b128 v[194:197], v186 offset:33792
	ds_read_b128 v[198:201], v186 offset:34816
	ds_read_b128 v[202:205], v186 offset:35840
	ds_read_b128 v[206:209], v186 offset:36864
	ds_read_b128 v[210:213], v186 offset:37888
	ds_read_b128 v[214:217], v186 offset:38912
	ds_read_b128 v[218:221], v186 offset:39936
	global_load_lds_dwordx4 v162, s[22:23]
	s_mov_b32 m0, s27
	s_nop 0
	global_load_lds_dwordx4 v166, s[22:23]
	s_waitcnt vmcnt(8) lgkmcnt(0)
	s_barrier
	v_mfma_f32_16x16x128_f8f6f4 v[122:125], v[10:17], v[206:213], v[122:125]
	v_mfma_f32_16x16x128_f8f6f4 v[130:133], v[2:9], v[206:213], v[130:133]
	v_mfma_f32_16x16x128_f8f6f4 v[158:161], v[2:9], v[190:197], v[158:161]
	v_mfma_f32_16x16x128_f8f6f4 v[154:157], v[10:17], v[190:197], v[154:157]
	v_mfma_f32_16x16x128_f8f6f4 v[138:141], v[10:17], v[198:205], v[138:141]
	v_mfma_f32_16x16x128_f8f6f4 v[146:149], v[2:9], v[198:205], v[146:149]
	v_mfma_f32_16x16x128_f8f6f4 v[114:117], v[2:9], v[214:221], v[114:117]
	v_mfma_f32_16x16x128_f8f6f4 v[106:109], v[10:17], v[214:221], v[106:109]
	v_mfma_f32_16x16x128_f8f6f4 v[102:105], v[18:25], v[214:221], v[102:105]
	v_mfma_f32_16x16x128_f8f6f4 v[98:101], v[26:33], v[214:221], v[98:101]
	v_mfma_f32_16x16x128_f8f6f4 v[142:145], v[26:33], v[190:197], v[142:145]
	v_mfma_f32_16x16x128_f8f6f4 v[150:153], v[18:25], v[190:197], v[150:153]
	v_mfma_f32_16x16x128_f8f6f4 v[134:137], v[18:25], v[198:205], v[134:137]
	v_mfma_f32_16x16x128_f8f6f4 v[126:129], v[26:33], v[198:205], v[126:129]
	v_mfma_f32_16x16x128_f8f6f4 v[110:113], v[26:33], v[206:213], v[110:113]
	v_mfma_f32_16x16x128_f8f6f4 v[118:121], v[18:25], v[206:213], v[118:121]
	s_barrier
	s_mov_b32 m0, s42
	v_lshl_add_u64 v[174:175], v[174:175], 0, s[12:13]
	s_add_u32 s20, s20, 0x80080
	ds_read_b128 v[190:193], v186 offset:49152
	ds_read_b128 v[194:197], v186 offset:50176
	ds_read_b128 v[198:201], v186 offset:51200
	ds_read_b128 v[202:205], v186 offset:52224
	ds_read_b128 v[206:209], v186 offset:53248
	ds_read_b128 v[210:213], v186 offset:54272
	ds_read_b128 v[214:217], v186 offset:55296
	ds_read_b128 v[218:221], v186 offset:56320
	global_load_lds_dwordx4 v[174:175], off
	v_lshl_add_u64 v[174:175], v[176:177], 0, s[12:13]
	s_mov_b32 m0, s43
	s_addc_u32 s21, s21, 0
	global_load_lds_dwordx4 v[174:175], off
	s_mov_b32 m0, s44
	s_nop 0
	global_load_lds_dwordx4 v164, s[20:21]
	s_mov_b32 m0, s45
	s_nop 0
	global_load_lds_dwordx4 v168, s[20:21]
	v_lshl_add_u64 v[174:175], v[178:179], 0, s[12:13]
	s_mov_b32 m0, s29
	s_nop 0
	global_load_lds_dwordx4 v[174:175], off
	v_lshl_add_u64 v[174:175], v[180:181], 0, s[12:13]
	s_mov_b32 m0, s30
	s_nop 0
	global_load_lds_dwordx4 v[174:175], off
	s_waitcnt vmcnt(8) lgkmcnt(0)
	s_barrier
	v_mfma_f32_16x16x128_f8f6f4 v[66:69], v[2:9], v[206:213], v[66:69]
	v_mfma_f32_16x16x128_f8f6f4 v[58:61], v[10:17], v[206:213], v[58:61]
	v_mfma_f32_16x16x128_f8f6f4 v[90:93], v[10:17], v[190:197], v[90:93]
	v_mfma_f32_16x16x128_f8f6f4 v[94:97], v[2:9], v[190:197], v[94:97]
	v_mfma_f32_16x16x128_f8f6f4 v[82:85], v[2:9], v[198:205], v[82:85]
	v_mfma_f32_16x16x128_f8f6f4 v[74:77], v[10:17], v[198:205], v[74:77]
	v_mfma_f32_16x16x128_f8f6f4 v[42:45], v[10:17], v[214:221], v[42:45]
	v_mfma_f32_16x16x128_f8f6f4 v[50:53], v[2:9], v[214:221], v[50:53]
	v_mfma_f32_16x16x128_f8f6f4 v[38:41], v[18:25], v[214:221], v[38:41]
	v_mfma_f32_16x16x128_f8f6f4 v[34:37], v[26:33], v[214:221], v[34:37]
	v_mfma_f32_16x16x128_f8f6f4 v[78:81], v[26:33], v[190:197], v[78:81]
	v_mfma_f32_16x16x128_f8f6f4 v[86:89], v[18:25], v[190:197], v[86:89]
	v_mfma_f32_16x16x128_f8f6f4 v[70:73], v[18:25], v[198:205], v[70:73]
	v_mfma_f32_16x16x128_f8f6f4 v[62:65], v[26:33], v[198:205], v[62:65]
	v_mfma_f32_16x16x128_f8f6f4 v[46:49], v[26:33], v[206:213], v[46:49]
	v_mfma_f32_16x16x128_f8f6f4 v[54:57], v[18:25], v[206:213], v[54:57]
	s_barrier
	s_add_i32 s35, s35, 2
	s_add_u32 s16, s16, 0x100
	s_addc_u32 s17, s17, 0
	s_cmp_gt_u32 s35, 13
	s_cbranch_scc0 .LBB0_1291
	s_cmpk_lt_u32 s19, 0x100
	s_cbranch_scc0 .LBB0_1294
	s_barrier

.LBB0_1309:
	ds_read_b128 v[26:29], v189
	ds_read_b128 v[30:33], v189 offset:1024
	ds_read_b128 v[18:21], v189 offset:2048
	ds_read_b128 v[22:25], v189 offset:3072
	ds_read_b128 v[10:13], v190
	ds_read_b128 v[14:17], v190 offset:1024
	ds_read_b128 v[2:5], v190 offset:2048
	ds_read_b128 v[6:9], v190 offset:3072
	s_add_u32 s40, s38, 0xfff80080
	s_addc_u32 s41, s39, -1
	s_cmp_eq_u32 s72, 28
	s_cselect_b32 s43, s18, s41
	s_cselect_b32 s42, s19, s40
	s_cselect_b32 s41, s27, s71
	s_cselect_b32 s40, s29, s70
	s_add_i32 m0, s37, 0xc000
	ds_read_b128 v[178:181], v191
	ds_read_b128 v[182:185], v191 offset:1024
	ds_read_b128 v[192:195], v191 offset:2048
	ds_read_b128 v[196:199], v191 offset:3072
	ds_read_b128 v[200:203], v191 offset:4096
	ds_read_b128 v[204:207], v191 offset:5120
	ds_read_b128 v[208:211], v191 offset:6144
	ds_read_b128 v[212:215], v191 offset:7168
	global_load_lds_dwordx4 v170, s[38:39]
	v_lshl_add_u64 v[216:217], s[38:39], 0, v[172:173]
	s_add_i32 m0, s37, 0xe000
	s_nop 0
	global_load_lds_dwordx4 v[216:217], off
	s_waitcnt vmcnt(8) lgkmcnt(0)
	s_barrier
	v_mfma_f32_16x16x128_f8f6f4 v[158:161], v[26:33], v[178:185], v[158:161]
	v_mfma_f32_16x16x128_f8f6f4 v[154:157], v[18:25], v[178:185], v[154:157]
	v_mfma_f32_16x16x128_f8f6f4 v[138:141], v[18:25], v[192:199], v[138:141]
	v_mfma_f32_16x16x128_f8f6f4 v[146:149], v[26:33], v[192:199], v[146:149]
	v_mfma_f32_16x16x128_f8f6f4 v[130:133], v[26:33], v[200:207], v[130:133]
	v_mfma_f32_16x16x128_f8f6f4 v[122:125], v[18:25], v[200:207], v[122:125]
	v_mfma_f32_16x16x128_f8f6f4 v[106:109], v[18:25], v[208:215], v[106:109]
	v_mfma_f32_16x16x128_f8f6f4 v[114:117], v[26:33], v[208:215], v[114:117]
	v_mfma_f32_16x16x128_f8f6f4 v[102:105], v[10:17], v[208:215], v[102:105]
	v_mfma_f32_16x16x128_f8f6f4 v[98:101], v[2:9], v[208:215], v[98:101]
	v_mfma_f32_16x16x128_f8f6f4 v[142:145], v[2:9], v[178:185], v[142:145]
	v_mfma_f32_16x16x128_f8f6f4 v[150:153], v[10:17], v[178:185], v[150:153]
	v_mfma_f32_16x16x128_f8f6f4 v[134:137], v[10:17], v[192:199], v[134:137]
	v_mfma_f32_16x16x128_f8f6f4 v[126:129], v[2:9], v[192:199], v[126:129]
	v_mfma_f32_16x16x128_f8f6f4 v[110:113], v[2:9], v[200:207], v[110:113]
	v_mfma_f32_16x16x128_f8f6f4 v[118:121], v[10:17], v[200:207], v[118:121]
	s_barrier
	s_add_i32 s64, s59, s3
	v_lshl_add_u64 v[178:179], s[40:41], 0, v[166:167]
	s_mov_b32 m0, s64
	ds_read_b128 v[192:195], v191 offset:16384
	ds_read_b128 v[196:199], v191 offset:17408
	ds_read_b128 v[200:203], v191 offset:18432
	ds_read_b128 v[204:207], v191 offset:19456
	ds_read_b128 v[208:211], v191 offset:20480
	ds_read_b128 v[212:215], v191 offset:21504
	ds_read_b128 v[216:219], v191 offset:22528
	ds_read_b128 v[220:223], v191 offset:23552
	global_load_lds_dwordx4 v[178:179], off
	s_add_i32 m0, s64, 0x2000
	s_add_u32 s64, s40, 0x80000
	v_lshl_add_u64 v[180:181], s[40:41], 0, v[162:163]
	s_addc_u32 s65, s41, 0
	s_add_i32 s73, s62, s3
	global_load_lds_dwordx4 v[180:181], off
	s_mov_b32 m0, s73
	v_lshl_add_u64 v[184:185], s[42:43], 0, v[164:165]
	global_load_lds_dwordx4 v166, s[64:65]
	s_add_i32 m0, s73, 0x2000
	s_nop 0
	global_load_lds_dwordx4 v162, s[64:65]
	v_lshl_add_u64 v[182:183], s[42:43], 0, v[168:169]
	s_mov_b32 m0, s37
	s_nop 0
	global_load_lds_dwordx4 v[182:183], off
	s_mov_b32 m0, s44
	s_nop 0
	global_load_lds_dwordx4 v[184:185], off
	s_waitcnt vmcnt(8) lgkmcnt(0)
	s_barrier
	v_mfma_f32_16x16x128_f8f6f4 v[82:85], v[26:33], v[200:207], v[82:85]
	v_mfma_f32_16x16x128_f8f6f4 v[74:77], v[18:25], v[200:207], v[74:77]
	v_mfma_f32_16x16x128_f8f6f4 v[90:93], v[18:25], v[192:199], v[90:93]
	v_mfma_f32_16x16x128_f8f6f4 v[94:97], v[26:33], v[192:199], v[94:97]
	v_mfma_f32_16x16x128_f8f6f4 v[66:69], v[26:33], v[208:215], v[66:69]
	v_mfma_f32_16x16x128_f8f6f4 v[58:61], v[18:25], v[208:215], v[58:61]
	v_mfma_f32_16x16x128_f8f6f4 v[42:45], v[18:25], v[216:223], v[42:45]
	v_mfma_f32_16x16x128_f8f6f4 v[50:53], v[26:33], v[216:223], v[50:53]
	v_mfma_f32_16x16x128_f8f6f4 v[38:41], v[10:17], v[216:223], v[38:41]
	v_mfma_f32_16x16x128_f8f6f4 v[34:37], v[2:9], v[216:223], v[34:37]
	v_mfma_f32_16x16x128_f8f6f4 v[78:81], v[2:9], v[192:199], v[78:81]
	v_mfma_f32_16x16x128_f8f6f4 v[86:89], v[10:17], v[192:199], v[86:89]
	v_mfma_f32_16x16x128_f8f6f4 v[70:73], v[10:17], v[200:207], v[70:73]
	v_mfma_f32_16x16x128_f8f6f4 v[62:65], v[2:9], v[200:207], v[62:65]
	v_mfma_f32_16x16x128_f8f6f4 v[46:49], v[2:9], v[208:215], v[46:49]
	v_mfma_f32_16x16x128_f8f6f4 v[54:57], v[10:17], v[208:215], v[54:57]
	s_barrier
	s_add_i32 s64, 0, 0x18000
	s_add_i32 s65, 0, 0x1c000
	v_add_u32_e32 v14, s64, v187
	v_add_u32_e32 v30, s65, v187
	ds_read_b128 v[2:5], v14
	ds_read_b128 v[6:9], v14 offset:1024
	ds_read_b128 v[10:13], v14 offset:2048
	ds_read_b128 v[14:17], v14 offset:3072
	ds_read_b128 v[18:21], v30
	ds_read_b128 v[22:25], v30 offset:1024
	ds_read_b128 v[26:29], v30 offset:2048
	ds_read_b128 v[30:33], v30 offset:3072
	s_add_u32 s42, s42, 0x80000
	s_addc_u32 s43, s43, 0
	s_mov_b32 m0, s45
	ds_read_b128 v[192:195], v191 offset:32768
	ds_read_b128 v[196:199], v191 offset:33792
	ds_read_b128 v[200:203], v191 offset:34816
	ds_read_b128 v[204:207], v191 offset:35840
	ds_read_b128 v[208:211], v191 offset:36864
	ds_read_b128 v[212:215], v191 offset:37888
	ds_read_b128 v[216:219], v191 offset:38912
	ds_read_b128 v[220:223], v191 offset:39936
	global_load_lds_dwordx4 v168, s[42:43]
	s_mov_b32 m0, s48
	s_nop 0
	global_load_lds_dwordx4 v164, s[42:43]
	s_waitcnt vmcnt(8) lgkmcnt(0)
	s_barrier
	v_mfma_f32_16x16x128_f8f6f4 v[122:125], v[10:17], v[208:215], v[122:125]
	v_mfma_f32_16x16x128_f8f6f4 v[130:133], v[2:9], v[208:215], v[130:133]
	v_mfma_f32_16x16x128_f8f6f4 v[158:161], v[2:9], v[192:199], v[158:161]
	v_mfma_f32_16x16x128_f8f6f4 v[154:157], v[10:17], v[192:199], v[154:157]
	v_mfma_f32_16x16x128_f8f6f4 v[138:141], v[10:17], v[200:207], v[138:141]
	v_mfma_f32_16x16x128_f8f6f4 v[146:149], v[2:9], v[200:207], v[146:149]
	v_mfma_f32_16x16x128_f8f6f4 v[114:117], v[2:9], v[216:223], v[114:117]
	v_mfma_f32_16x16x128_f8f6f4 v[106:109], v[10:17], v[216:223], v[106:109]
	v_mfma_f32_16x16x128_f8f6f4 v[102:105], v[18:25], v[216:223], v[102:105]
	v_mfma_f32_16x16x128_f8f6f4 v[98:101], v[26:33], v[216:223], v[98:101]
	v_mfma_f32_16x16x128_f8f6f4 v[142:145], v[26:33], v[192:199], v[142:145]
	v_mfma_f32_16x16x128_f8f6f4 v[150:153], v[18:25], v[192:199], v[150:153]
	v_mfma_f32_16x16x128_f8f6f4 v[134:137], v[18:25], v[200:207], v[134:137]
	v_mfma_f32_16x16x128_f8f6f4 v[126:129], v[26:33], v[200:207], v[126:129]
	v_mfma_f32_16x16x128_f8f6f4 v[110:113], v[26:33], v[208:215], v[110:113]
	v_mfma_f32_16x16x128_f8f6f4 v[118:121], v[18:25], v[208:215], v[118:121]
	s_barrier
	s_add_i32 s42, s64, s3
	v_lshl_add_u64 v[178:179], v[178:179], 0, s[12:13]
	s_mov_b32 m0, s42
	ds_read_b128 v[192:195], v191 offset:49152
	ds_read_b128 v[196:199], v191 offset:50176
	ds_read_b128 v[200:203], v191 offset:51200
	ds_read_b128 v[204:207], v191 offset:52224
	ds_read_b128 v[208:211], v191 offset:53248
	ds_read_b128 v[212:215], v191 offset:54272
	ds_read_b128 v[216:219], v191 offset:55296
	ds_read_b128 v[220:223], v191 offset:56320
	global_load_lds_dwordx4 v[178:179], off
	s_add_i32 m0, s42, 0x2000
	s_add_u32 s40, s40, 0x80080
	v_lshl_add_u64 v[178:179], v[180:181], 0, s[12:13]
	s_addc_u32 s41, s41, 0
	s_add_i32 s42, s65, s3
	global_load_lds_dwordx4 v[178:179], off
	s_mov_b32 m0, s42
	s_nop 0
	global_load_lds_dwordx4 v166, s[40:41]
	s_add_i32 m0, s42, 0x2000
	s_nop 0
	global_load_lds_dwordx4 v162, s[40:41]
	v_lshl_add_u64 v[178:179], v[182:183], 0, s[12:13]
	s_mov_b32 m0, s51
	s_nop 0
	global_load_lds_dwordx4 v[178:179], off
	v_lshl_add_u64 v[178:179], v[184:185], 0, s[12:13]
	s_mov_b32 m0, s58
	s_nop 0
	global_load_lds_dwordx4 v[178:179], off
	s_waitcnt vmcnt(8) lgkmcnt(0)
	s_barrier
	v_mfma_f32_16x16x128_f8f6f4 v[66:69], v[2:9], v[208:215], v[66:69]
	v_mfma_f32_16x16x128_f8f6f4 v[58:61], v[10:17], v[208:215], v[58:61]
	v_mfma_f32_16x16x128_f8f6f4 v[90:93], v[10:17], v[192:199], v[90:93]
	v_mfma_f32_16x16x128_f8f6f4 v[94:97], v[2:9], v[192:199], v[94:97]
	v_mfma_f32_16x16x128_f8f6f4 v[82:85], v[2:9], v[200:207], v[82:85]
	v_mfma_f32_16x16x128_f8f6f4 v[74:77], v[10:17], v[200:207], v[74:77]
	v_mfma_f32_16x16x128_f8f6f4 v[42:45], v[10:17], v[216:223], v[42:45]
	v_mfma_f32_16x16x128_f8f6f4 v[50:53], v[2:9], v[216:223], v[50:53]
	v_mfma_f32_16x16x128_f8f6f4 v[38:41], v[18:25], v[216:223], v[38:41]
	v_mfma_f32_16x16x128_f8f6f4 v[34:37], v[26:33], v[216:223], v[34:37]
	v_mfma_f32_16x16x128_f8f6f4 v[78:81], v[26:33], v[192:199], v[78:81]
	v_mfma_f32_16x16x128_f8f6f4 v[86:89], v[18:25], v[192:199], v[86:89]
	v_mfma_f32_16x16x128_f8f6f4 v[70:73], v[18:25], v[200:207], v[70:73]
	v_mfma_f32_16x16x128_f8f6f4 v[62:65], v[26:33], v[200:207], v[62:65]
	v_mfma_f32_16x16x128_f8f6f4 v[46:49], v[26:33], v[208:215], v[46:49]
	v_mfma_f32_16x16x128_f8f6f4 v[54:57], v[18:25], v[208:215], v[54:57]
	s_barrier
	s_add_i32 s72, s72, 2
	s_add_u32 s38, s38, 0x100
	s_addc_u32 s39, s39, 0
	s_add_u32 s70, s70, 0x100
	s_addc_u32 s71, s71, 0
	s_cmp_gt_u32 s72, 29
	s_cbranch_scc0 .LBB0_1309
	s_and_b64 vcc, exec, s[14:15]
	s_cbranch_vccz .LBB0_1312
	s_barrier

.LBB0_1437:
	v_and_b32_e32 v188, 15, v189
	v_and_b32_e32 v2, 48, v189
	v_lshlrev_b32_e32 v3, 2, v189
	s_and_b32 s8, s6, 3
	s_lshl_b32 s9, s7, 13
	v_lshl_or_b32 v2, v188, 6, v2
	v_and_b32_e32 v3, 32, v3
	v_bitop3_b32 v4, v2, s9, v3 bitop3:0xde
	s_lshl_b32 s9, s8, 12
	v_lshl_add_u64 v[180:181], s[20:21], 0, v[154:155]
	v_bitop3_b32 v2, v2, s9, v3 bitop3:0xde
	s_add_i32 s9, s60, s72
	v_lshl_add_u64 v[178:179], s[20:21], 0, v[182:183]
	v_lshl_add_u64 v[72:73], v[180:181], 0, s[36:37]
	s_mov_b32 m0, s9
	s_add_i32 s19, s9, 0x2000
	s_waitcnt vmcnt(2)
	s_barrier
	global_load_lds_dwordx4 v[72:73], off
	v_lshl_add_u64 v[158:159], v[178:179], 0, s[36:37]
	s_mov_b32 m0, s19
	s_add_i32 s18, s67, 0x8000
	global_load_lds_dwordx4 v[158:159], off
	v_lshl_add_u64 v[70:71], v[172:173], 0, s[36:37]
	s_mov_b32 m0, s18
	s_add_i32 s43, s67, 0xa000
	global_load_lds_dwordx4 v[70:71], off
	v_lshl_add_u64 v[160:161], v[170:171], 0, s[36:37]
	s_mov_b32 m0, s43
	s_add_i32 s44, s61, s72
	global_load_lds_dwordx4 v[160:161], off
	v_lshl_add_u64 v[162:163], s[24:25], 0, v[154:155]
	s_mov_b32 m0, s44
	s_add_i32 s45, s44, 0x2000
	global_load_lds_dwordx4 v[162:163], off
	v_lshl_add_u64 v[164:165], s[24:25], 0, v[182:183]
	s_mov_b32 m0, s45
	s_add_i32 s73, 0, 0x10000
	global_load_lds_dwordx4 v[164:165], off
	v_add_u32_e32 v195, s73, v2
	s_add_i32 s75, 0, 0x14000
	s_waitcnt vmcnt(6)
	s_barrier
	v_add_u32_e32 v194, s75, v2
	v_add_u32_e32 v191, 0, v4
	v_add_u32_e32 v193, s60, v2
	v_add_u32_e32 v192, s61, v2
	ds_read_b128 v[54:57], v195
	ds_read_b128 v[58:61], v195 offset:1024
	ds_read_b128 v[196:199], v195 offset:2048
	ds_read_b128 v[200:203], v195 offset:3072
	ds_read_b128 v[10:13], v194
	ds_read_b128 v[14:17], v194 offset:1024
	ds_read_b128 v[2:5], v194 offset:2048
	ds_read_b128 v[6:9], v194 offset:3072
	s_lshl_b32 s66, s7, 6
	v_lshl_add_u64 v[176:177], s[22:23], 0, v[154:155]
	v_lshl_add_u64 v[174:175], s[22:23], 0, v[182:183]
	s_add_u32 s70, s4, 0x10080
	s_addc_u32 s71, s5, 0
	s_add_i32 s74, s67, 0xc000
	v_lshl_add_u64 v[30:31], s[70:71], 0, v[154:155]
	s_mov_b32 m0, s74
	s_add_i32 s69, s67, 0xe000
	ds_read_b128 v[22:25], v191
	ds_read_b128 v[26:29], v191 offset:1024
	ds_read_b128 v[34:37], v191 offset:2048
	ds_read_b128 v[38:41], v191 offset:3072
	ds_read_b128 v[82:85], v191 offset:4096
	ds_read_b128 v[86:89], v191 offset:5120
	ds_read_b128 v[94:97], v191 offset:6144
	ds_read_b128 v[98:101], v191 offset:7168
	global_load_lds_dwordx4 v[30:31], off
	v_lshl_add_u64 v[30:31], s[70:71], 0, v[182:183]
	s_mov_b32 m0, s69
	s_nop 0
	global_load_lds_dwordx4 v[30:31], off
	s_waitcnt vmcnt(8) lgkmcnt(0)
	s_barrier
	v_mov_b64_e32 v[32:33], v[20:21]
	v_mov_b64_e32 v[152:153], v[20:21]
	v_mov_b64_e32 v[92:93], v[20:21]
	v_mov_b64_e32 v[44:45], v[20:21]
	v_mov_b64_e32 v[116:117], v[20:21]
	v_mov_b64_e32 v[64:65], v[20:21]
	v_mov_b64_e32 v[80:81], v[20:21]
	v_mov_b64_e32 v[52:53], v[20:21]
	v_mov_b64_e32 v[30:31], v[18:19]
	v_mov_b64_e32 v[150:151], v[18:19]
	v_mov_b64_e32 v[90:91], v[18:19]
	v_mov_b64_e32 v[42:43], v[18:19]
	v_mov_b64_e32 v[114:115], v[18:19]
	v_mov_b64_e32 v[62:63], v[18:19]
	v_mov_b64_e32 v[78:79], v[18:19]
	v_mov_b64_e32 v[50:51], v[18:19]
	s_waitcnt lgkmcnt(0)
	v_mfma_f32_16x16x128_f8f6f4 v[30:33], v[54:61], v[22:29], v[30:33]
	v_mfma_f32_16x16x128_f8f6f4 v[150:153], v[196:203], v[22:29], v[150:153]
	v_mfma_f32_16x16x128_f8f6f4 v[42:45], v[196:203], v[34:41], v[42:45]
	v_mfma_f32_16x16x128_f8f6f4 v[90:93], v[54:61], v[34:41], v[90:93]
	v_mfma_f32_16x16x128_f8f6f4 v[114:117], v[54:61], v[82:89], v[114:117]
	v_mfma_f32_16x16x128_f8f6f4 v[62:65], v[196:203], v[82:89], v[62:65]
	v_mfma_f32_16x16x128_f8f6f4 v[50:53], v[196:203], v[94:101], v[50:53]
	v_mfma_f32_16x16x128_f8f6f4 v[78:81], v[54:61], v[94:101], v[78:81]
	v_mov_b64_e32 v[144:145], v[20:21]
	v_mov_b64_e32 v[148:149], v[20:21]
	v_mov_b64_e32 v[142:143], v[18:19]
	v_mov_b64_e32 v[146:147], v[18:19]
	v_mfma_f32_16x16x128_f8f6f4 v[142:145], v[10:17], v[22:29], v[142:145]
	v_mfma_f32_16x16x128_f8f6f4 v[146:149], v[2:9], v[22:29], v[146:149]
	v_mov_b64_e32 v[28:29], v[20:21]
	v_mov_b64_e32 v[140:141], v[20:21]
	v_mov_b64_e32 v[26:27], v[18:19]
	v_mov_b64_e32 v[138:139], v[18:19]
	v_mfma_f32_16x16x128_f8f6f4 v[26:29], v[10:17], v[34:41], v[26:29]
	v_mfma_f32_16x16x128_f8f6f4 v[138:141], v[2:9], v[34:41], v[138:141]
	v_mov_b64_e32 v[40:41], v[20:21]
	v_mov_b64_e32 v[128:129], v[20:21]
	v_mov_b64_e32 v[24:25], v[20:21]
	v_mov_b64_e32 v[76:77], v[20:21]
	v_mov_b64_e32 v[38:39], v[18:19]
	v_mov_b64_e32 v[126:127], v[18:19]
	v_mov_b64_e32 v[22:23], v[18:19]
	v_mov_b64_e32 v[74:75], v[18:19]
	v_mfma_f32_16x16x128_f8f6f4 v[38:41], v[10:17], v[82:89], v[38:41]
	v_mfma_f32_16x16x128_f8f6f4 v[126:129], v[2:9], v[82:89], v[126:129]
	v_mfma_f32_16x16x128_f8f6f4 v[22:25], v[10:17], v[94:101], v[22:25]
	v_mfma_f32_16x16x128_f8f6f4 v[74:77], v[2:9], v[94:101], v[74:77]
	s_barrier
	s_add_i32 s70, s73, s72
	v_lshl_add_u64 v[34:35], v[180:181], 0, s[14:15]
	s_mov_b32 m0, s70
	s_add_i32 s71, s70, 0x2000
	ds_read_b128 v[204:207], v191 offset:16384
	ds_read_b128 v[208:211], v191 offset:17408
	ds_read_b128 v[212:215], v191 offset:18432
	ds_read_b128 v[216:219], v191 offset:19456
	ds_read_b128 v[220:223], v191 offset:20480
	ds_read_b128 v[224:227], v191 offset:21504
	ds_read_b128 v[228:231], v191 offset:22528
	ds_read_b128 v[232:235], v191 offset:23552
	global_load_lds_dwordx4 v[34:35], off
	v_lshl_add_u64 v[34:35], v[178:179], 0, s[14:15]
	s_mov_b32 m0, s71
	s_add_i32 s72, s75, s72
	global_load_lds_dwordx4 v[34:35], off
	v_lshl_add_u64 v[34:35], s[26:27], 0, v[154:155]
	s_mov_b32 m0, s72
	s_add_i32 s73, s72, 0x2000
	global_load_lds_dwordx4 v[34:35], off
	v_lshl_add_u64 v[34:35], s[26:27], 0, v[182:183]
	s_mov_b32 m0, s73
	s_nop 0
	global_load_lds_dwordx4 v[34:35], off
	v_lshl_add_u64 v[34:35], v[172:173], 0, s[14:15]
	s_mov_b32 m0, s67
	s_nop 0
	global_load_lds_dwordx4 v[34:35], off
	v_lshl_add_u64 v[34:35], v[170:171], 0, s[14:15]
	s_mov_b32 m0, s68
	s_nop 0
	global_load_lds_dwordx4 v[34:35], off
	s_waitcnt vmcnt(8) lgkmcnt(0)
	s_barrier
	v_mov_b64_e32 v[136:137], v[20:21]
	v_mov_b64_e32 v[104:105], v[20:21]
	v_mov_b64_e32 v[124:125], v[20:21]
	v_mov_b64_e32 v[100:101], v[20:21]
	v_mov_b64_e32 v[112:113], v[20:21]
	v_mov_b64_e32 v[108:109], v[20:21]
	v_mov_b64_e32 v[88:89], v[20:21]
	v_mov_b64_e32 v[84:85], v[20:21]
	v_mov_b64_e32 v[134:135], v[18:19]
	v_mov_b64_e32 v[102:103], v[18:19]
	v_mov_b64_e32 v[122:123], v[18:19]
	v_mov_b64_e32 v[98:99], v[18:19]
	v_mov_b64_e32 v[110:111], v[18:19]
	v_mov_b64_e32 v[106:107], v[18:19]
	v_mov_b64_e32 v[86:87], v[18:19]
	v_mov_b64_e32 v[82:83], v[18:19]
	s_waitcnt lgkmcnt(0)
	v_mfma_f32_16x16x128_f8f6f4 v[134:137], v[54:61], v[204:211], v[134:137]
	v_mfma_f32_16x16x128_f8f6f4 v[102:105], v[196:203], v[204:211], v[102:105]
	v_mfma_f32_16x16x128_f8f6f4 v[98:101], v[196:203], v[212:219], v[98:101]
	v_mfma_f32_16x16x128_f8f6f4 v[122:125], v[54:61], v[212:219], v[122:125]
	v_mfma_f32_16x16x128_f8f6f4 v[110:113], v[54:61], v[220:227], v[110:113]
	v_mfma_f32_16x16x128_f8f6f4 v[106:109], v[196:203], v[220:227], v[106:109]
	v_mfma_f32_16x16x128_f8f6f4 v[82:85], v[196:203], v[228:235], v[82:85]
	v_mfma_f32_16x16x128_f8f6f4 v[86:89], v[54:61], v[228:235], v[86:89]
	v_mov_b64_e32 v[36:37], v[20:21]
	v_mov_b64_e32 v[132:133], v[20:21]
	v_mov_b64_e32 v[48:49], v[20:21]
	v_mov_b64_e32 v[120:121], v[20:21]
	v_mov_b64_e32 v[68:69], v[20:21]
	v_mov_b64_e32 v[96:97], v[20:21]
	v_mov_b64_e32 v[56:57], v[20:21]
	v_mov_b64_e32 v[60:61], v[20:21]
	v_mov_b64_e32 v[34:35], v[18:19]
	v_mov_b64_e32 v[130:131], v[18:19]
	v_mov_b64_e32 v[46:47], v[18:19]
	v_mov_b64_e32 v[118:119], v[18:19]
	v_mov_b64_e32 v[66:67], v[18:19]
	v_mov_b64_e32 v[94:95], v[18:19]
	v_mov_b64_e32 v[54:55], v[18:19]
	v_mov_b64_e32 v[58:59], v[18:19]
	v_mfma_f32_16x16x128_f8f6f4 v[54:57], v[10:17], v[228:235], v[54:57]
	v_mfma_f32_16x16x128_f8f6f4 v[58:61], v[2:9], v[228:235], v[58:61]
	v_mfma_f32_16x16x128_f8f6f4 v[130:133], v[2:9], v[204:211], v[130:133]
	v_mfma_f32_16x16x128_f8f6f4 v[34:37], v[10:17], v[204:211], v[34:37]
	v_mfma_f32_16x16x128_f8f6f4 v[46:49], v[10:17], v[212:219], v[46:49]
	v_mfma_f32_16x16x128_f8f6f4 v[118:121], v[2:9], v[212:219], v[118:121]
	v_mfma_f32_16x16x128_f8f6f4 v[94:97], v[2:9], v[220:227], v[94:97]
	v_mfma_f32_16x16x128_f8f6f4 v[66:69], v[10:17], v[220:227], v[66:69]
	s_barrier
	ds_read_b128 v[2:5], v193
	ds_read_b128 v[6:9], v193 offset:1024
	ds_read_b128 v[10:13], v193 offset:2048
	ds_read_b128 v[14:17], v193 offset:3072
	ds_read_b128 v[196:199], v192
	ds_read_b128 v[200:203], v192 offset:1024
	ds_read_b128 v[204:207], v192 offset:2048
	ds_read_b128 v[208:211], v192 offset:3072
	s_add_u32 s76, s4, 0x10100
	s_addc_u32 s77, s5, 0
	s_mov_b32 m0, s48
	v_lshl_add_u64 v[244:245], s[76:77], 0, v[154:155]
	ds_read_b128 v[212:215], v191 offset:32768
	ds_read_b128 v[216:219], v191 offset:33792
	ds_read_b128 v[220:223], v191 offset:34816
	ds_read_b128 v[224:227], v191 offset:35840
	ds_read_b128 v[228:231], v191 offset:36864
	ds_read_b128 v[232:235], v191 offset:37888
	ds_read_b128 v[236:239], v191 offset:38912
	ds_read_b128 v[240:243], v191 offset:39936
	global_load_lds_dwordx4 v[244:245], off
	v_lshl_add_u64 v[244:245], s[76:77], 0, v[182:183]
	s_mov_b32 m0, s49
	s_nop 0
	global_load_lds_dwordx4 v[244:245], off
	s_waitcnt vmcnt(8) lgkmcnt(0)
	s_barrier
	v_mfma_f32_16x16x128_f8f6f4 v[42:45], v[10:17], v[220:227], v[42:45]
	v_mfma_f32_16x16x128_f8f6f4 v[90:93], v[2:9], v[220:227], v[90:93]
	v_mfma_f32_16x16x128_f8f6f4 v[30:33], v[2:9], v[212:219], v[30:33]
	v_mfma_f32_16x16x128_f8f6f4 v[150:153], v[10:17], v[212:219], v[150:153]
	v_mfma_f32_16x16x128_f8f6f4 v[62:65], v[10:17], v[228:235], v[62:65]
	v_mfma_f32_16x16x128_f8f6f4 v[114:117], v[2:9], v[228:235], v[114:117]
	v_mfma_f32_16x16x128_f8f6f4 v[78:81], v[2:9], v[236:243], v[78:81]
	v_mfma_f32_16x16x128_f8f6f4 v[50:53], v[10:17], v[236:243], v[50:53]
	v_mfma_f32_16x16x128_f8f6f4 v[22:25], v[196:203], v[236:243], v[22:25]
	v_mfma_f32_16x16x128_f8f6f4 v[74:77], v[204:211], v[236:243], v[74:77]
	v_mfma_f32_16x16x128_f8f6f4 v[146:149], v[204:211], v[212:219], v[146:149]
	v_mfma_f32_16x16x128_f8f6f4 v[142:145], v[196:203], v[212:219], v[142:145]
	v_mfma_f32_16x16x128_f8f6f4 v[26:29], v[196:203], v[220:227], v[26:29]
	v_mfma_f32_16x16x128_f8f6f4 v[138:141], v[204:211], v[220:227], v[138:141]
	v_mfma_f32_16x16x128_f8f6f4 v[126:129], v[204:211], v[228:235], v[126:129]
	v_mfma_f32_16x16x128_f8f6f4 v[38:41], v[196:203], v[228:235], v[38:41]
	s_barrier
	s_mov_b32 m0, s9
	v_lshl_add_u64 v[244:245], v[180:181], 0, s[38:39]
	ds_read_b128 v[212:215], v191 offset:49152
	ds_read_b128 v[216:219], v191 offset:50176
	ds_read_b128 v[220:223], v191 offset:51200
	ds_read_b128 v[224:227], v191 offset:52224
	ds_read_b128 v[228:231], v191 offset:53248
	ds_read_b128 v[232:235], v191 offset:54272
	ds_read_b128 v[236:239], v191 offset:55296
	ds_read_b128 v[240:243], v191 offset:56320
	global_load_lds_dwordx4 v[244:245], off
	v_lshl_add_u64 v[244:245], v[178:179], 0, s[38:39]
	s_mov_b32 m0, s19
	s_nop 0
	global_load_lds_dwordx4 v[244:245], off
	v_lshl_add_u64 v[244:245], s[28:29], 0, v[154:155]
	s_mov_b32 m0, s44
	s_nop 0
	global_load_lds_dwordx4 v[244:245], off
	v_lshl_add_u64 v[244:245], s[28:29], 0, v[182:183]
	s_mov_b32 m0, s45
	s_nop 0
	global_load_lds_dwordx4 v[244:245], off
	v_lshl_add_u64 v[244:245], v[172:173], 0, s[38:39]
	s_mov_b32 m0, s18
	s_nop 0
	global_load_lds_dwordx4 v[244:245], off
	v_lshl_add_u64 v[244:245], v[170:171], 0, s[38:39]
	s_mov_b32 m0, s43
	s_nop 0
	global_load_lds_dwordx4 v[244:245], off
	s_waitcnt vmcnt(8) lgkmcnt(0)
	s_barrier
	v_mfma_f32_16x16x128_f8f6f4 v[110:113], v[2:9], v[228:235], v[110:113]
	v_mfma_f32_16x16x128_f8f6f4 v[106:109], v[10:17], v[228:235], v[106:109]
	v_mfma_f32_16x16x128_f8f6f4 v[102:105], v[10:17], v[212:219], v[102:105]
	v_mfma_f32_16x16x128_f8f6f4 v[134:137], v[2:9], v[212:219], v[134:137]
	v_mfma_f32_16x16x128_f8f6f4 v[122:125], v[2:9], v[220:227], v[122:125]
	v_mfma_f32_16x16x128_f8f6f4 v[98:101], v[10:17], v[220:227], v[98:101]
	v_mfma_f32_16x16x128_f8f6f4 v[82:85], v[10:17], v[236:243], v[82:85]
	v_mfma_f32_16x16x128_f8f6f4 v[86:89], v[2:9], v[236:243], v[86:89]
	v_mfma_f32_16x16x128_f8f6f4 v[54:57], v[196:203], v[236:243], v[54:57]
	v_mfma_f32_16x16x128_f8f6f4 v[58:61], v[204:211], v[236:243], v[58:61]
	v_mfma_f32_16x16x128_f8f6f4 v[130:133], v[204:211], v[212:219], v[130:133]
	v_mfma_f32_16x16x128_f8f6f4 v[34:37], v[196:203], v[212:219], v[34:37]
	v_mfma_f32_16x16x128_f8f6f4 v[46:49], v[196:203], v[220:227], v[46:49]
	v_mfma_f32_16x16x128_f8f6f4 v[118:121], v[204:211], v[220:227], v[118:121]
	v_mfma_f32_16x16x128_f8f6f4 v[94:97], v[204:211], v[228:235], v[94:97]
	v_mfma_f32_16x16x128_f8f6f4 v[66:69], v[196:203], v[228:235], v[66:69]
	s_barrier
	ds_read_b128 v[2:5], v195
	ds_read_b128 v[6:9], v195 offset:1024
	ds_read_b128 v[10:13], v195 offset:2048
	ds_read_b128 v[14:17], v195 offset:3072
	ds_read_b128 v[196:199], v194
	ds_read_b128 v[200:203], v194 offset:1024
	ds_read_b128 v[204:207], v194 offset:2048
	ds_read_b128 v[208:211], v194 offset:3072
	s_add_u32 s4, s4, 0x10180
	s_addc_u32 s5, s5, 0
	s_mov_b32 m0, s74
	v_lshl_add_u64 v[194:195], s[4:5], 0, v[154:155]
	ds_read_b128 v[212:215], v191
	ds_read_b128 v[216:219], v191 offset:1024
	ds_read_b128 v[220:223], v191 offset:2048
	ds_read_b128 v[224:227], v191 offset:3072
	ds_read_b128 v[228:231], v191 offset:4096
	ds_read_b128 v[232:235], v191 offset:5120
	ds_read_b128 v[236:239], v191 offset:6144
	ds_read_b128 v[240:243], v191 offset:7168
	global_load_lds_dwordx4 v[194:195], off
	v_lshl_add_u64 v[182:183], s[4:5], 0, v[182:183]
	s_mov_b32 m0, s69
	s_nop 0
	global_load_lds_dwordx4 v[182:183], off
	s_waitcnt vmcnt(8) lgkmcnt(0)
	s_barrier
	v_mfma_f32_16x16x128_f8f6f4 v[114:117], v[2:9], v[228:235], v[114:117]
	v_mfma_f32_16x16x128_f8f6f4 v[62:65], v[10:17], v[228:235], v[62:65]
	v_mfma_f32_16x16x128_f8f6f4 v[150:153], v[10:17], v[212:219], v[150:153]
	v_mfma_f32_16x16x128_f8f6f4 v[30:33], v[2:9], v[212:219], v[30:33]
	v_mfma_f32_16x16x128_f8f6f4 v[90:93], v[2:9], v[220:227], v[90:93]
	v_mfma_f32_16x16x128_f8f6f4 v[42:45], v[10:17], v[220:227], v[42:45]
	v_mfma_f32_16x16x128_f8f6f4 v[50:53], v[10:17], v[236:243], v[50:53]
	v_mfma_f32_16x16x128_f8f6f4 v[78:81], v[2:9], v[236:243], v[78:81]
	v_mfma_f32_16x16x128_f8f6f4 v[22:25], v[196:203], v[236:243], v[22:25]
	v_mfma_f32_16x16x128_f8f6f4 v[74:77], v[204:211], v[236:243], v[74:77]
	v_mfma_f32_16x16x128_f8f6f4 v[146:149], v[204:211], v[212:219], v[146:149]
	v_mfma_f32_16x16x128_f8f6f4 v[142:145], v[196:203], v[212:219], v[142:145]
	v_mfma_f32_16x16x128_f8f6f4 v[26:29], v[196:203], v[220:227], v[26:29]
	v_mfma_f32_16x16x128_f8f6f4 v[138:141], v[204:211], v[220:227], v[138:141]
	v_mfma_f32_16x16x128_f8f6f4 v[126:129], v[204:211], v[228:235], v[126:129]
	v_mfma_f32_16x16x128_f8f6f4 v[38:41], v[196:203], v[228:235], v[38:41]
	s_barrier
	s_mov_b32 m0, s70
	ds_read_b128 v[212:215], v191 offset:16384
	ds_read_b128 v[216:219], v191 offset:17408
	ds_read_b128 v[220:223], v191 offset:18432
	ds_read_b128 v[224:227], v191 offset:19456
	ds_read_b128 v[228:231], v191 offset:20480
	ds_read_b128 v[232:235], v191 offset:21504
	ds_read_b128 v[236:239], v191 offset:22528
	ds_read_b128 v[240:243], v191 offset:23552
	global_load_lds_dwordx4 v[180:181], off
	s_mov_b32 m0, s71
	s_nop 0
	global_load_lds_dwordx4 v[178:179], off
	s_mov_b32 m0, s72
	s_nop 0
	global_load_lds_dwordx4 v[176:177], off
	s_mov_b32 m0, s73
	s_nop 0
	global_load_lds_dwordx4 v[174:175], off
	s_mov_b32 m0, s67
	s_nop 0
	global_load_lds_dwordx4 v[172:173], off
	s_mov_b32 m0, s68
	s_nop 0
	global_load_lds_dwordx4 v[170:171], off
	s_waitcnt vmcnt(8) lgkmcnt(0)
	s_barrier
	v_mfma_f32_16x16x128_f8f6f4 v[110:113], v[2:9], v[228:235], v[110:113]
	v_mfma_f32_16x16x128_f8f6f4 v[106:109], v[10:17], v[228:235], v[106:109]
	v_mfma_f32_16x16x128_f8f6f4 v[102:105], v[10:17], v[212:219], v[102:105]
	v_mfma_f32_16x16x128_f8f6f4 v[134:137], v[2:9], v[212:219], v[134:137]
	v_mfma_f32_16x16x128_f8f6f4 v[122:125], v[2:9], v[220:227], v[122:125]
	v_mfma_f32_16x16x128_f8f6f4 v[98:101], v[10:17], v[220:227], v[98:101]
	v_mfma_f32_16x16x128_f8f6f4 v[82:85], v[10:17], v[236:243], v[82:85]
	v_mfma_f32_16x16x128_f8f6f4 v[86:89], v[2:9], v[236:243], v[86:89]
	v_mfma_f32_16x16x128_f8f6f4 v[54:57], v[196:203], v[236:243], v[54:57]
	v_mfma_f32_16x16x128_f8f6f4 v[58:61], v[204:211], v[236:243], v[58:61]
	v_mfma_f32_16x16x128_f8f6f4 v[130:133], v[204:211], v[212:219], v[130:133]
	v_mfma_f32_16x16x128_f8f6f4 v[34:37], v[196:203], v[212:219], v[34:37]
	v_mfma_f32_16x16x128_f8f6f4 v[46:49], v[196:203], v[220:227], v[46:49]
	v_mfma_f32_16x16x128_f8f6f4 v[118:121], v[204:211], v[220:227], v[118:121]
	v_mfma_f32_16x16x128_f8f6f4 v[94:97], v[204:211], v[228:235], v[94:97]
	v_mfma_f32_16x16x128_f8f6f4 v[66:69], v[196:203], v[228:235], v[66:69]
	s_barrier
	ds_read_b128 v[2:5], v193
	ds_read_b128 v[6:9], v193 offset:1024
	ds_read_b128 v[10:13], v193 offset:2048
	ds_read_b128 v[14:17], v193 offset:3072
	ds_read_b128 v[170:173], v192
	ds_read_b128 v[174:177], v192 offset:1024
	ds_read_b128 v[194:197], v192 offset:2048
	ds_read_b128 v[198:201], v192 offset:3072
	s_mov_b32 m0, s48
	ds_read_b128 v[202:205], v191 offset:32768
	ds_read_b128 v[206:209], v191 offset:33792
	ds_read_b128 v[210:213], v191 offset:34816
	ds_read_b128 v[214:217], v191 offset:35840
	ds_read_b128 v[218:221], v191 offset:36864
	ds_read_b128 v[222:225], v191 offset:37888
	ds_read_b128 v[226:229], v191 offset:38912
	ds_read_b128 v[230:233], v191 offset:39936
	global_load_lds_dwordx4 v[166:167], off
	s_mov_b32 m0, s49
	s_nop 0
	global_load_lds_dwordx4 v[168:169], off
	s_waitcnt vmcnt(8) lgkmcnt(0)
	s_barrier
	v_mfma_f32_16x16x128_f8f6f4 v[30:33], v[2:9], v[202:209], v[30:33]
	v_mfma_f32_16x16x128_f8f6f4 v[150:153], v[10:17], v[202:209], v[150:153]
	v_mfma_f32_16x16x128_f8f6f4 v[42:45], v[10:17], v[210:217], v[42:45]
	v_mfma_f32_16x16x128_f8f6f4 v[90:93], v[2:9], v[210:217], v[90:93]
	v_mfma_f32_16x16x128_f8f6f4 v[114:117], v[2:9], v[218:225], v[114:117]
	v_mfma_f32_16x16x128_f8f6f4 v[62:65], v[10:17], v[218:225], v[62:65]
	v_mfma_f32_16x16x128_f8f6f4 v[50:53], v[10:17], v[226:233], v[50:53]
	v_mfma_f32_16x16x128_f8f6f4 v[78:81], v[2:9], v[226:233], v[78:81]
	v_mfma_f32_16x16x128_f8f6f4 v[22:25], v[170:177], v[226:233], v[22:25]
	v_mfma_f32_16x16x128_f8f6f4 v[74:77], v[194:201], v[226:233], v[74:77]
	v_mfma_f32_16x16x128_f8f6f4 v[146:149], v[194:201], v[202:209], v[146:149]
	v_mfma_f32_16x16x128_f8f6f4 v[142:145], v[170:177], v[202:209], v[142:145]
	v_mfma_f32_16x16x128_f8f6f4 v[26:29], v[170:177], v[210:217], v[26:29]
	v_mfma_f32_16x16x128_f8f6f4 v[138:141], v[194:201], v[210:217], v[138:141]
	v_mfma_f32_16x16x128_f8f6f4 v[126:129], v[194:201], v[218:225], v[126:129]
	v_mfma_f32_16x16x128_f8f6f4 v[38:41], v[170:177], v[218:225], v[38:41]
	s_barrier
	s_mov_b32 m0, s9
	ds_read_b128 v[202:205], v191 offset:49152
	ds_read_b128 v[206:209], v191 offset:50176
	ds_read_b128 v[210:213], v191 offset:51200
	ds_read_b128 v[214:217], v191 offset:52224
	ds_read_b128 v[218:221], v191 offset:53248
	ds_read_b128 v[222:225], v191 offset:54272
	ds_read_b128 v[226:229], v191 offset:55296
	ds_read_b128 v[230:233], v191 offset:56320
	global_load_lds_dwordx4 v[72:73], off
	s_mov_b32 m0, s19
	s_nop 0
	global_load_lds_dwordx4 v[158:159], off
	s_mov_b32 m0, s44
	s_nop 0
	global_load_lds_dwordx4 v[162:163], off
	s_mov_b32 m0, s45
	s_nop 0
	global_load_lds_dwordx4 v[164:165], off
	s_mov_b32 m0, s18
	s_nop 0
	global_load_lds_dwordx4 v[70:71], off
	s_mov_b32 m0, s43
	s_nop 0
	global_load_lds_dwordx4 v[160:161], off
	s_waitcnt vmcnt(8) lgkmcnt(0)
	s_barrier
	v_mfma_f32_16x16x128_f8f6f4 v[110:113], v[2:9], v[218:225], v[110:113]
	v_mfma_f32_16x16x128_f8f6f4 v[106:109], v[10:17], v[218:225], v[106:109]
	v_mfma_f32_16x16x128_f8f6f4 v[102:105], v[10:17], v[202:209], v[102:105]
	v_mfma_f32_16x16x128_f8f6f4 v[134:137], v[2:9], v[202:209], v[134:137]
	v_mfma_f32_16x16x128_f8f6f4 v[122:125], v[2:9], v[210:217], v[122:125]
	v_mfma_f32_16x16x128_f8f6f4 v[98:101], v[10:17], v[210:217], v[98:101]
	v_mfma_f32_16x16x128_f8f6f4 v[82:85], v[10:17], v[226:233], v[82:85]
	v_mfma_f32_16x16x128_f8f6f4 v[86:89], v[2:9], v[226:233], v[86:89]
	v_mfma_f32_16x16x128_f8f6f4 v[54:57], v[170:177], v[226:233], v[54:57]
	v_mfma_f32_16x16x128_f8f6f4 v[58:61], v[194:201], v[226:233], v[58:61]
	v_mfma_f32_16x16x128_f8f6f4 v[130:133], v[194:201], v[202:209], v[130:133]
	v_mfma_f32_16x16x128_f8f6f4 v[34:37], v[170:177], v[202:209], v[34:37]
	v_mfma_f32_16x16x128_f8f6f4 v[46:49], v[170:177], v[210:217], v[46:49]
	v_mfma_f32_16x16x128_f8f6f4 v[118:121], v[194:201], v[210:217], v[118:121]
	v_mfma_f32_16x16x128_f8f6f4 v[94:97], v[194:201], v[218:225], v[94:97]
	v_mfma_f32_16x16x128_f8f6f4 v[66:69], v[170:177], v[218:225], v[66:69]
	s_barrier
	s_waitcnt vmcnt(0)
	s_cmpk_gt_u32 s65, 0xff
	s_cbranch_scc1 .LBB0_1439
	s_barrier

.LBB0_1558:
	s_add_u32 s39, s30, s38
	s_addc_u32 s44, s31, 0
	s_add_u32 s42, s39, 0x100
	s_addc_u32 s43, s44, 0
	s_and_b64 s[40:41], s[36:37], exec
	s_cselect_b32 s41, s18, s43
	s_cselect_b32 s40, s19, s42
	s_add_u32 s38, s28, s38
	s_addc_u32 s42, s29, 0
	s_add_u32 s38, s38, 0x100
	s_addc_u32 s42, s42, 0
	s_and_b64 s[36:37], s[36:37], exec
	s_cselect_b32 s43, s17, s42
	s_cselect_b32 s42, s21, s38
	s_add_u32 s76, s39, 0x10080
	ds_read_b128 v[26:29], v181
	ds_read_b128 v[30:33], v181 offset:1024
	ds_read_b128 v[18:21], v181 offset:2048
	ds_read_b128 v[22:25], v181 offset:3072
	ds_read_b128 v[10:13], v182
	ds_read_b128 v[14:17], v182 offset:1024
	ds_read_b128 v[2:5], v182 offset:2048
	ds_read_b128 v[6:9], v182 offset:3072
	s_addc_u32 s77, s44, 0
	s_add_i32 s75, s63, s15
	s_add_i32 m0, s27, 0xc000
	s_add_i32 s78, s27, 0xe000
	s_add_i32 s72, s75, 0x2000
	s_add_u32 s44, s42, 0x10000
	s_addc_u32 s45, s43, 0
	s_add_i32 s74, s64, s15
	s_add_i32 s73, s74, 0x2000
	s_add_i32 s71, 0, 0x18000
	s_add_i32 s70, 0, 0x1c000
	s_add_u32 s38, s40, 0x10000
	s_addc_u32 s39, s41, 0
	s_add_i32 s69, s71, s15
	s_add_i32 s67, s69, 0x2000
	s_add_u32 s36, s42, 0x10080
	s_addc_u32 s37, s43, 0
	s_add_i32 s68, s70, s15
	s_add_i32 s66, s68, 0x2000
	ds_read_b128 v[170:173], v183
	ds_read_b128 v[174:177], v183 offset:1024
	ds_read_b128 v[184:187], v183 offset:2048
	ds_read_b128 v[188:191], v183 offset:3072
	ds_read_b128 v[192:195], v183 offset:4096
	ds_read_b128 v[196:199], v183 offset:5120
	ds_read_b128 v[200:203], v183 offset:6144
	ds_read_b128 v[204:207], v183 offset:7168
	global_load_lds_dwordx4 v164, s[76:77]
	v_lshl_add_u64 v[208:209], s[76:77], 0, v[162:163]
	s_mov_b32 m0, s78
	s_nop 0
	global_load_lds_dwordx4 v[208:209], off
	s_waitcnt vmcnt(8) lgkmcnt(0)
	s_barrier
	v_mfma_f32_16x16x128_f8f6f4 v[158:161], v[26:33], v[170:177], v[158:161]
	v_mfma_f32_16x16x128_f8f6f4 v[154:157], v[18:25], v[170:177], v[154:157]
	v_mfma_f32_16x16x128_f8f6f4 v[138:141], v[18:25], v[184:191], v[138:141]
	v_mfma_f32_16x16x128_f8f6f4 v[142:145], v[26:33], v[184:191], v[142:145]
	v_mfma_f32_16x16x128_f8f6f4 v[126:129], v[26:33], v[192:199], v[126:129]
	v_mfma_f32_16x16x128_f8f6f4 v[122:125], v[18:25], v[192:199], v[122:125]
	v_mfma_f32_16x16x128_f8f6f4 v[106:109], v[18:25], v[200:207], v[106:109]
	v_mfma_f32_16x16x128_f8f6f4 v[110:113], v[26:33], v[200:207], v[110:113]
	v_mfma_f32_16x16x128_f8f6f4 v[102:105], v[10:17], v[200:207], v[102:105]
	v_mfma_f32_16x16x128_f8f6f4 v[98:101], v[2:9], v[200:207], v[98:101]
	v_mfma_f32_16x16x128_f8f6f4 v[146:149], v[2:9], v[170:177], v[146:149]
	v_mfma_f32_16x16x128_f8f6f4 v[150:153], v[10:17], v[170:177], v[150:153]
	v_mfma_f32_16x16x128_f8f6f4 v[134:137], v[10:17], v[184:191], v[134:137]
	v_mfma_f32_16x16x128_f8f6f4 v[130:133], v[2:9], v[184:191], v[130:133]
	v_mfma_f32_16x16x128_f8f6f4 v[114:117], v[2:9], v[192:199], v[114:117]
	v_mfma_f32_16x16x128_f8f6f4 v[118:121], v[10:17], v[192:199], v[118:121]
	s_barrier
	s_mov_b32 m0, s75
	v_lshl_add_u64 v[170:171], s[42:43], 0, v[164:165]
	ds_read_b128 v[184:187], v183 offset:16384
	ds_read_b128 v[188:191], v183 offset:17408
	ds_read_b128 v[192:195], v183 offset:18432
	ds_read_b128 v[196:199], v183 offset:19456
	ds_read_b128 v[200:203], v183 offset:20480
	ds_read_b128 v[204:207], v183 offset:21504
	ds_read_b128 v[208:211], v183 offset:22528
	ds_read_b128 v[212:215], v183 offset:23552
	global_load_lds_dwordx4 v[170:171], off
	v_lshl_add_u64 v[172:173], s[42:43], 0, v[162:163]
	s_mov_b32 m0, s72
	global_load_lds_dwordx4 v[172:173], off
	s_mov_b32 m0, s74
	v_lshl_add_u64 v[176:177], s[40:41], 0, v[162:163]
	global_load_lds_dwordx4 v164, s[44:45]
	s_mov_b32 m0, s73
	s_nop 0
	global_load_lds_dwordx4 v162, s[44:45]
	v_lshl_add_u64 v[174:175], s[40:41], 0, v[164:165]
	s_mov_b32 m0, s27
	s_nop 0
	global_load_lds_dwordx4 v[174:175], off
	s_mov_b32 m0, s49
	s_nop 0
	global_load_lds_dwordx4 v[176:177], off
	s_waitcnt vmcnt(8) lgkmcnt(0)
	s_barrier
	v_mfma_f32_16x16x128_f8f6f4 v[78:81], v[26:33], v[192:199], v[78:81]
	v_mfma_f32_16x16x128_f8f6f4 v[74:77], v[18:25], v[192:199], v[74:77]
	v_mfma_f32_16x16x128_f8f6f4 v[90:93], v[18:25], v[184:191], v[90:93]
	v_mfma_f32_16x16x128_f8f6f4 v[94:97], v[26:33], v[184:191], v[94:97]
	v_mfma_f32_16x16x128_f8f6f4 v[62:65], v[26:33], v[200:207], v[62:65]
	v_mfma_f32_16x16x128_f8f6f4 v[58:61], v[18:25], v[200:207], v[58:61]
	v_mfma_f32_16x16x128_f8f6f4 v[42:45], v[18:25], v[208:215], v[42:45]
	v_mfma_f32_16x16x128_f8f6f4 v[54:57], v[26:33], v[208:215], v[54:57]
	v_mfma_f32_16x16x128_f8f6f4 v[38:41], v[10:17], v[208:215], v[38:41]
	v_mfma_f32_16x16x128_f8f6f4 v[34:37], v[2:9], v[208:215], v[34:37]
	v_mfma_f32_16x16x128_f8f6f4 v[82:85], v[2:9], v[184:191], v[82:85]
	v_mfma_f32_16x16x128_f8f6f4 v[86:89], v[10:17], v[184:191], v[86:89]
	v_mfma_f32_16x16x128_f8f6f4 v[70:73], v[10:17], v[192:199], v[70:73]
	v_mfma_f32_16x16x128_f8f6f4 v[66:69], v[2:9], v[192:199], v[66:69]
	v_mfma_f32_16x16x128_f8f6f4 v[46:49], v[2:9], v[200:207], v[46:49]
	v_mfma_f32_16x16x128_f8f6f4 v[50:53], v[10:17], v[200:207], v[50:53]
	s_barrier
	v_add_u32_e32 v14, s71, v179
	v_add_u32_e32 v30, s70, v179
	ds_read_b128 v[2:5], v14
	ds_read_b128 v[6:9], v14 offset:1024
	ds_read_b128 v[10:13], v14 offset:2048
	ds_read_b128 v[14:17], v14 offset:3072
	ds_read_b128 v[18:21], v30
	ds_read_b128 v[22:25], v30 offset:1024
	ds_read_b128 v[26:29], v30 offset:2048
	ds_read_b128 v[30:33], v30 offset:3072
	s_mov_b32 m0, s50
	ds_read_b128 v[184:187], v183 offset:32768
	ds_read_b128 v[188:191], v183 offset:33792
	ds_read_b128 v[192:195], v183 offset:34816
	ds_read_b128 v[196:199], v183 offset:35840
	ds_read_b128 v[200:203], v183 offset:36864
	ds_read_b128 v[204:207], v183 offset:37888
	ds_read_b128 v[208:211], v183 offset:38912
	ds_read_b128 v[212:215], v183 offset:39936
	global_load_lds_dwordx4 v164, s[38:39]
	s_mov_b32 m0, s51
	s_nop 0
	global_load_lds_dwordx4 v162, s[38:39]
	s_waitcnt vmcnt(8) lgkmcnt(0)
	s_barrier
	v_mfma_f32_16x16x128_f8f6f4 v[122:125], v[10:17], v[200:207], v[122:125]
	v_mfma_f32_16x16x128_f8f6f4 v[126:129], v[2:9], v[200:207], v[126:129]
	v_mfma_f32_16x16x128_f8f6f4 v[158:161], v[2:9], v[184:191], v[158:161]
	v_mfma_f32_16x16x128_f8f6f4 v[154:157], v[10:17], v[184:191], v[154:157]
	v_mfma_f32_16x16x128_f8f6f4 v[138:141], v[10:17], v[192:199], v[138:141]
	v_mfma_f32_16x16x128_f8f6f4 v[142:145], v[2:9], v[192:199], v[142:145]
	v_mfma_f32_16x16x128_f8f6f4 v[110:113], v[2:9], v[208:215], v[110:113]
	v_mfma_f32_16x16x128_f8f6f4 v[106:109], v[10:17], v[208:215], v[106:109]
	v_mfma_f32_16x16x128_f8f6f4 v[102:105], v[18:25], v[208:215], v[102:105]
	v_mfma_f32_16x16x128_f8f6f4 v[98:101], v[26:33], v[208:215], v[98:101]
	v_mfma_f32_16x16x128_f8f6f4 v[146:149], v[26:33], v[184:191], v[146:149]
	v_mfma_f32_16x16x128_f8f6f4 v[150:153], v[18:25], v[184:191], v[150:153]
	v_mfma_f32_16x16x128_f8f6f4 v[134:137], v[18:25], v[192:199], v[134:137]
	v_mfma_f32_16x16x128_f8f6f4 v[130:133], v[26:33], v[192:199], v[130:133]
	v_mfma_f32_16x16x128_f8f6f4 v[114:117], v[26:33], v[200:207], v[114:117]
	v_mfma_f32_16x16x128_f8f6f4 v[118:121], v[18:25], v[200:207], v[118:121]
	s_barrier
	s_mov_b32 m0, s69
	v_lshl_add_u64 v[170:171], v[170:171], 0, s[8:9]
	ds_read_b128 v[184:187], v183 offset:49152
	ds_read_b128 v[188:191], v183 offset:50176
	ds_read_b128 v[192:195], v183 offset:51200
	ds_read_b128 v[196:199], v183 offset:52224
	ds_read_b128 v[200:203], v183 offset:53248
	ds_read_b128 v[204:207], v183 offset:54272
	ds_read_b128 v[208:211], v183 offset:55296
	ds_read_b128 v[212:215], v183 offset:56320
	global_load_lds_dwordx4 v[170:171], off
	v_lshl_add_u64 v[170:171], v[172:173], 0, s[8:9]
	s_mov_b32 m0, s67
	s_nop 0
	global_load_lds_dwordx4 v[170:171], off
	s_mov_b32 m0, s68
	s_nop 0
	global_load_lds_dwordx4 v164, s[36:37]
	s_mov_b32 m0, s66
	s_nop 0
	global_load_lds_dwordx4 v162, s[36:37]
	v_lshl_add_u64 v[170:171], v[174:175], 0, s[8:9]
	s_mov_b32 m0, s61
	s_nop 0
	global_load_lds_dwordx4 v[170:171], off
	v_lshl_add_u64 v[170:171], v[176:177], 0, s[8:9]
	s_mov_b32 m0, s62
	s_nop 0
	global_load_lds_dwordx4 v[170:171], off
	s_waitcnt vmcnt(8) lgkmcnt(0)
	s_barrier
	v_mfma_f32_16x16x128_f8f6f4 v[62:65], v[2:9], v[200:207], v[62:65]
	v_mfma_f32_16x16x128_f8f6f4 v[58:61], v[10:17], v[200:207], v[58:61]
	v_mfma_f32_16x16x128_f8f6f4 v[90:93], v[10:17], v[184:191], v[90:93]
	v_mfma_f32_16x16x128_f8f6f4 v[94:97], v[2:9], v[184:191], v[94:97]
	v_mfma_f32_16x16x128_f8f6f4 v[78:81], v[2:9], v[192:199], v[78:81]
	v_mfma_f32_16x16x128_f8f6f4 v[74:77], v[10:17], v[192:199], v[74:77]
	v_mfma_f32_16x16x128_f8f6f4 v[42:45], v[10:17], v[208:215], v[42:45]
	v_mfma_f32_16x16x128_f8f6f4 v[54:57], v[2:9], v[208:215], v[54:57]
	v_mfma_f32_16x16x128_f8f6f4 v[38:41], v[18:25], v[208:215], v[38:41]
	v_mfma_f32_16x16x128_f8f6f4 v[34:37], v[26:33], v[208:215], v[34:37]
	v_mfma_f32_16x16x128_f8f6f4 v[82:85], v[26:33], v[184:191], v[82:85]
	v_mfma_f32_16x16x128_f8f6f4 v[86:89], v[18:25], v[184:191], v[86:89]
	v_mfma_f32_16x16x128_f8f6f4 v[70:73], v[18:25], v[192:199], v[70:73]
	v_mfma_f32_16x16x128_f8f6f4 v[66:69], v[26:33], v[192:199], v[66:69]
	v_mfma_f32_16x16x128_f8f6f4 v[46:49], v[26:33], v[200:207], v[46:49]
	v_mfma_f32_16x16x128_f8f6f4 v[50:53], v[18:25], v[200:207], v[50:53]
	s_barrier
	s_movk_i32 s38, 0x100
	s_andn2_b64 vcc, exec, s[34:35]
	s_mov_b64 s[36:37], -1
	s_mov_b64 s[34:35], 0
	s_cbranch_vccz .LBB0_1558
	s_and_b64 vcc, exec, s[12:13]
	s_cbranch_vccz .LBB0_1561
	s_barrier

.LBB0_1681:
	ds_read_b128 v[26:29], v189
	ds_read_b128 v[30:33], v189 offset:1024
	ds_read_b128 v[18:21], v189 offset:2048
	ds_read_b128 v[22:25], v189 offset:3072
	ds_read_b128 v[10:13], v190
	ds_read_b128 v[14:17], v190 offset:1024
	ds_read_b128 v[2:5], v190 offset:2048
	ds_read_b128 v[6:9], v190 offset:3072
	s_add_u32 s34, s30, 0xfff80080
	s_addc_u32 s35, s31, -1
	s_cmp_eq_u32 s60, 28
	s_cselect_b32 s37, s18, s35
	s_cselect_b32 s36, s19, s34
	s_cselect_b32 s35, s21, s59
	s_cselect_b32 s34, s23, s58
	s_mov_b32 m0, s43
	s_nop 0
	global_load_lds_dwordx4 v168, s[100:101]
	s_mov_b32 m0, s44
	s_nop 0
	global_load_lds_dwordx4 v164, s[100:101]
	s_add_i32 m0, s29, 0xc000
	ds_read_b128 v[178:181], v191
	ds_read_b128 v[182:185], v191 offset:1024
	ds_read_b128 v[194:197], v191 offset:2048
	ds_read_b128 v[198:201], v191 offset:3072
	ds_read_b128 v[202:205], v191 offset:4096
	ds_read_b128 v[206:209], v191 offset:5120
	ds_read_b128 v[210:213], v191 offset:6144
	ds_read_b128 v[214:217], v191 offset:7168
	global_load_lds_dwordx4 v170, s[30:31]
	s_add_i32 m0, s29, 0xe000
	s_nop 0
	global_load_lds_dwordx4 v172, s[30:31]
	s_waitcnt vmcnt(8) lgkmcnt(0)
	s_barrier
	v_mfma_f32_16x16x128_f8f6f4 v[158:161], v[26:33], v[178:185], v[158:161]
	v_mfma_f32_16x16x128_f8f6f4 v[154:157], v[18:25], v[178:185], v[154:157]
	v_mfma_f32_16x16x128_f8f6f4 v[138:141], v[18:25], v[194:201], v[138:141]
	v_mfma_f32_16x16x128_f8f6f4 v[142:145], v[26:33], v[194:201], v[142:145]
	v_mfma_f32_16x16x128_f8f6f4 v[126:129], v[26:33], v[202:209], v[126:129]
	v_mfma_f32_16x16x128_f8f6f4 v[122:125], v[18:25], v[202:209], v[122:125]
	v_mfma_f32_16x16x128_f8f6f4 v[106:109], v[18:25], v[210:217], v[106:109]
	v_mfma_f32_16x16x128_f8f6f4 v[110:113], v[26:33], v[210:217], v[110:113]
	v_mfma_f32_16x16x128_f8f6f4 v[102:105], v[10:17], v[210:217], v[102:105]
	v_mfma_f32_16x16x128_f8f6f4 v[98:101], v[2:9], v[210:217], v[98:101]
	v_mfma_f32_16x16x128_f8f6f4 v[146:149], v[2:9], v[178:185], v[146:149]
	v_mfma_f32_16x16x128_f8f6f4 v[150:153], v[10:17], v[178:185], v[150:153]
	v_mfma_f32_16x16x128_f8f6f4 v[134:137], v[10:17], v[194:201], v[134:137]
	v_mfma_f32_16x16x128_f8f6f4 v[130:133], v[2:9], v[194:201], v[130:133]
	v_mfma_f32_16x16x128_f8f6f4 v[114:117], v[2:9], v[202:209], v[114:117]
	v_mfma_f32_16x16x128_f8f6f4 v[118:121], v[10:17], v[202:209], v[118:121]
	s_barrier
	s_add_i32 s61, s45, s3
	s_mov_b32 m0, s61
	ds_read_b128 v[194:197], v191 offset:16384
	ds_read_b128 v[198:201], v191 offset:17408
	ds_read_b128 v[202:205], v191 offset:18432
	ds_read_b128 v[206:209], v191 offset:19456
	ds_read_b128 v[210:213], v191 offset:20480
	ds_read_b128 v[214:217], v191 offset:21504
	ds_read_b128 v[218:221], v191 offset:22528
	ds_read_b128 v[222:225], v191 offset:23552
	global_load_lds_dwordx4 v166, s[34:35]
	s_add_i32 m0, s61, 0x2000
	s_add_u32 s62, s34, 0x80000
	s_addc_u32 s63, s35, 0
	s_add_i32 s61, s48, s3
	global_load_lds_dwordx4 v162, s[34:35]
	s_mov_b32 m0, s61
	s_nop 0
	global_load_lds_dwordx4 v166, s[62:63]
	s_add_i32 m0, s61, 0x2000
	s_nop 0
	global_load_lds_dwordx4 v162, s[62:63]
	s_waitcnt vmcnt(6) lgkmcnt(0)
	s_barrier
	v_mfma_f32_16x16x128_f8f6f4 v[78:81], v[26:33], v[202:209], v[78:81]
	v_mfma_f32_16x16x128_f8f6f4 v[74:77], v[18:25], v[202:209], v[74:77]
	v_mfma_f32_16x16x128_f8f6f4 v[90:93], v[18:25], v[194:201], v[90:93]
	v_mfma_f32_16x16x128_f8f6f4 v[94:97], v[26:33], v[194:201], v[94:97]
	v_mfma_f32_16x16x128_f8f6f4 v[62:65], v[26:33], v[210:217], v[62:65]
	v_mfma_f32_16x16x128_f8f6f4 v[58:61], v[18:25], v[210:217], v[58:61]
	v_mfma_f32_16x16x128_f8f6f4 v[42:45], v[18:25], v[218:225], v[42:45]
	v_mfma_f32_16x16x128_f8f6f4 v[46:49], v[26:33], v[218:225], v[46:49]
	v_mfma_f32_16x16x128_f8f6f4 v[38:41], v[10:17], v[218:225], v[38:41]
	v_mfma_f32_16x16x128_f8f6f4 v[34:37], v[2:9], v[218:225], v[34:37]
	v_mfma_f32_16x16x128_f8f6f4 v[82:85], v[2:9], v[194:201], v[82:85]
	v_mfma_f32_16x16x128_f8f6f4 v[86:89], v[10:17], v[194:201], v[86:89]
	v_mfma_f32_16x16x128_f8f6f4 v[70:73], v[10:17], v[202:209], v[70:73]
	v_mfma_f32_16x16x128_f8f6f4 v[66:69], v[2:9], v[202:209], v[66:69]
	v_mfma_f32_16x16x128_f8f6f4 v[50:53], v[2:9], v[210:217], v[50:53]
	v_mfma_f32_16x16x128_f8f6f4 v[54:57], v[10:17], v[210:217], v[54:57]
	s_barrier
	s_add_i32 s61, 0, 0x18000
	s_add_i32 s62, 0, 0x1c000
	v_add_u32_e32 v14, s61, v187
	v_add_u32_e32 v30, s62, v187
	ds_read_b128 v[2:5], v14
	ds_read_b128 v[6:9], v14 offset:1024
	ds_read_b128 v[10:13], v14 offset:2048
	ds_read_b128 v[14:17], v14 offset:3072
	ds_read_b128 v[18:21], v30
	ds_read_b128 v[22:25], v30 offset:1024
	ds_read_b128 v[26:29], v30 offset:2048
	ds_read_b128 v[30:33], v30 offset:3072
	s_mov_b32 m0, s29
	s_nop 0
	global_load_lds_dwordx4 v168, s[36:37]
	s_mov_b32 m0, s38
	s_nop 0
	global_load_lds_dwordx4 v164, s[36:37]
	s_add_u32 s36, s36, 0x80000
	s_addc_u32 s37, s37, 0
	s_add_u32 s100, s36, 0xfff80080
	s_addc_u32 s101, s37, -1
	s_mov_b32 m0, s39
	ds_read_b128 v[194:197], v191 offset:32768
	ds_read_b128 v[198:201], v191 offset:33792
	ds_read_b128 v[202:205], v191 offset:34816
	ds_read_b128 v[206:209], v191 offset:35840
	ds_read_b128 v[210:213], v191 offset:36864
	ds_read_b128 v[214:217], v191 offset:37888
	ds_read_b128 v[218:221], v191 offset:38912
	ds_read_b128 v[222:225], v191 offset:39936
	global_load_lds_dwordx4 v168, s[36:37]
	s_mov_b32 m0, s40
	s_nop 0
	global_load_lds_dwordx4 v164, s[36:37]
	s_waitcnt vmcnt(8) lgkmcnt(0)
	s_barrier
	v_mfma_f32_16x16x128_f8f6f4 v[122:125], v[10:17], v[210:217], v[122:125]
	v_mfma_f32_16x16x128_f8f6f4 v[126:129], v[2:9], v[210:217], v[126:129]
	v_mfma_f32_16x16x128_f8f6f4 v[158:161], v[2:9], v[194:201], v[158:161]
	v_mfma_f32_16x16x128_f8f6f4 v[154:157], v[10:17], v[194:201], v[154:157]
	v_mfma_f32_16x16x128_f8f6f4 v[138:141], v[10:17], v[202:209], v[138:141]
	v_mfma_f32_16x16x128_f8f6f4 v[142:145], v[2:9], v[202:209], v[142:145]
	v_mfma_f32_16x16x128_f8f6f4 v[110:113], v[2:9], v[218:225], v[110:113]
	v_mfma_f32_16x16x128_f8f6f4 v[106:109], v[10:17], v[218:225], v[106:109]
	v_mfma_f32_16x16x128_f8f6f4 v[102:105], v[18:25], v[218:225], v[102:105]
	v_mfma_f32_16x16x128_f8f6f4 v[98:101], v[26:33], v[218:225], v[98:101]
	v_mfma_f32_16x16x128_f8f6f4 v[146:149], v[26:33], v[194:201], v[146:149]
	v_mfma_f32_16x16x128_f8f6f4 v[150:153], v[18:25], v[194:201], v[150:153]
	v_mfma_f32_16x16x128_f8f6f4 v[134:137], v[18:25], v[202:209], v[134:137]
	v_mfma_f32_16x16x128_f8f6f4 v[130:133], v[26:33], v[202:209], v[130:133]
	v_mfma_f32_16x16x128_f8f6f4 v[114:117], v[26:33], v[210:217], v[114:117]
	v_mfma_f32_16x16x128_f8f6f4 v[118:121], v[18:25], v[210:217], v[118:121]
	s_barrier
	s_add_i32 s36, s61, s3
	s_mov_b32 m0, s36
	s_add_u32 s98, s34, 0x80
	s_addc_u32 s99, s35, 0
	ds_read_b128 v[194:197], v191 offset:49152
	ds_read_b128 v[198:201], v191 offset:50176
	ds_read_b128 v[202:205], v191 offset:51200
	ds_read_b128 v[206:209], v191 offset:52224
	ds_read_b128 v[210:213], v191 offset:53248
	ds_read_b128 v[214:217], v191 offset:54272
	ds_read_b128 v[218:221], v191 offset:55296
	ds_read_b128 v[222:225], v191 offset:56320
	global_load_lds_dwordx4 v166, s[98:99]
	s_add_i32 m0, s36, 0x2000
	s_add_u32 s34, s34, 0x80080
	s_addc_u32 s35, s35, 0
	s_add_i32 s36, s62, s3
	global_load_lds_dwordx4 v162, s[98:99]
	s_mov_b32 m0, s36
	s_nop 0
	global_load_lds_dwordx4 v166, s[34:35]
	s_add_i32 m0, s36, 0x2000
	s_nop 0
	global_load_lds_dwordx4 v162, s[34:35]
	s_waitcnt vmcnt(6) lgkmcnt(0)
	s_barrier
	v_mfma_f32_16x16x128_f8f6f4 v[62:65], v[2:9], v[210:217], v[62:65]
	v_mfma_f32_16x16x128_f8f6f4 v[58:61], v[10:17], v[210:217], v[58:61]
	v_mfma_f32_16x16x128_f8f6f4 v[90:93], v[10:17], v[194:201], v[90:93]
	v_mfma_f32_16x16x128_f8f6f4 v[94:97], v[2:9], v[194:201], v[94:97]
	v_mfma_f32_16x16x128_f8f6f4 v[78:81], v[2:9], v[202:209], v[78:81]
	v_mfma_f32_16x16x128_f8f6f4 v[74:77], v[10:17], v[202:209], v[74:77]
	v_mfma_f32_16x16x128_f8f6f4 v[42:45], v[10:17], v[218:225], v[42:45]
	v_mfma_f32_16x16x128_f8f6f4 v[46:49], v[2:9], v[218:225], v[46:49]
	v_mfma_f32_16x16x128_f8f6f4 v[38:41], v[18:25], v[218:225], v[38:41]
	v_mfma_f32_16x16x128_f8f6f4 v[34:37], v[26:33], v[218:225], v[34:37]
	v_mfma_f32_16x16x128_f8f6f4 v[82:85], v[26:33], v[194:201], v[82:85]
	v_mfma_f32_16x16x128_f8f6f4 v[86:89], v[18:25], v[194:201], v[86:89]
	v_mfma_f32_16x16x128_f8f6f4 v[70:73], v[18:25], v[202:209], v[70:73]
	v_mfma_f32_16x16x128_f8f6f4 v[66:69], v[26:33], v[202:209], v[66:69]
	v_mfma_f32_16x16x128_f8f6f4 v[50:53], v[26:33], v[210:217], v[50:53]
	v_mfma_f32_16x16x128_f8f6f4 v[54:57], v[18:25], v[210:217], v[54:57]
	s_barrier
	s_add_i32 s60, s60, 2
	s_add_u32 s30, s30, 0x100
	s_addc_u32 s31, s31, 0
	s_add_u32 s58, s58, 0x100
	s_addc_u32 s59, s59, 0
	s_cmp_gt_u32 s60, 29
	s_cbranch_scc0 .LBB0_1681
	s_and_b64 vcc, exec, s[12:13]
	s_cbranch_vccz .LBB0_1684
	s_barrier

.LBB0_1745:
	s_add_u32 s8, s49, s6
	s_addc_u32 s9, s50, s7
	s_add_u32 s8, s8, 0x32800100
	s_addc_u32 s9, s9, 0
	s_add_u32 s73, s51, s6
	s_addc_u32 s74, s54, s7
	s_add_i32 s72, 0, 0x10000
	s_cmpk_eq_i32 s6, 0x2a00
	s_cselect_b32 s37, s5, s9
	s_cselect_b32 s36, s4, s8
	s_cselect_b32 s9, s13, s74
	s_cselect_b32 s8, s12, s73
	s_add_i32 s73, 0, 0x14000
	v_add_u32_e32 v2, s72, v188
	v_add_u32_e32 v6, s73, v188
	ds_read_b128 v[26:29], v2
	ds_read_b128 v[30:33], v2 offset:1024
	ds_read_b128 v[18:21], v2 offset:2048
	ds_read_b128 v[22:25], v2 offset:3072
	ds_read_b128 v[10:13], v6
	ds_read_b128 v[14:17], v6 offset:1024
	ds_read_b128 v[2:5], v6 offset:2048
	ds_read_b128 v[6:9], v6 offset:3072
	v_lshl_add_u64 v[214:215], v[168:169], 0, s[6:7]
	s_add_i32 m0, s64, 0xc000
	ds_read_b128 v[172:175], v189
	ds_read_b128 v[176:179], v189 offset:1024
	ds_read_b128 v[190:193], v189 offset:2048
	ds_read_b128 v[194:197], v189 offset:3072
	ds_read_b128 v[198:201], v189 offset:4096
	ds_read_b128 v[202:205], v189 offset:5120
	ds_read_b128 v[206:209], v189 offset:6144
	ds_read_b128 v[210:213], v189 offset:7168
	global_load_lds_dwordx4 v[214:215], off
	v_lshl_add_u64 v[214:215], v[170:171], 0, s[6:7]
	s_add_i32 m0, s64, 0xe000
	s_nop 0
	global_load_lds_dwordx4 v[214:215], off
	s_waitcnt vmcnt(8) lgkmcnt(0)
	s_barrier
	v_mfma_f32_16x16x128_f8f6f4 v[158:161], v[26:33], v[172:179], v[158:161]
	v_mfma_f32_16x16x128_f8f6f4 v[154:157], v[18:25], v[172:179], v[154:157]
	v_mfma_f32_16x16x128_f8f6f4 v[118:121], v[18:25], v[190:197], v[118:121]
	v_mfma_f32_16x16x128_f8f6f4 v[122:125], v[26:33], v[190:197], v[122:125]
	v_mfma_f32_16x16x128_f8f6f4 v[126:129], v[26:33], v[198:205], v[126:129]
	v_mfma_f32_16x16x128_f8f6f4 v[114:117], v[18:25], v[198:205], v[114:117]
	v_mfma_f32_16x16x128_f8f6f4 v[106:109], v[18:25], v[206:213], v[106:109]
	v_mfma_f32_16x16x128_f8f6f4 v[110:113], v[26:33], v[206:213], v[110:113]
	v_mfma_f32_16x16x128_f8f6f4 v[102:105], v[10:17], v[206:213], v[102:105]
	v_mfma_f32_16x16x128_f8f6f4 v[98:101], v[2:9], v[206:213], v[98:101]
	v_mfma_f32_16x16x128_f8f6f4 v[146:149], v[2:9], v[172:179], v[146:149]
	v_mfma_f32_16x16x128_f8f6f4 v[150:153], v[10:17], v[172:179], v[150:153]
	v_mfma_f32_16x16x128_f8f6f4 v[142:145], v[10:17], v[190:197], v[142:145]
	v_mfma_f32_16x16x128_f8f6f4 v[138:141], v[2:9], v[190:197], v[138:141]
	v_mfma_f32_16x16x128_f8f6f4 v[130:133], v[2:9], v[198:205], v[130:133]
	v_mfma_f32_16x16x128_f8f6f4 v[134:137], v[10:17], v[198:205], v[134:137]
	s_barrier
	s_add_i32 s72, s72, s43
	v_lshl_add_u64 v[172:173], s[8:9], 0, v[162:163]
	s_mov_b32 m0, s72
	ds_read_b128 v[190:193], v189 offset:16384
	ds_read_b128 v[194:197], v189 offset:17408
	ds_read_b128 v[198:201], v189 offset:18432
	ds_read_b128 v[202:205], v189 offset:19456
	ds_read_b128 v[206:209], v189 offset:20480
	ds_read_b128 v[210:213], v189 offset:21504
	ds_read_b128 v[214:217], v189 offset:22528
	ds_read_b128 v[218:221], v189 offset:23552
	global_load_lds_dwordx4 v[172:173], off
	s_add_i32 m0, s72, 0x2000
	s_add_u32 s74, s8, 0x158000
	v_lshl_add_u64 v[174:175], s[8:9], 0, v[166:167]
	s_addc_u32 s75, s9, 0
	s_add_i32 s72, s73, s43
	global_load_lds_dwordx4 v[174:175], off
	s_mov_b32 m0, s72
	v_lshl_add_u64 v[178:179], s[36:37], 0, v[166:167]
	global_load_lds_dwordx4 v162, s[74:75]
	s_add_i32 m0, s72, 0x2000
	s_nop 0
	global_load_lds_dwordx4 v166, s[74:75]
	v_lshl_add_u64 v[176:177], s[36:37], 0, v[162:163]
	s_mov_b32 m0, s64
	s_nop 0
	global_load_lds_dwordx4 v[176:177], off
	s_mov_b32 m0, s65
	s_nop 0
	global_load_lds_dwordx4 v[178:179], off
	s_waitcnt vmcnt(8) lgkmcnt(0)
	s_barrier
	v_mfma_f32_16x16x128_f8f6f4 v[78:81], v[26:33], v[198:205], v[78:81]
	v_mfma_f32_16x16x128_f8f6f4 v[74:77], v[18:25], v[198:205], v[74:77]
	v_mfma_f32_16x16x128_f8f6f4 v[90:93], v[18:25], v[190:197], v[90:93]
	v_mfma_f32_16x16x128_f8f6f4 v[94:97], v[26:33], v[190:197], v[94:97]
	v_mfma_f32_16x16x128_f8f6f4 v[62:65], v[26:33], v[206:213], v[62:65]
	v_mfma_f32_16x16x128_f8f6f4 v[58:61], v[18:25], v[206:213], v[58:61]
	v_mfma_f32_16x16x128_f8f6f4 v[42:45], v[18:25], v[214:221], v[42:45]
	v_mfma_f32_16x16x128_f8f6f4 v[46:49], v[26:33], v[214:221], v[46:49]
	v_mfma_f32_16x16x128_f8f6f4 v[38:41], v[10:17], v[214:221], v[38:41]
	v_mfma_f32_16x16x128_f8f6f4 v[34:37], v[2:9], v[214:221], v[34:37]
	v_mfma_f32_16x16x128_f8f6f4 v[82:85], v[2:9], v[190:197], v[82:85]
	v_mfma_f32_16x16x128_f8f6f4 v[86:89], v[10:17], v[190:197], v[86:89]
	v_mfma_f32_16x16x128_f8f6f4 v[70:73], v[10:17], v[198:205], v[70:73]
	v_mfma_f32_16x16x128_f8f6f4 v[66:69], v[2:9], v[198:205], v[66:69]
	v_mfma_f32_16x16x128_f8f6f4 v[50:53], v[2:9], v[206:213], v[50:53]
	v_mfma_f32_16x16x128_f8f6f4 v[54:57], v[10:17], v[206:213], v[54:57]
	s_barrier
	s_add_i32 s72, 0, 0x18000
	s_add_i32 s73, 0, 0x1c000
	v_add_u32_e32 v14, s72, v188
	v_add_u32_e32 v30, s73, v188
	ds_read_b128 v[2:5], v14
	ds_read_b128 v[6:9], v14 offset:1024
	ds_read_b128 v[10:13], v14 offset:2048
	ds_read_b128 v[14:17], v14 offset:3072
	ds_read_b128 v[18:21], v30
	ds_read_b128 v[22:25], v30 offset:1024
	ds_read_b128 v[26:29], v30 offset:2048
	ds_read_b128 v[30:33], v30 offset:3072
	s_add_u32 s36, s36, 0x158000
	s_addc_u32 s37, s37, 0
	s_mov_b32 m0, s66
	ds_read_b128 v[190:193], v189 offset:32768
	ds_read_b128 v[194:197], v189 offset:33792
	ds_read_b128 v[198:201], v189 offset:34816
	ds_read_b128 v[202:205], v189 offset:35840
	ds_read_b128 v[206:209], v189 offset:36864
	ds_read_b128 v[210:213], v189 offset:37888
	ds_read_b128 v[214:217], v189 offset:38912
	ds_read_b128 v[218:221], v189 offset:39936
	global_load_lds_dwordx4 v162, s[36:37]
	s_mov_b32 m0, s67
	s_nop 0
	global_load_lds_dwordx4 v166, s[36:37]
	s_waitcnt vmcnt(8) lgkmcnt(0)
	s_barrier
	v_mfma_f32_16x16x128_f8f6f4 v[114:117], v[10:17], v[206:213], v[114:117]
	v_mfma_f32_16x16x128_f8f6f4 v[126:129], v[2:9], v[206:213], v[126:129]
	v_mfma_f32_16x16x128_f8f6f4 v[158:161], v[2:9], v[190:197], v[158:161]
	v_mfma_f32_16x16x128_f8f6f4 v[154:157], v[10:17], v[190:197], v[154:157]
	v_mfma_f32_16x16x128_f8f6f4 v[118:121], v[10:17], v[198:205], v[118:121]
	v_mfma_f32_16x16x128_f8f6f4 v[122:125], v[2:9], v[198:205], v[122:125]
	v_mfma_f32_16x16x128_f8f6f4 v[110:113], v[2:9], v[214:221], v[110:113]
	v_mfma_f32_16x16x128_f8f6f4 v[106:109], v[10:17], v[214:221], v[106:109]
	v_mfma_f32_16x16x128_f8f6f4 v[102:105], v[18:25], v[214:221], v[102:105]
	v_mfma_f32_16x16x128_f8f6f4 v[98:101], v[26:33], v[214:221], v[98:101]
	v_mfma_f32_16x16x128_f8f6f4 v[146:149], v[26:33], v[190:197], v[146:149]
	v_mfma_f32_16x16x128_f8f6f4 v[150:153], v[18:25], v[190:197], v[150:153]
	v_mfma_f32_16x16x128_f8f6f4 v[142:145], v[18:25], v[198:205], v[142:145]
	v_mfma_f32_16x16x128_f8f6f4 v[138:141], v[26:33], v[198:205], v[138:141]
	v_mfma_f32_16x16x128_f8f6f4 v[130:133], v[26:33], v[206:213], v[130:133]
	v_mfma_f32_16x16x128_f8f6f4 v[134:137], v[18:25], v[206:213], v[134:137]
	s_barrier
	s_add_i32 s36, s72, s43
	v_lshl_add_u64 v[172:173], v[172:173], 0, s[22:23]
	s_mov_b32 m0, s36
	ds_read_b128 v[190:193], v189 offset:49152
	ds_read_b128 v[194:197], v189 offset:50176
	ds_read_b128 v[198:201], v189 offset:51200
	ds_read_b128 v[202:205], v189 offset:52224
	ds_read_b128 v[206:209], v189 offset:53248
	ds_read_b128 v[210:213], v189 offset:54272
	ds_read_b128 v[214:217], v189 offset:55296
	ds_read_b128 v[218:221], v189 offset:56320
	global_load_lds_dwordx4 v[172:173], off
	s_add_i32 m0, s36, 0x2000
	s_add_u32 s8, s8, 0x158080
	v_lshl_add_u64 v[172:173], v[174:175], 0, s[22:23]
	s_addc_u32 s9, s9, 0
	s_add_i32 s36, s73, s43
	global_load_lds_dwordx4 v[172:173], off
	s_mov_b32 m0, s36
	s_nop 0
	global_load_lds_dwordx4 v162, s[8:9]
	s_add_i32 m0, s36, 0x2000
	s_nop 0
	global_load_lds_dwordx4 v166, s[8:9]
	v_lshl_add_u64 v[172:173], v[176:177], 0, s[22:23]
	s_mov_b32 m0, s69
	s_nop 0
	global_load_lds_dwordx4 v[172:173], off
	v_lshl_add_u64 v[172:173], v[178:179], 0, s[22:23]
	s_mov_b32 m0, s70
	s_nop 0
	global_load_lds_dwordx4 v[172:173], off
	s_waitcnt vmcnt(8) lgkmcnt(0)
	s_barrier
	v_mfma_f32_16x16x128_f8f6f4 v[62:65], v[2:9], v[206:213], v[62:65]
	v_mfma_f32_16x16x128_f8f6f4 v[58:61], v[10:17], v[206:213], v[58:61]
	v_mfma_f32_16x16x128_f8f6f4 v[90:93], v[10:17], v[190:197], v[90:93]
	v_mfma_f32_16x16x128_f8f6f4 v[94:97], v[2:9], v[190:197], v[94:97]
	v_mfma_f32_16x16x128_f8f6f4 v[78:81], v[2:9], v[198:205], v[78:81]
	v_mfma_f32_16x16x128_f8f6f4 v[74:77], v[10:17], v[198:205], v[74:77]
	v_mfma_f32_16x16x128_f8f6f4 v[42:45], v[10:17], v[214:221], v[42:45]
	v_mfma_f32_16x16x128_f8f6f4 v[46:49], v[2:9], v[214:221], v[46:49]
	v_mfma_f32_16x16x128_f8f6f4 v[38:41], v[18:25], v[214:221], v[38:41]
	v_mfma_f32_16x16x128_f8f6f4 v[34:37], v[26:33], v[214:221], v[34:37]
	v_mfma_f32_16x16x128_f8f6f4 v[82:85], v[26:33], v[190:197], v[82:85]
	v_mfma_f32_16x16x128_f8f6f4 v[86:89], v[18:25], v[190:197], v[86:89]
	v_mfma_f32_16x16x128_f8f6f4 v[70:73], v[18:25], v[198:205], v[70:73]
	v_mfma_f32_16x16x128_f8f6f4 v[66:69], v[26:33], v[198:205], v[66:69]
	v_mfma_f32_16x16x128_f8f6f4 v[50:53], v[26:33], v[206:213], v[50:53]
	v_mfma_f32_16x16x128_f8f6f4 v[54:57], v[18:25], v[206:213], v[54:57]
	s_barrier
	s_add_i32 s71, s71, 2
	s_add_u32 s6, s6, 0x100
	s_addc_u32 s7, s7, 0
	s_cmpk_lt_u32 s71, 0x54
	s_cbranch_scc1 .LBB0_1745
	s_waitcnt vmcnt(0)
	s_cmpk_gt_u32 s40, 0xff
	s_cbranch_scc1 .LBB0_1748
	s_barrier

.LBB0_1807:
	ds_read_b128 v[26:29], v185
	ds_read_b128 v[30:33], v185 offset:1024
	ds_read_b128 v[18:21], v185 offset:2048
	ds_read_b128 v[22:25], v185 offset:3072
	ds_read_b128 v[10:13], v186
	ds_read_b128 v[14:17], v186 offset:1024
	ds_read_b128 v[2:5], v186 offset:2048
	ds_read_b128 v[6:9], v186 offset:3072
	s_add_u32 s28, s26, 0xffea8080
	s_addc_u32 s29, s27, -1
	s_cmpk_eq_i32 s58, 0x52
	s_cselect_b32 s31, s5, s29
	s_cselect_b32 s30, s4, s28
	s_cselect_b32 s29, s25, s57
	s_cselect_b32 s28, s24, s56
	s_add_i32 m0, s34, 0xc000
	ds_read_b128 v[174:177], v187
	ds_read_b128 v[178:181], v187 offset:1024
	ds_read_b128 v[188:191], v187 offset:2048
	ds_read_b128 v[192:195], v187 offset:3072
	ds_read_b128 v[196:199], v187 offset:4096
	ds_read_b128 v[200:203], v187 offset:5120
	ds_read_b128 v[204:207], v187 offset:6144
	ds_read_b128 v[208:211], v187 offset:7168
	global_load_lds_dwordx4 v166, s[26:27]
	v_lshl_add_u64 v[212:213], s[26:27], 0, v[168:169]
	s_add_i32 m0, s34, 0xe000
	s_nop 0
	global_load_lds_dwordx4 v[212:213], off
	s_waitcnt vmcnt(8) lgkmcnt(0)
	s_barrier
	v_mfma_f32_16x16x128_f8f6f4 v[158:161], v[26:33], v[174:181], v[158:161]
	v_mfma_f32_16x16x128_f8f6f4 v[154:157], v[18:25], v[174:181], v[154:157]
	v_mfma_f32_16x16x128_f8f6f4 v[138:141], v[18:25], v[188:195], v[138:141]
	v_mfma_f32_16x16x128_f8f6f4 v[142:145], v[26:33], v[188:195], v[142:145]
	v_mfma_f32_16x16x128_f8f6f4 v[126:129], v[26:33], v[196:203], v[126:129]
	v_mfma_f32_16x16x128_f8f6f4 v[122:125], v[18:25], v[196:203], v[122:125]
	v_mfma_f32_16x16x128_f8f6f4 v[106:109], v[18:25], v[204:211], v[106:109]
	v_mfma_f32_16x16x128_f8f6f4 v[110:113], v[26:33], v[204:211], v[110:113]
	v_mfma_f32_16x16x128_f8f6f4 v[102:105], v[10:17], v[204:211], v[102:105]
	v_mfma_f32_16x16x128_f8f6f4 v[98:101], v[2:9], v[204:211], v[98:101]
	v_mfma_f32_16x16x128_f8f6f4 v[146:149], v[2:9], v[174:181], v[146:149]
	v_mfma_f32_16x16x128_f8f6f4 v[150:153], v[10:17], v[174:181], v[150:153]
	v_mfma_f32_16x16x128_f8f6f4 v[134:137], v[10:17], v[188:195], v[134:137]
	v_mfma_f32_16x16x128_f8f6f4 v[130:133], v[2:9], v[188:195], v[130:133]
	v_mfma_f32_16x16x128_f8f6f4 v[114:117], v[2:9], v[196:203], v[114:117]
	v_mfma_f32_16x16x128_f8f6f4 v[118:121], v[10:17], v[196:203], v[118:121]
	s_barrier
	s_add_i32 s59, s42, s3
	v_lshl_add_u64 v[174:175], s[28:29], 0, v[164:165]
	s_mov_b32 m0, s59
	ds_read_b128 v[188:191], v187 offset:16384
	ds_read_b128 v[192:195], v187 offset:17408
	ds_read_b128 v[196:199], v187 offset:18432
	ds_read_b128 v[200:203], v187 offset:19456
	ds_read_b128 v[204:207], v187 offset:20480
	ds_read_b128 v[208:211], v187 offset:21504
	ds_read_b128 v[212:215], v187 offset:22528
	ds_read_b128 v[216:219], v187 offset:23552
	global_load_lds_dwordx4 v[174:175], off
	s_add_i32 m0, s59, 0x2000
	s_add_u32 s60, s28, 0x158000
	v_lshl_add_u64 v[176:177], s[28:29], 0, v[162:163]
	s_addc_u32 s61, s29, 0
	s_add_i32 s59, s43, s3
	global_load_lds_dwordx4 v[176:177], off
	s_mov_b32 m0, s59
	v_lshl_add_u64 v[180:181], s[30:31], 0, v[162:163]
	global_load_lds_dwordx4 v164, s[60:61]
	s_add_i32 m0, s59, 0x2000
	s_nop 0
	global_load_lds_dwordx4 v162, s[60:61]
	v_lshl_add_u64 v[178:179], s[30:31], 0, v[164:165]
	s_mov_b32 m0, s34
	s_nop 0
	global_load_lds_dwordx4 v[178:179], off
	s_mov_b32 m0, s35
	s_nop 0
	global_load_lds_dwordx4 v[180:181], off
	s_waitcnt vmcnt(8) lgkmcnt(0)
	s_barrier
	v_mfma_f32_16x16x128_f8f6f4 v[78:81], v[26:33], v[196:203], v[78:81]
	v_mfma_f32_16x16x128_f8f6f4 v[74:77], v[18:25], v[196:203], v[74:77]
	v_mfma_f32_16x16x128_f8f6f4 v[90:93], v[18:25], v[188:195], v[90:93]
	v_mfma_f32_16x16x128_f8f6f4 v[94:97], v[26:33], v[188:195], v[94:97]
	v_mfma_f32_16x16x128_f8f6f4 v[62:65], v[26:33], v[204:211], v[62:65]
	v_mfma_f32_16x16x128_f8f6f4 v[58:61], v[18:25], v[204:211], v[58:61]
	v_mfma_f32_16x16x128_f8f6f4 v[42:45], v[18:25], v[212:219], v[42:45]
	v_mfma_f32_16x16x128_f8f6f4 v[54:57], v[26:33], v[212:219], v[54:57]
	v_mfma_f32_16x16x128_f8f6f4 v[38:41], v[10:17], v[212:219], v[38:41]
	v_mfma_f32_16x16x128_f8f6f4 v[34:37], v[2:9], v[212:219], v[34:37]
	v_mfma_f32_16x16x128_f8f6f4 v[82:85], v[2:9], v[188:195], v[82:85]
	v_mfma_f32_16x16x128_f8f6f4 v[86:89], v[10:17], v[188:195], v[86:89]
	v_mfma_f32_16x16x128_f8f6f4 v[70:73], v[10:17], v[196:203], v[70:73]
	v_mfma_f32_16x16x128_f8f6f4 v[66:69], v[2:9], v[196:203], v[66:69]
	v_mfma_f32_16x16x128_f8f6f4 v[46:49], v[2:9], v[204:211], v[46:49]
	v_mfma_f32_16x16x128_f8f6f4 v[50:53], v[10:17], v[204:211], v[50:53]
	s_barrier
	s_add_i32 s59, 0, 0x18000
	s_add_i32 s60, 0, 0x1c000
	v_add_u32_e32 v14, s59, v183
	v_add_u32_e32 v30, s60, v183
	ds_read_b128 v[2:5], v14
	ds_read_b128 v[6:9], v14 offset:1024
	ds_read_b128 v[10:13], v14 offset:2048
	ds_read_b128 v[14:17], v14 offset:3072
	ds_read_b128 v[18:21], v30
	ds_read_b128 v[22:25], v30 offset:1024
	ds_read_b128 v[26:29], v30 offset:2048
	ds_read_b128 v[30:33], v30 offset:3072
	s_add_u32 s30, s30, 0x158000
	s_addc_u32 s31, s31, 0
	s_mov_b32 m0, s36
	ds_read_b128 v[188:191], v187 offset:32768
	ds_read_b128 v[192:195], v187 offset:33792
	ds_read_b128 v[196:199], v187 offset:34816
	ds_read_b128 v[200:203], v187 offset:35840
	ds_read_b128 v[204:207], v187 offset:36864
	ds_read_b128 v[208:211], v187 offset:37888
	ds_read_b128 v[212:215], v187 offset:38912
	ds_read_b128 v[216:219], v187 offset:39936
	global_load_lds_dwordx4 v164, s[30:31]
	s_mov_b32 m0, s37
	s_nop 0
	global_load_lds_dwordx4 v162, s[30:31]
	s_waitcnt vmcnt(8) lgkmcnt(0)
	s_barrier
	v_mfma_f32_16x16x128_f8f6f4 v[122:125], v[10:17], v[204:211], v[122:125]
	v_mfma_f32_16x16x128_f8f6f4 v[126:129], v[2:9], v[204:211], v[126:129]
	v_mfma_f32_16x16x128_f8f6f4 v[158:161], v[2:9], v[188:195], v[158:161]
	v_mfma_f32_16x16x128_f8f6f4 v[154:157], v[10:17], v[188:195], v[154:157]
	v_mfma_f32_16x16x128_f8f6f4 v[138:141], v[10:17], v[196:203], v[138:141]
	v_mfma_f32_16x16x128_f8f6f4 v[142:145], v[2:9], v[196:203], v[142:145]
	v_mfma_f32_16x16x128_f8f6f4 v[110:113], v[2:9], v[212:219], v[110:113]
	v_mfma_f32_16x16x128_f8f6f4 v[106:109], v[10:17], v[212:219], v[106:109]
	v_mfma_f32_16x16x128_f8f6f4 v[102:105], v[18:25], v[212:219], v[102:105]
	v_mfma_f32_16x16x128_f8f6f4 v[98:101], v[26:33], v[212:219], v[98:101]
	v_mfma_f32_16x16x128_f8f6f4 v[146:149], v[26:33], v[188:195], v[146:149]
	v_mfma_f32_16x16x128_f8f6f4 v[150:153], v[18:25], v[188:195], v[150:153]
	v_mfma_f32_16x16x128_f8f6f4 v[134:137], v[18:25], v[196:203], v[134:137]
	v_mfma_f32_16x16x128_f8f6f4 v[130:133], v[26:33], v[196:203], v[130:133]
	v_mfma_f32_16x16x128_f8f6f4 v[114:117], v[26:33], v[204:211], v[114:117]
	v_mfma_f32_16x16x128_f8f6f4 v[118:121], v[18:25], v[204:211], v[118:121]
	s_barrier
	s_add_i32 s30, s59, s3
	v_lshl_add_u64 v[174:175], v[174:175], 0, s[10:11]
	s_mov_b32 m0, s30
	ds_read_b128 v[188:191], v187 offset:49152
	ds_read_b128 v[192:195], v187 offset:50176
	ds_read_b128 v[196:199], v187 offset:51200
	ds_read_b128 v[200:203], v187 offset:52224
	ds_read_b128 v[204:207], v187 offset:53248
	ds_read_b128 v[208:211], v187 offset:54272
	ds_read_b128 v[212:215], v187 offset:55296
	ds_read_b128 v[216:219], v187 offset:56320
	global_load_lds_dwordx4 v[174:175], off
	s_add_i32 m0, s30, 0x2000
	s_add_u32 s28, s28, 0x158080
	v_lshl_add_u64 v[174:175], v[176:177], 0, s[10:11]
	s_addc_u32 s29, s29, 0
	s_add_i32 s30, s60, s3
	global_load_lds_dwordx4 v[174:175], off
	s_mov_b32 m0, s30
	s_nop 0
	global_load_lds_dwordx4 v164, s[28:29]
	s_add_i32 m0, s30, 0x2000
	s_nop 0
	global_load_lds_dwordx4 v162, s[28:29]
	v_lshl_add_u64 v[174:175], v[178:179], 0, s[10:11]
	s_mov_b32 m0, s40
	s_nop 0
	global_load_lds_dwordx4 v[174:175], off
	v_lshl_add_u64 v[174:175], v[180:181], 0, s[10:11]
	s_mov_b32 m0, s41
	s_nop 0
	global_load_lds_dwordx4 v[174:175], off
	s_waitcnt vmcnt(8) lgkmcnt(0)
	s_barrier
	v_mfma_f32_16x16x128_f8f6f4 v[62:65], v[2:9], v[204:211], v[62:65]
	v_mfma_f32_16x16x128_f8f6f4 v[58:61], v[10:17], v[204:211], v[58:61]
	v_mfma_f32_16x16x128_f8f6f4 v[90:93], v[10:17], v[188:195], v[90:93]
	v_mfma_f32_16x16x128_f8f6f4 v[94:97], v[2:9], v[188:195], v[94:97]
	v_mfma_f32_16x16x128_f8f6f4 v[78:81], v[2:9], v[196:203], v[78:81]
	v_mfma_f32_16x16x128_f8f6f4 v[74:77], v[10:17], v[196:203], v[74:77]
	v_mfma_f32_16x16x128_f8f6f4 v[42:45], v[10:17], v[212:219], v[42:45]
	v_mfma_f32_16x16x128_f8f6f4 v[54:57], v[2:9], v[212:219], v[54:57]
	v_mfma_f32_16x16x128_f8f6f4 v[38:41], v[18:25], v[212:219], v[38:41]
	v_mfma_f32_16x16x128_f8f6f4 v[34:37], v[26:33], v[212:219], v[34:37]
	v_mfma_f32_16x16x128_f8f6f4 v[82:85], v[26:33], v[188:195], v[82:85]
	v_mfma_f32_16x16x128_f8f6f4 v[86:89], v[18:25], v[188:195], v[86:89]
	v_mfma_f32_16x16x128_f8f6f4 v[70:73], v[18:25], v[196:203], v[70:73]
	v_mfma_f32_16x16x128_f8f6f4 v[66:69], v[26:33], v[196:203], v[66:69]
	v_mfma_f32_16x16x128_f8f6f4 v[46:49], v[26:33], v[204:211], v[46:49]
	v_mfma_f32_16x16x128_f8f6f4 v[50:53], v[18:25], v[204:211], v[50:53]
	s_barrier
	s_add_i32 s58, s58, 2
	s_add_u32 s26, s26, 0x100
	s_addc_u32 s27, s27, 0
	s_add_u32 s56, s56, 0x100
	s_addc_u32 s57, s57, 0
	s_cmpk_gt_u32 s58, 0x53
	s_cbranch_scc0 .LBB0_1807
	s_and_b64 vcc, exec, s[12:13]
	s_cbranch_vccz .LBB0_1810
	s_barrier
